# cache policy: once-read gate operand loads (z/u dwords) in all four mixer unit epilogues made non-temporal
# speedup vs baseline: 1.0020x; 1.0020x over previous
; #define LAS __attribute__((address_space(3)))
; __device__ __forceinline__ s16x4 tr_read(LAS const unsigned char* p) { return __builtin_bit_cast(s16x4, __builtin_amdgcn_ds_read_tr16_b64_v4i16((LAS v4i16_t*)p)); }
; __device__ __forceinline__ void finishSM(f32x16& p0, f32x16& p1, float alpha, float& l_reg, bf16x8& pa0, bf16x8& pa1, bf16x8& pa2, bf16x8& pa3) {
; #pragma unroll
;     for (int r = 0; r < 16; ++r) p1[r] = __builtin_amdgcn_exp2f(p1[r]);
;     float ps = 0;
; #pragma unroll
;     for (int r = 0; r < 16; ++r) ps += p0[r];
; #pragma unroll
;     for (int r = 0; r < 16; ++r) ps += p1[r];
;     { auto rr = __builtin_amdgcn_permlane32_swap(__float_as_uint(ps), __float_as_uint(ps), false, false);
;       ps = __uint_as_float(rr[0]) + __uint_as_float(rr[1]); }
;     l_reg = l_reg * alpha + ps;
;     ...
;     ATT_PK4(p0, 0, pa0); ATT_PK4(p0, 8, pa1); ATT_PK4(p1, 0, pa2); ATT_PK4(p1, 8, pa3);
;     ...
; }
; template <int D0> __device__ __forceinline__ void pv_one(f32x16& od, LAS const unsigned char* vb, bf16x8 pa0, bf16x8 pa1, bf16x8 pa2, bf16x8 pa3) {
;     const s16x4 l0 = tr_read(vb + v_rd_off(D0, 0, 0)), h0 = tr_read(vb + v_rd_off(D0, 0, 1)), l1 = tr_read(vb + v_rd_off(D0, 1, 0)), h1 = tr_read(vb + v_rd_off(D0, 1, 1));
;     const s16x4 l2 = tr_read(vb + v_rd_off(D0, 2, 0)), h2 = tr_read(vb + v_rd_off(D0, 2, 1)), l3 = tr_read(vb + v_rd_off(D0, 3, 0)), h3 = tr_read(vb + v_rd_off(D0, 3, 1));
;     ...
;     od = __builtin_amdgcn_mfma_f32_32x32x16_bf16(pa0, ATT_PK(l0, h0), od, 0, 0, 0);
;     od = __builtin_amdgcn_mfma_f32_32x32x16_bf16(pa1, ATT_PK(l1, h1), od, 0, 0, 0);
;     od = __builtin_amdgcn_mfma_f32_32x32x16_bf16(pa2, ATT_PK(l2, h2), od, 0, 0, 0);
;     od = __builtin_amdgcn_mfma_f32_32x32x16_bf16(pa3, ATT_PK(l3, h3), od, 0, 0, 0);
;     ...
; }
; __device__ __forceinline__ void pv_d0(f32x16* o, LAS const unsigned char* vb, bf16x8 pa0, bf16x8 pa1, bf16x8 pa2, bf16x8 pa3) {
;     pv_one<0>(o[0], vb, pa0, pa1, pa2, pa3); pv_one<1>(o[1], vb, pa0, pa1, pa2, pa3); pv_one<2>(o[2], vb, pa0, pa1, pa2, pa3); pv_one<3>(o[3], vb, pa0, pa1, pa2, pa3);
.LBB0_666:
	v_sub_f32_e32 v85, v106, v180
	v_sub_f32_e32 v86, v107, v180
	v_sub_f32_e32 v88, v95, v180
	v_exp_f32_e32 v95, v85
	v_sub_f32_e32 v87, v94, v180
	v_sub_f32_e32 v89, v96, v180
	v_exp_f32_e32 v96, v86
	v_sub_f32_e32 v90, v97, v180
	v_exp_f32_e32 v97, v87
	v_sub_f32_e32 v91, v98, v180
	v_exp_f32_e32 v98, v88
	v_sub_f32_e32 v68, v68, v180
	v_sub_f32_e32 v94, v99, v180
	v_exp_f32_e32 v99, v89
	v_exp_f32_e32 v115, v68
	v_add_f32_e32 v68, 0, v95
	v_sub_f32_e32 v107, v100, v180
	v_exp_f32_e32 v100, v90
	v_add_f32_e32 v68, v96, v68
	v_sub_f32_e32 v108, v101, v180
	v_exp_f32_e32 v101, v91
	v_add_f32_e32 v68, v97, v68
	v_sub_f32_e32 v92, v92, v180
	v_sub_f32_e32 v106, v102, v180
	v_exp_f32_e32 v102, v94
	v_add_f32_e32 v68, v98, v68
	v_sub_f32_e32 v93, v93, v180
	v_exp_f32_e32 v87, v92
	v_add_f32_e32 v68, v99, v68
	v_sub_f32_e32 v104, v104, v180
	v_exp_f32_e32 v88, v93
	v_add_f32_e32 v68, v100, v68
	v_sub_f32_e32 v105, v105, v180
	v_exp_f32_e32 v89, v104
	v_add_f32_e32 v68, v101, v68
	v_exp_f32_e32 v90, v105
	v_add_f32_e32 v68, v102, v68
	v_sub_f32_e32 v103, v103, v180
	v_exp_f32_e32 v91, v106
	v_add_f32_e32 v68, v87, v68
	v_exp_f32_e32 v92, v103
	v_add_f32_e32 v68, v88, v68
	v_exp_f32_e32 v93, v107
	v_add_f32_e32 v68, v89, v68
	v_exp_f32_e32 v94, v108
	v_sub_f32_e32 v76, v76, v180
	v_add_f32_e32 v68, v90, v68
	v_sub_f32_e32 v77, v77, v180
	v_exp_f32_e32 v103, v76
	v_add_f32_e32 v68, v91, v68
	v_sub_f32_e32 v78, v78, v180
	v_exp_f32_e32 v104, v77
	v_add_f32_e32 v68, v92, v68
	v_sub_f32_e32 v79, v79, v180
	v_exp_f32_e32 v105, v78
	v_add_f32_e32 v68, v93, v68
	v_sub_f32_e32 v80, v80, v180
	v_exp_f32_e32 v106, v79
	v_add_f32_e32 v68, v94, v68
	v_sub_f32_e32 v81, v81, v180
	v_exp_f32_e32 v107, v80
	v_add_f32_e32 v68, v103, v68
	v_sub_f32_e32 v82, v82, v180
	v_exp_f32_e32 v108, v81
	v_add_f32_e32 v68, v104, v68
	v_sub_f32_e32 v83, v83, v180
	v_exp_f32_e32 v109, v82
	v_add_f32_e32 v68, v105, v68
	v_sub_f32_e32 v74, v74, v180
	v_exp_f32_e32 v110, v83
	v_add_f32_e32 v68, v106, v68
	v_sub_f32_e32 v75, v75, v180
	v_exp_f32_e32 v111, v74
	v_add_f32_e32 v68, v107, v68
	v_sub_f32_e32 v72, v72, v180
	v_exp_f32_e32 v112, v75
	v_add_f32_e32 v68, v108, v68
	v_sub_f32_e32 v73, v73, v180
	v_exp_f32_e32 v113, v72
	v_add_f32_e32 v68, v109, v68
	v_sub_f32_e32 v70, v70, v180
	v_exp_f32_e32 v114, v73
	v_add_f32_e32 v68, v110, v68
	v_sub_f32_e32 v71, v71, v180
	v_exp_f32_e32 v70, v70
	v_add_f32_e32 v68, v111, v68
	v_exp_f32_e32 v71, v71
	v_add_f32_e32 v68, v112, v68
	v_sub_f32_e32 v69, v69, v180
	v_add_f32_e32 v68, v113, v68
	v_exp_f32_e32 v116, v69
	v_add_f32_e32 v68, v114, v68
	v_add_f32_e32 v68, v70, v68
	v_add_f32_e32 v68, v71, v68
	v_add_f32_e32 v68, v115, v68
	v_add_f32_e32 v85, v116, v68
	v_mov_b32_e32 v86, v85
	s_nop 1
	v_permlane32_swap_b32_e32 v85, v86
	v_cvt_pk_bf16_f32 v80, v95, v96
	v_cvt_pk_bf16_f32 v81, v97, v98
	v_cvt_pk_bf16_f32 v82, v99, v100
	v_cvt_pk_bf16_f32 v83, v101, v102
	v_cvt_pk_bf16_f32 v76, v87, v88
	v_cvt_pk_bf16_f32 v77, v89, v90
	v_cvt_pk_bf16_f32 v78, v91, v92
	v_cvt_pk_bf16_f32 v79, v93, v94
	v_cvt_pk_bf16_f32 v72, v103, v104
	v_cvt_pk_bf16_f32 v73, v105, v106
	v_cvt_pk_bf16_f32 v74, v107, v108
	v_cvt_pk_bf16_f32 v75, v109, v110
	v_cvt_pk_bf16_f32 v68, v111, v112
	v_cvt_pk_bf16_f32 v69, v113, v114
	v_cvt_pk_bf16_f32 v70, v70, v71
	v_cvt_pk_bf16_f32 v71, v115, v116
	v_permlane32_swap_b32_e32 v80, v82
	v_permlane32_swap_b32_e32 v81, v83
	v_permlane32_swap_b32_e32 v76, v78
	v_permlane32_swap_b32_e32 v77, v79
	v_permlane32_swap_b32_e32 v72, v74
	v_permlane32_swap_b32_e32 v73, v75
	v_permlane32_swap_b32_e32 v68, v70
	v_permlane32_swap_b32_e32 v69, v71
	ds_read_b64_tr_b16 v[88:89], v196 offset:16384
	ds_read_b64_tr_b16 v[90:91], v196 offset:18432
	s_waitcnt lgkmcnt(0)
	v_mfma_f32_32x32x16_bf16 v[52:67], v[80:83], v[88:91], v[52:67]
	ds_read_b64_tr_b16 v[88:89], v196 offset:20480
	ds_read_b64_tr_b16 v[90:91], v196 offset:22528
	s_waitcnt lgkmcnt(0)
	v_mfma_f32_32x32x16_bf16 v[52:67], v[76:79], v[88:91], v[52:67]
	ds_read_b64_tr_b16 v[88:89], v196 offset:24576
	ds_read_b64_tr_b16 v[90:91], v196 offset:26624
	s_waitcnt lgkmcnt(0)
	v_mfma_f32_32x32x16_bf16 v[52:67], v[72:75], v[88:91], v[52:67]
	ds_read_b64_tr_b16 v[88:89], v196 offset:28672
	ds_read_b64_tr_b16 v[90:91], v196 offset:30720
	s_waitcnt lgkmcnt(0)
	v_mfma_f32_32x32x16_bf16 v[52:67], v[68:71], v[88:91], v[52:67]
	ds_read_b64_tr_b16 v[88:89], v196 offset:16896
	ds_read_b64_tr_b16 v[90:91], v196 offset:18944
	s_waitcnt lgkmcnt(0)
	v_mfma_f32_32x32x16_bf16 v[36:51], v[80:83], v[88:91], v[36:51]
	ds_read_b64_tr_b16 v[88:89], v196 offset:20992
	ds_read_b64_tr_b16 v[90:91], v196 offset:23040
	s_waitcnt lgkmcnt(0)
	v_mfma_f32_32x32x16_bf16 v[36:51], v[76:79], v[88:91], v[36:51]
	ds_read_b64_tr_b16 v[88:89], v196 offset:25088
	ds_read_b64_tr_b16 v[90:91], v196 offset:27136
	s_waitcnt lgkmcnt(0)
	v_mfma_f32_32x32x16_bf16 v[36:51], v[72:75], v[88:91], v[36:51]
	ds_read_b64_tr_b16 v[88:89], v196 offset:29184
	ds_read_b64_tr_b16 v[90:91], v196 offset:31232
	s_waitcnt lgkmcnt(0)
	v_mfma_f32_32x32x16_bf16 v[36:51], v[68:71], v[88:91], v[36:51]
	ds_read_b64_tr_b16 v[88:89], v196 offset:17408
	ds_read_b64_tr_b16 v[90:91], v196 offset:19456
	s_waitcnt lgkmcnt(0)
	v_mfma_f32_32x32x16_bf16 v[20:35], v[80:83], v[88:91], v[20:35]
	ds_read_b64_tr_b16 v[88:89], v196 offset:21504
	ds_read_b64_tr_b16 v[90:91], v196 offset:23552
	s_waitcnt lgkmcnt(0)
	v_mfma_f32_32x32x16_bf16 v[20:35], v[76:79], v[88:91], v[20:35]
	ds_read_b64_tr_b16 v[88:89], v196 offset:25600
	ds_read_b64_tr_b16 v[90:91], v196 offset:27648
	s_waitcnt lgkmcnt(0)
; #define ATT_SBAR() __builtin_amdgcn_sched_barrier(0)
; __device__ __forceinline__ int crow(int r, int hi) { return (r & 3) + 8 * (r >> 2) + 4 * hi; }
; template <bool MOBA>
; __device__ __forceinline__ void run_unit(const UnitDesc& U, LAS unsigned char* lds, f32x16 (&o)[4], float (&rli)[16]) {
;     ...
;     finishSM(pB0, pB1, alB, l_reg, pa0, pa1, pa2, pa3); ATT_SBAR();
;     pv_d0(o, vb0 + SHM_V, pa0, pa1, pa2, pa3);
;     if (hi == 0) li_l[r32] = l_reg;
;     asm volatile("s_waitcnt lgkmcnt(0)" ::: "memory");
; #pragma unroll
;     for (int r = 0; r < 16; ++r) rli[r] = 1.0f / li_l[crow(r, hi)];
;     __syncthreads();
; __global__ void __launch_bounds__(NWAVES * 64, 2) mega_fwd(Args args) {
;     ...
;                     { unsigned zz[64];
; #pragma unroll
;                       for (int r = 0; r < 16; ++r) { const int bt = b * SEQ + L * 256 + wave * 32 + att::crow(r, hi);
; #pragma unroll
;                           for (int d0 = 0; d0 < 4; ++d0) zz[r * 4 + d0] = *(const unsigned*)(PROJ + (size_t)bt * NC + C_ZA + h * 128 + d0 * 32 + (r32 & ~1)); }
	v_mfma_f32_32x32x16_bf16 v[20:35], v[72:75], v[88:91], v[20:35]
	ds_read_b64_tr_b16 v[88:89], v196 offset:29696
	ds_read_b64_tr_b16 v[90:91], v196 offset:31744
	s_waitcnt lgkmcnt(0)
	v_mfma_f32_32x32x16_bf16 v[20:35], v[68:71], v[88:91], v[20:35]
	ds_read_b64_tr_b16 v[88:89], v196 offset:17920
	ds_read_b64_tr_b16 v[90:91], v196 offset:19968
	s_waitcnt lgkmcnt(0)
	v_mfma_f32_32x32x16_bf16 v[4:19], v[80:83], v[88:91], v[4:19]
	ds_read_b64_tr_b16 v[80:81], v196 offset:22016
	ds_read_b64_tr_b16 v[82:83], v196 offset:24064
	s_waitcnt lgkmcnt(0)
	v_mfma_f32_32x32x16_bf16 v[4:19], v[76:79], v[80:83], v[4:19]
	ds_read_b64_tr_b16 v[76:77], v196 offset:26112
	ds_read_b64_tr_b16 v[78:79], v196 offset:28160
	s_waitcnt lgkmcnt(0)
	v_mfma_f32_32x32x16_bf16 v[4:19], v[72:75], v[76:79], v[4:19]
	ds_read_b64_tr_b16 v[72:73], v196 offset:30208
	ds_read_b64_tr_b16 v[74:75], v196 offset:32256
	s_waitcnt lgkmcnt(0)
	v_mfma_f32_32x32x16_bf16 v[4:19], v[68:71], v[72:75], v[4:19]
	s_and_saveexec_b64 s[0:1], s[6:7]
	v_add_f32_e32 v1, v1, v2
	v_fmac_f32_e32 v1, v199, v222
	v_add_f32_e32 v2, v85, v86
	v_fmac_f32_e32 v2, v1, v84
	ds_write_b32 v198, v2
	s_or_b64 exec, exec, s[0:1]
	s_waitcnt lgkmcnt(0)
	ds_read_b128 v[80:83], v197
	ds_read_b128 v[76:79], v197 offset:32
	v_mov_b32_e32 v167, v219
	s_mov_b32 s4, 0xe800
	s_mov_b64 s[6:7], 0x1800
	s_waitcnt lgkmcnt(1)
	v_div_scale_f32 v1, s[0:1], v80, v80, 1.0
	v_rcp_f32_e32 v2, v1
	v_readlane_b32 s0, v254, 25
	v_readlane_b32 s1, v254, 50
	s_add_i32 s0, s1, s0
	v_fma_f32 v68, -v1, v2, 1.0
	v_fmac_f32_e32 v2, v68, v2
	v_div_scale_f32 v68, vcc, 1.0, v80, 1.0
	v_mul_f32_e32 v69, v68, v2
	v_fma_f32 v70, -v1, v69, v68
	v_fmac_f32_e32 v69, v70, v2
	v_fma_f32 v1, -v1, v69, v68
	v_div_fmas_f32 v1, v1, v2, v69
	v_div_fixup_f32 v111, v1, v80, 1.0
	ds_read_b128 v[72:75], v197 offset:64
	ds_read_b128 v[68:71], v197 offset:96
	s_waitcnt lgkmcnt(0)
	s_barrier
	s_movk_i32 s5, 0x1000
	v_ashrrev_i32_e32 v1, 3, v167
	v_and_b32_e32 v1, -4, v1
	v_add_u32_e32 v112, s0, v1
	v_readlane_b32 s0, v253, 48
	v_readlane_b32 s1, v253, 49
	v_and_b32_e32 v170, 30, v167
	v_lshlrev_b32_e32 v2, 1, v170
	v_mov_b64_e32 v[114:115], s[0:1]
	v_mad_i64_i32 v[84:85], s[0:1], v112, s4, v[114:115]
	v_lshl_add_u64 v[84:85], v[84:85], 0, s[2:3]
	v_lshl_add_u64 v[84:85], v[84:85], 0, v[2:3]
	v_lshl_add_u64 v[86:87], v[84:85], 0, s[6:7]
	v_add_co_u32_e32 v84, vcc, s5, v84
	v_or_b32_e32 v110, 1, v112
	s_nop 0
	v_addc_co_u32_e32 v85, vcc, 0, v85, vcc
	global_load_dword v166, v[84:85], off offset:2048 nt
	global_load_dword v165, v[86:87], off offset:64 nt
	global_load_dword v164, v[86:87], off offset:128 nt
	global_load_dword v163, v[86:87], off offset:192 nt
	v_mad_i64_i32 v[84:85], s[0:1], v110, s4, v[114:115]
	v_lshl_add_u64 v[84:85], v[84:85], 0, s[2:3]
	v_lshl_add_u64 v[84:85], v[84:85], 0, v[2:3]
	v_lshl_add_u64 v[86:87], v[84:85], 0, s[6:7]
	v_add_co_u32_e32 v84, vcc, s5, v84
	v_or_b32_e32 v108, 2, v112
	s_nop 0
	v_addc_co_u32_e32 v85, vcc, 0, v85, vcc
	global_load_dword v162, v[84:85], off offset:2048 nt
	global_load_dword v161, v[86:87], off offset:64 nt
	global_load_dword v160, v[86:87], off offset:128 nt
	global_load_dword v109, v[86:87], off offset:192 nt
	v_mad_i64_i32 v[84:85], s[0:1], v108, s4, v[114:115]
	v_lshl_add_u64 v[84:85], v[84:85], 0, s[2:3]
	v_lshl_add_u64 v[84:85], v[84:85], 0, v[2:3]
	v_lshl_add_u64 v[86:87], v[84:85], 0, s[6:7]
	v_add_co_u32_e32 v84, vcc, s5, v84
	v_or_b32_e32 v106, 3, v112
	s_nop 0
	v_addc_co_u32_e32 v85, vcc, 0, v85, vcc
	global_load_dword v159, v[84:85], off offset:2048 nt
	global_load_dword v158, v[86:87], off offset:64 nt
	global_load_dword v157, v[86:87], off offset:128 nt
	global_load_dword v107, v[86:87], off offset:192 nt
	v_mad_i64_i32 v[84:85], s[0:1], v106, s4, v[114:115]
	v_lshl_add_u64 v[84:85], v[84:85], 0, s[2:3]
	v_lshl_add_u64 v[84:85], v[84:85], 0, v[2:3]
	v_lshl_add_u64 v[86:87], v[84:85], 0, s[6:7]
	v_add_co_u32_e32 v84, vcc, s5, v84
	v_add_u32_e32 v104, 8, v112
	s_nop 0
	v_addc_co_u32_e32 v85, vcc, 0, v85, vcc
	global_load_dword v156, v[84:85], off offset:2048 nt
	global_load_dword v155, v[86:87], off offset:64 nt
	global_load_dword v154, v[86:87], off offset:128 nt
	global_load_dword v105, v[86:87], off offset:192 nt
	v_mad_i64_i32 v[84:85], s[0:1], v104, s4, v[114:115]
	v_lshl_add_u64 v[84:85], v[84:85], 0, s[2:3]
	v_lshl_add_u64 v[84:85], v[84:85], 0, v[2:3]
	v_lshl_add_u64 v[86:87], v[84:85], 0, s[6:7]
	v_add_co_u32_e32 v84, vcc, s5, v84
	v_add_u32_e32 v102, 9, v112
	s_nop 0
	v_addc_co_u32_e32 v85, vcc, 0, v85, vcc
	global_load_dword v153, v[84:85], off offset:2048 nt
	global_load_dword v152, v[86:87], off offset:64 nt
	global_load_dword v151, v[86:87], off offset:128 nt
	global_load_dword v103, v[86:87], off offset:192 nt
	v_mad_i64_i32 v[84:85], s[0:1], v102, s4, v[114:115]
	v_lshl_add_u64 v[84:85], v[84:85], 0, s[2:3]
	v_lshl_add_u64 v[84:85], v[84:85], 0, v[2:3]
	v_lshl_add_u64 v[86:87], v[84:85], 0, s[6:7]
	v_add_co_u32_e32 v84, vcc, s5, v84
	v_add_u32_e32 v100, 10, v112
	s_nop 0
	v_addc_co_u32_e32 v85, vcc, 0, v85, vcc
	global_load_dword v150, v[84:85], off offset:2048 nt
	global_load_dword v149, v[86:87], off offset:64 nt
	global_load_dword v148, v[86:87], off offset:128 nt
	global_load_dword v101, v[86:87], off offset:192 nt
	v_mad_i64_i32 v[84:85], s[0:1], v100, s4, v[114:115]
	v_lshl_add_u64 v[84:85], v[84:85], 0, s[2:3]
	v_lshl_add_u64 v[84:85], v[84:85], 0, v[2:3]
	v_lshl_add_u64 v[86:87], v[84:85], 0, s[6:7]
	v_add_co_u32_e32 v84, vcc, s5, v84
	v_add_u32_e32 v98, 11, v112
	s_nop 0
	v_addc_co_u32_e32 v85, vcc, 0, v85, vcc
	global_load_dword v147, v[84:85], off offset:2048 nt
; __device__ __forceinline__ float bflo(unsigned w) { return __uint_as_float(w << 16); }
; __device__ __forceinline__ float bfhi(unsigned w) { return __uint_as_float(w & 0xffff0000u); }
; __device__ __forceinline__ unsigned pk2(float lo, float hi) { return f2bf(lo) | (f2bf(hi) << 16); }
; __device__ __forceinline__ int crow(int r, int hi) { return (r & 3) + 8 * (r >> 2) + 4 * hi; }
; __global__ void __launch_bounds__(NWAVES * 64, 2) mega_fwd(Args args) {
;     ...
;                     { unsigned zz[64];
; #pragma unroll
;                       for (int r = 0; r < 16; ++r) { const int bt = b * SEQ + L * 256 + wave * 32 + att::crow(r, hi);
; #pragma unroll
;                           for (int d0 = 0; d0 < 4; ++d0) zz[r * 4 + d0] = *(const unsigned*)(PROJ + (size_t)bt * NC + C_ZA + h * 128 + d0 * 32 + (r32 & ~1)); }
;                       asm volatile("" ::: "memory");
; #pragma unroll
;                       for (int r = 0; r < 16; ++r) { const int bt = b * SEQ + L * 256 + wave * 32 + att::crow(r, hi);
; #pragma unroll
;                           for (int d0 = 0; d0 < 4; ++d0) { const float val = o[d0][r] * rli[r], vn = __shfl_xor(val, 1); const int col = h * 128 + d0 * 32 + r32;
;                               if ((r32 & 1) == 0) *(unsigned*)(Y + (size_t)bt * YS + col) = pk2(val * bflo(zz[r * 4 + d0]), vn * bfhi(zz[r * 4 + d0])); } } }
	global_load_dword v146, v[86:87], off offset:64 nt
	global_load_dword v145, v[86:87], off offset:128 nt
	global_load_dword v99, v[86:87], off offset:192 nt
	v_mad_i64_i32 v[84:85], s[0:1], v98, s4, v[114:115]
	v_lshl_add_u64 v[84:85], v[84:85], 0, s[2:3]
	v_lshl_add_u64 v[84:85], v[84:85], 0, v[2:3]
	v_lshl_add_u64 v[86:87], v[84:85], 0, s[6:7]
	v_add_co_u32_e32 v84, vcc, s5, v84
	v_add_u32_e32 v96, 16, v112
	s_nop 0
	v_addc_co_u32_e32 v85, vcc, 0, v85, vcc
	global_load_dword v144, v[84:85], off offset:2048 nt
	global_load_dword v143, v[86:87], off offset:64 nt
	global_load_dword v142, v[86:87], off offset:128 nt
	global_load_dword v97, v[86:87], off offset:192 nt
	v_mad_i64_i32 v[84:85], s[0:1], v96, s4, v[114:115]
	v_lshl_add_u64 v[84:85], v[84:85], 0, s[2:3]
	v_lshl_add_u64 v[84:85], v[84:85], 0, v[2:3]
	v_lshl_add_u64 v[86:87], v[84:85], 0, s[6:7]
	v_add_co_u32_e32 v84, vcc, s5, v84
	v_add_u32_e32 v94, 17, v112
	s_nop 0
	v_addc_co_u32_e32 v85, vcc, 0, v85, vcc
	global_load_dword v141, v[84:85], off offset:2048 nt
	global_load_dword v140, v[86:87], off offset:64 nt
	global_load_dword v139, v[86:87], off offset:128 nt
	global_load_dword v95, v[86:87], off offset:192 nt
	v_mad_i64_i32 v[84:85], s[0:1], v94, s4, v[114:115]
	v_lshl_add_u64 v[84:85], v[84:85], 0, s[2:3]
	v_lshl_add_u64 v[84:85], v[84:85], 0, v[2:3]
	v_lshl_add_u64 v[86:87], v[84:85], 0, s[6:7]
	v_add_co_u32_e32 v84, vcc, s5, v84
	v_add_u32_e32 v92, 18, v112
	s_nop 0
	v_addc_co_u32_e32 v85, vcc, 0, v85, vcc
	global_load_dword v138, v[84:85], off offset:2048 nt
	global_load_dword v137, v[86:87], off offset:64 nt
	global_load_dword v136, v[86:87], off offset:128 nt
	global_load_dword v93, v[86:87], off offset:192 nt
	v_mad_i64_i32 v[84:85], s[0:1], v92, s4, v[114:115]
	v_lshl_add_u64 v[84:85], v[84:85], 0, s[2:3]
	v_lshl_add_u64 v[84:85], v[84:85], 0, v[2:3]
	v_lshl_add_u64 v[86:87], v[84:85], 0, s[6:7]
	v_add_co_u32_e32 v84, vcc, s5, v84
	v_add_u32_e32 v90, 19, v112
	s_nop 0
	v_addc_co_u32_e32 v85, vcc, 0, v85, vcc
	global_load_dword v135, v[84:85], off offset:2048 nt
	global_load_dword v134, v[86:87], off offset:64 nt
	global_load_dword v133, v[86:87], off offset:128 nt
	global_load_dword v91, v[86:87], off offset:192 nt
	v_mad_i64_i32 v[84:85], s[0:1], v90, s4, v[114:115]
	v_lshl_add_u64 v[84:85], v[84:85], 0, s[2:3]
	v_lshl_add_u64 v[84:85], v[84:85], 0, v[2:3]
	v_lshl_add_u64 v[86:87], v[84:85], 0, s[6:7]
	v_add_co_u32_e32 v84, vcc, s5, v84
	v_add_u32_e32 v88, 24, v112
	s_nop 0
	v_addc_co_u32_e32 v85, vcc, 0, v85, vcc
	global_load_dword v132, v[84:85], off offset:2048 nt
	global_load_dword v131, v[86:87], off offset:64 nt
	global_load_dword v130, v[86:87], off offset:128 nt
	global_load_dword v89, v[86:87], off offset:192 nt
	v_mad_i64_i32 v[84:85], s[0:1], v88, s4, v[114:115]
	v_lshl_add_u64 v[84:85], v[84:85], 0, s[2:3]
	v_lshl_add_u64 v[84:85], v[84:85], 0, v[2:3]
	v_lshl_add_u64 v[86:87], v[84:85], 0, s[6:7]
	v_add_co_u32_e32 v84, vcc, s5, v84
	v_add_u32_e32 v80, 27, v112
	s_nop 0
	v_addc_co_u32_e32 v85, vcc, 0, v85, vcc
	global_load_dword v129, v[84:85], off offset:2048 nt
	global_load_dword v128, v[86:87], off offset:64 nt
	global_load_dword v127, v[86:87], off offset:128 nt
	s_nop 0
	global_load_dword v87, v[86:87], off offset:192 nt
	v_add_u32_e32 v86, 25, v112
	v_mad_i64_i32 v[84:85], s[0:1], v86, s4, v[114:115]
	v_lshl_add_u64 v[84:85], v[84:85], 0, s[2:3]
	v_lshl_add_u64 v[84:85], v[84:85], 0, v[2:3]
	v_lshl_add_u64 v[116:117], v[84:85], 0, s[6:7]
	v_add_co_u32_e32 v84, vcc, s5, v84
	v_ashrrev_i32_e32 v113, 31, v112
	s_nop 0
	v_addc_co_u32_e32 v85, vcc, 0, v85, vcc
	global_load_dword v126, v[84:85], off offset:2048 nt
	global_load_dword v125, v[116:117], off offset:64 nt
	global_load_dword v124, v[116:117], off offset:128 nt
	s_nop 0
	global_load_dword v85, v[116:117], off offset:192 nt
	v_add_u32_e32 v84, 26, v112
	v_mad_i64_i32 v[116:117], s[0:1], v84, s4, v[114:115]
	v_lshl_add_u64 v[116:117], v[116:117], 0, s[2:3]
	v_lshl_add_u64 v[116:117], v[116:117], 0, v[2:3]
	v_mad_i64_i32 v[114:115], s[0:1], v80, s4, v[114:115]
	v_lshl_add_u64 v[118:119], v[116:117], 0, s[6:7]
	v_add_co_u32_e32 v116, vcc, s5, v116
	v_lshl_add_u64 v[114:115], v[114:115], 0, s[2:3]
	s_nop 0
	v_addc_co_u32_e32 v117, vcc, 0, v117, vcc
	v_lshl_add_u64 v[114:115], v[114:115], 0, v[2:3]
	v_lshl_add_u64 v[168:169], v[114:115], 0, s[6:7]
	v_add_co_u32_e32 v114, vcc, s5, v114
	global_load_dword v123, v[116:117], off offset:2048 nt
	global_load_dword v122, v[118:119], off offset:64 nt
	global_load_dword v121, v[118:119], off offset:128 nt
	global_load_dword v120, v[118:119], off offset:192 nt
	v_addc_co_u32_e32 v115, vcc, 0, v115, vcc
	global_load_dword v119, v[114:115], off offset:2048 nt
	global_load_dword v117, v[168:169], off offset:64 nt
	global_load_dword v116, v[168:169], off offset:128 nt
	global_load_dword v1, v[168:169], off offset:192 nt
	v_and_b32_e32 v114, 64, v229
	v_xor_b32_e32 v2, 1, v229
	v_add_u32_e32 v114, 64, v114
	v_cmp_lt_i32_e32 vcc, v2, v114
	v_mul_f32_e32 v115, v111, v52
	v_readlane_b32 s2, v254, 51
	v_cndmask_b32_e32 v2, v229, v2, vcc
	v_lshlrev_b32_e32 v118, 2, v2
	ds_bpermute_b32 v114, v118, v115
	v_and_b32_e32 v2, 1, v167
	v_readlane_b32 s4, v253, 57
	v_cmp_eq_u32_e64 s[0:1], 0, v2
	v_or_b32_e32 v2, s2, v170
	v_lshlrev_b64 v[112:113], 13, v[112:113]
	v_readlane_b32 s5, v253, 58
	v_lshlrev_b32_e32 v2, 1, v2
	s_nop 0
	v_lshl_add_u64 v[112:113], s[4:5], 0, v[112:113]
	s_and_saveexec_b64 s[4:5], s[0:1]
	s_cbranch_execz .LBB0_670
	s_waitcnt vmcnt(62)
	v_lshlrev_b32_e32 v167, 16, v166
	v_and_b32_e32 v166, 0xffff0000, v166
	s_waitcnt lgkmcnt(0)
	v_pk_mul_f32 v[114:115], v[114:115], v[166:167]
	s_nop 0
	v_and_b32_sdwa v52, v115, v227 dst_sel:DWORD dst_unused:UNUSED_PAD src0_sel:WORD_1 src1_sel:DWORD
	v_and_b32_sdwa v166, v114, v227 dst_sel:DWORD dst_unused:UNUSED_PAD src0_sel:WORD_1 src1_sel:DWORD
	v_add3_u32 v52, v115, v52, s97
	v_add3_u32 v114, v114, v166, s97
	v_lshrrev_b32_e32 v52, 16, v52
	v_and_or_b32 v52, v114, s8, v52
	v_lshl_add_u64 v[114:115], v[112:113], 0, v[2:3]
	global_store_dword v[114:115], v52, off

; #define INP(k) launder_p(args.in[k])
; __global__ void __launch_bounds__(NWAVES * 64, 2) mega_fwd(Args args) {
;     ...
;                             const float* q1 = INP(6) + l * 128; const float* k1 = INP(7) + l * 128; const float* q2 = INP(8) + l * 128; const float* k2 = INP(9) + l * 128;
;                             const float s1 = wave_sum(q1[lane_p] * k1[lane_p] + q1[lane_p + 64] * k1[lane_p + 64]), s2 = wave_sum(q2[lane_p] * k2[lane_p] + q2[lane_p + 64] * k2[lane_p + 64]);
;                             const float lam = expf(s1) - expf(s2) + lam_init;
;                             asm volatile("s_waitcnt vmcnt(0)" ::: "memory");
;                             { f32x4 t[16];
; #pragma unroll
;                               for (int r = 0; r < 16; ++r) t[r] = *(const f32x4*)(sp + r * 4);
;                               asm volatile("" ::: "memory");
; #pragma unroll
;                               for (int r = 0; r < 16; ++r) { const float a_ = lam * rli[r];
; #pragma unroll
;                                   for (int d0 = 0; d0 < 4; ++d0) o[d0][r] = t[r][d0] - a_ * o[d0][r]; } }
.LBB0_854:
	v_readlane_b32 s8, v252, 14
	v_readlane_b32 s9, v252, 15
	v_readlane_b32 s10, v252, 16
	v_readlane_b32 s11, v252, 17
	v_readlane_b32 s12, v252, 18
	v_readlane_b32 s13, v252, 19
	v_readlane_b32 s14, v252, 20
	v_readlane_b32 s15, v252, 21
	v_readlane_b32 s16, v252, 22
	v_readlane_b32 s17, v252, 23
	v_readlane_b32 s18, v252, 24
	v_readlane_b32 s19, v252, 25
	v_readlane_b32 s20, v252, 26
	v_readlane_b32 s21, v252, 27
	v_readlane_b32 s22, v252, 28
	v_readlane_b32 s23, v252, 29
	s_mov_b64 s[8:9], s[12:13]
	s_mov_b64 s[10:11], s[14:15]
	s_mov_b64 s[12:13], s[16:17]
	s_mov_b64 s[14:15], s[18:19]
	s_mov_b64 s[16:17], s[20:21]
	s_mov_b64 s[0:1], s[16:17]
	v_readlane_b32 s28, v254, 39
	s_mov_b64 s[18:19], s[22:23]
	v_readlane_b32 s29, v254, 40
	s_add_u32 s8, s0, s28
	s_addc_u32 s9, s1, s29
	s_mov_b64 s[0:1], s[18:19]
	s_add_u32 s10, s0, s28
	v_readlane_b32 s12, v252, 35
	v_ashrrev_i32_e32 v239, 31, v238
	v_lshrrev_b64 v[132:133], 2, v[68:69]
	s_addc_u32 s11, s1, s29
	v_readlane_b32 s13, v252, 36
	v_readlane_b32 s14, v252, 37
	v_readlane_b32 s15, v252, 38
	v_lshlrev_b64 v[68:69], 2, v[238:239]
	s_mov_b64 s[0:1], s[12:13]
	s_mov_b64 s[6:7], s[14:15]
	v_lshl_add_u64 v[70:71], s[8:9], 0, v[68:69]
	v_lshl_add_u64 v[74:75], s[10:11], 0, v[68:69]
	global_load_dword v72, v[70:71], off
	global_load_dword v76, v[74:75], off
	global_load_dword v73, v[70:71], off offset:256
	global_load_dword v77, v[74:75], off offset:256
	v_and_b32_e32 v1, 64, v229
	s_add_u32 s0, s0, s28
	s_addc_u32 s1, s1, s29
	s_add_u32 s6, s6, s28
	s_addc_u32 s7, s7, s29
	s_mov_b32 s2, 0x42b17218
	v_mov_b32_e32 v134, v36
	v_mov_b32_e32 v135, v20
	v_readlane_b32 s16, v252, 39
	v_readlane_b32 s17, v252, 40
	v_readlane_b32 s18, v252, 41
	v_readlane_b32 s19, v252, 42
	v_readlane_b32 s20, v252, 43
	v_readlane_b32 s21, v252, 44
	v_readlane_b32 s22, v252, 45
	v_readlane_b32 s23, v252, 46
	v_readlane_b32 s24, v252, 47
	v_readlane_b32 s25, v252, 48
	v_readlane_b32 s26, v252, 49
	v_readlane_b32 s27, v252, 50
	s_waitcnt vmcnt(0)
	v_pk_mul_f32 v[70:71], v[72:73], v[76:77]
	s_nop 0
	v_add_f32_e32 v2, v70, v71
	v_add_u32_e32 v70, 64, v1
	v_xor_b32_e32 v1, 1, v229
	v_cmp_lt_i32_e32 vcc, v1, v70
	s_nop 1
	v_cndmask_b32_e32 v1, v229, v1, vcc
	v_lshlrev_b32_e32 v1, 2, v1
	ds_bpermute_b32 v71, v1, v2
	s_waitcnt lgkmcnt(0)
	v_add_f32_e32 v2, v2, v71
	v_xor_b32_e32 v71, 2, v229
	v_cmp_lt_i32_e32 vcc, v71, v70
	s_nop 1
	v_cndmask_b32_e32 v71, v229, v71, vcc
	v_lshlrev_b32_e32 v246, 2, v71
	ds_bpermute_b32 v71, v246, v2
	s_waitcnt lgkmcnt(0)
	v_add_f32_e32 v2, v2, v71
	v_xor_b32_e32 v71, 4, v229
	v_cmp_lt_i32_e32 vcc, v71, v70
	s_nop 1
	v_cndmask_b32_e32 v71, v229, v71, vcc
	v_lshlrev_b32_e32 v247, 2, v71
	ds_bpermute_b32 v71, v247, v2
	s_waitcnt lgkmcnt(0)
	v_add_f32_e32 v2, v2, v71
	v_xor_b32_e32 v71, 8, v229
	v_cmp_lt_i32_e32 vcc, v71, v70
	s_nop 1
	v_cndmask_b32_e32 v71, v229, v71, vcc
	v_lshlrev_b32_e32 v248, 2, v71
	ds_bpermute_b32 v71, v248, v2
	s_waitcnt lgkmcnt(0)
	v_add_f32_e32 v2, v2, v71
	v_xor_b32_e32 v71, 16, v229
	v_cmp_lt_i32_e32 vcc, v71, v70
	s_nop 1
	v_cndmask_b32_e32 v71, v229, v71, vcc
	v_lshlrev_b32_e32 v249, 2, v71
	ds_bpermute_b32 v71, v249, v2
	s_waitcnt lgkmcnt(0)
	v_add_f32_e32 v2, v2, v71
	v_xor_b32_e32 v71, 32, v229
	v_cmp_lt_i32_e32 vcc, v71, v70
	s_nop 1
	v_cndmask_b32_e32 v70, v229, v71, vcc
	v_lshlrev_b32_e32 v76, 2, v70
	ds_bpermute_b32 v70, v76, v2
	s_waitcnt lgkmcnt(0)
	v_add_f32_e32 v2, v2, v70
	v_lshl_add_u64 v[70:71], s[0:1], 0, v[68:69]
	v_lshl_add_u64 v[68:69], s[6:7], 0, v[68:69]
	global_load_dword v72, v[70:71], off
	global_load_dword v74, v[68:69], off
	global_load_dword v73, v[70:71], off offset:256
	global_load_dword v75, v[68:69], off offset:256
	s_mov_b32 s0, 0x3fb8aa3b
	s_mov_b32 s1, 0xc2ce8ed0
	v_cmp_ngt_f32_e32 vcc, s1, v2
	s_waitcnt vmcnt(0)
	v_readlane_b32 s6, v253, 50
	v_readlane_b32 s7, v253, 51
	s_waitcnt vmcnt(0)
	v_pk_mul_f32 v[68:69], v[72:73], v[74:75]
	s_nop 0
	v_add_f32_e32 v68, v68, v69
	ds_bpermute_b32 v69, v1, v68
	s_waitcnt lgkmcnt(0)
	v_add_f32_e32 v68, v68, v69
	ds_bpermute_b32 v69, v246, v68
	s_waitcnt lgkmcnt(0)
	v_add_f32_e32 v68, v68, v69
	ds_bpermute_b32 v69, v247, v68
	s_waitcnt lgkmcnt(0)
	v_add_f32_e32 v68, v68, v69
	ds_bpermute_b32 v69, v248, v68
	s_waitcnt lgkmcnt(0)
	v_add_f32_e32 v68, v68, v69
	ds_bpermute_b32 v69, v249, v68
	s_waitcnt lgkmcnt(0)
	v_add_f32_e32 v68, v68, v69
	ds_bpermute_b32 v69, v76, v68
	s_waitcnt lgkmcnt(0)
	v_add_f32_e32 v68, v68, v69
	v_mul_f32_e32 v69, 0x3fb8aa3b, v2
	v_fma_f32 v70, v2, s0, -v69
	v_rndne_f32_e32 v71, v69
	v_fmac_f32_e32 v70, 0x32a5705f, v2
	v_sub_f32_e32 v69, v69, v71
	v_add_f32_e32 v69, v69, v70
	v_exp_f32_e32 v69, v69
	v_cvt_i32_f32_e32 v70, v71
	v_ldexp_f32 v69, v69, v70
	v_cndmask_b32_e32 v69, 0, v69, vcc
	v_cmp_nlt_f32_e32 vcc, s2, v2
	s_nop 1
	v_cndmask_b32_e32 v2, v243, v69, vcc
	v_mul_f32_e32 v69, 0x3fb8aa3b, v68
	v_fma_f32 v70, v68, s0, -v69
	v_rndne_f32_e32 v71, v69
	v_fmac_f32_e32 v70, 0x32a5705f, v68
	v_sub_f32_e32 v69, v69, v71
	v_add_f32_e32 v69, v69, v70
	v_exp_f32_e32 v69, v69
	v_cvt_i32_f32_e32 v70, v71
	v_cmp_ngt_f32_e32 vcc, s1, v68
	v_readlane_b32 s0, v254, 28
	v_readlane_b32 s1, v254, 29
	v_ldexp_f32 v69, v69, v70
	v_cndmask_b32_e32 v69, 0, v69, vcc
	v_cmp_nlt_f32_e32 vcc, s2, v68
	v_lshl_add_u64 v[236:237], v[132:133], 2, s[0:1]
	s_mov_b64 s[0:1], -1
	v_cndmask_b32_e32 v68, v243, v69, vcc
	v_sub_f32_e32 v2, v2, v68
	global_load_dwordx4 v[80:83], v[234:235], off offset:-1024
	global_load_dwordx4 v[76:79], v[234:235], off offset:-2048
	global_load_dwordx4 v[72:75], v[234:235], off offset:-3072
	global_load_dwordx4 v[68:71], v[234:235], off offset:-4096
	global_load_dwordx4 v[96:99], v[234:235], off offset:3072
	global_load_dwordx4 v[92:95], v[234:235], off offset:2048
	global_load_dwordx4 v[88:91], v[234:235], off offset:1024
	global_load_dwordx4 v[84:87], v[234:235], off
	s_mov_b64 s[100:101], 0x2000
	v_lshl_add_u64 v[234:235], v[234:235], 0, s[100:101]
	global_load_dwordx4 v[112:115], v[234:235], off offset:-1024
	global_load_dwordx4 v[108:111], v[234:235], off offset:-2048
	global_load_dwordx4 v[104:107], v[234:235], off offset:-3072
	global_load_dwordx4 v[100:103], v[234:235], off offset:-4096
	global_load_dwordx4 v[128:131], v[234:235], off offset:3072
	global_load_dwordx4 v[124:127], v[234:235], off offset:2048
	global_load_dwordx4 v[120:123], v[234:235], off offset:1024
	global_load_dwordx4 v[116:119], v[234:235], off
	s_mov_b32 s100, 0xffffe000
	s_mov_b32 s101, -1
	v_lshl_add_u64 v[234:235], v[234:235], 0, s[100:101]
	v_add_f32_e32 v136, v203, v2
	v_mul_f32_e32 v2, v136, v202
	s_and_b64 vcc, exec, s[6:7]
	s_waitcnt vmcnt(12)
; #define INP(k) launder_p(args.in[k])
; __global__ void __launch_bounds__(NWAVES * 64, 2) mega_fwd(Args args) {
;     ...
;                               for (int r = 0; r < 16; ++r) { const float a_ = lam * rli[r];
; #pragma unroll
;                                   for (int d0 = 0; d0 < 4; ++d0) o[d0][r] = t[r][d0] - a_ * o[d0][r]; } }
;                             float* sq = S2 + (size_t)(wave * 64 + lane_p) * 64;
;                             if (vh == 0) {
; #pragma unroll
;                                 for (int r = 0; r < 16; ++r) *(f32x4*)(sq + r * 4) = (f32x4){o[0][r], o[1][r], o[2][r], o[3][r]};
;                             } else { const float* subg = INP(10) + l * 256;
	v_pk_fma_f32 v[68:69], v[2:3], v[134:135], v[68:69] op_sel_hi:[0,1,1] neg_lo:[1,0,0] neg_hi:[1,0,0]
	v_mov_b32_e32 v134, v52
	v_mov_b32_e32 v135, v4
	v_pk_fma_f32 v[70:71], v[2:3], v[134:135], v[70:71] op_sel_hi:[0,1,1] neg_lo:[1,0,0] neg_hi:[1,0,0]
	v_mul_f32_e32 v2, v136, v204
	v_mov_b32_e32 v134, v37
	v_mov_b32_e32 v135, v21
	v_pk_fma_f32 v[72:73], v[2:3], v[134:135], v[72:73] op_sel_hi:[0,1,1] neg_lo:[1,0,0] neg_hi:[1,0,0]
	v_mov_b32_e32 v134, v53
	v_mov_b32_e32 v135, v5
	v_pk_fma_f32 v[74:75], v[2:3], v[134:135], v[74:75] op_sel_hi:[0,1,1] neg_lo:[1,0,0] neg_hi:[1,0,0]
	v_mul_f32_e32 v2, v136, v206
	v_mov_b32_e32 v134, v38
	v_mov_b32_e32 v135, v22
	v_pk_fma_f32 v[76:77], v[2:3], v[134:135], v[76:77] op_sel_hi:[0,1,1] neg_lo:[1,0,0] neg_hi:[1,0,0]
	v_mov_b32_e32 v134, v54
	v_mov_b32_e32 v135, v6
	v_pk_fma_f32 v[78:79], v[2:3], v[134:135], v[78:79] op_sel_hi:[0,1,1] neg_lo:[1,0,0] neg_hi:[1,0,0]
	v_mul_f32_e32 v2, v136, v208
	v_mov_b32_e32 v134, v39
	v_mov_b32_e32 v135, v23
	v_pk_fma_f32 v[80:81], v[2:3], v[134:135], v[80:81] op_sel_hi:[0,1,1] neg_lo:[1,0,0] neg_hi:[1,0,0]
	v_mov_b32_e32 v134, v55
	v_mov_b32_e32 v135, v7
	v_pk_fma_f32 v[82:83], v[2:3], v[134:135], v[82:83] op_sel_hi:[0,1,1] neg_lo:[1,0,0] neg_hi:[1,0,0]
	v_mul_f32_e32 v2, v136, v210
	v_mov_b32_e32 v134, v40
	v_mov_b32_e32 v135, v24
	s_waitcnt vmcnt(8)
	v_pk_fma_f32 v[84:85], v[2:3], v[134:135], v[84:85] op_sel_hi:[0,1,1] neg_lo:[1,0,0] neg_hi:[1,0,0]
	v_mov_b32_e32 v134, v56
	v_mov_b32_e32 v135, v8
	v_pk_fma_f32 v[86:87], v[2:3], v[134:135], v[86:87] op_sel_hi:[0,1,1] neg_lo:[1,0,0] neg_hi:[1,0,0]
	v_mul_f32_e32 v2, v136, v212
	v_mov_b32_e32 v134, v41
	v_mov_b32_e32 v135, v25
	v_pk_fma_f32 v[88:89], v[2:3], v[134:135], v[88:89] op_sel_hi:[0,1,1] neg_lo:[1,0,0] neg_hi:[1,0,0]
	v_mov_b32_e32 v134, v57
	v_mov_b32_e32 v135, v9
	v_pk_fma_f32 v[90:91], v[2:3], v[134:135], v[90:91] op_sel_hi:[0,1,1] neg_lo:[1,0,0] neg_hi:[1,0,0]
	v_mul_f32_e32 v2, v136, v214
	v_mov_b32_e32 v134, v42
	v_mov_b32_e32 v135, v26
	v_pk_fma_f32 v[92:93], v[2:3], v[134:135], v[92:93] op_sel_hi:[0,1,1] neg_lo:[1,0,0] neg_hi:[1,0,0]
	v_mov_b32_e32 v134, v58
	v_mov_b32_e32 v135, v10
	v_pk_fma_f32 v[94:95], v[2:3], v[134:135], v[94:95] op_sel_hi:[0,1,1] neg_lo:[1,0,0] neg_hi:[1,0,0]
	v_mul_f32_e32 v2, v136, v216
	v_mov_b32_e32 v134, v43
	v_mov_b32_e32 v135, v27
	v_pk_fma_f32 v[96:97], v[2:3], v[134:135], v[96:97] op_sel_hi:[0,1,1] neg_lo:[1,0,0] neg_hi:[1,0,0]
	v_mov_b32_e32 v134, v59
	v_mov_b32_e32 v135, v11
	v_pk_fma_f32 v[98:99], v[2:3], v[134:135], v[98:99] op_sel_hi:[0,1,1] neg_lo:[1,0,0] neg_hi:[1,0,0]
	v_mul_f32_e32 v2, v136, v218
	v_mov_b32_e32 v134, v44
	v_mov_b32_e32 v135, v28
	s_waitcnt vmcnt(4)
	v_pk_fma_f32 v[100:101], v[2:3], v[134:135], v[100:101] op_sel_hi:[0,1,1] neg_lo:[1,0,0] neg_hi:[1,0,0]
	v_mov_b32_e32 v134, v60
	v_mov_b32_e32 v135, v12
	v_pk_fma_f32 v[102:103], v[2:3], v[134:135], v[102:103] op_sel_hi:[0,1,1] neg_lo:[1,0,0] neg_hi:[1,0,0]
	v_mul_f32_e32 v2, v136, v220
	v_mov_b32_e32 v134, v45
	v_mov_b32_e32 v135, v29
	v_pk_fma_f32 v[104:105], v[2:3], v[134:135], v[104:105] op_sel_hi:[0,1,1] neg_lo:[1,0,0] neg_hi:[1,0,0]
	v_mov_b32_e32 v134, v61
	v_mov_b32_e32 v135, v13
	v_pk_fma_f32 v[106:107], v[2:3], v[134:135], v[106:107] op_sel_hi:[0,1,1] neg_lo:[1,0,0] neg_hi:[1,0,0]
	v_mul_f32_e32 v2, v136, v222
	v_mov_b32_e32 v134, v46
	v_mov_b32_e32 v135, v30
	v_pk_fma_f32 v[108:109], v[2:3], v[134:135], v[108:109] op_sel_hi:[0,1,1] neg_lo:[1,0,0] neg_hi:[1,0,0]
	v_mov_b32_e32 v134, v62
	v_mov_b32_e32 v135, v14
	v_pk_fma_f32 v[110:111], v[2:3], v[134:135], v[110:111] op_sel_hi:[0,1,1] neg_lo:[1,0,0] neg_hi:[1,0,0]
	v_mul_f32_e32 v2, v136, v224
	v_mov_b32_e32 v134, v47
	v_mov_b32_e32 v135, v31
	v_pk_fma_f32 v[112:113], v[2:3], v[134:135], v[112:113] op_sel_hi:[0,1,1] neg_lo:[1,0,0] neg_hi:[1,0,0]
	v_mov_b32_e32 v134, v63
	v_mov_b32_e32 v135, v15
	v_pk_fma_f32 v[114:115], v[2:3], v[134:135], v[114:115] op_sel_hi:[0,1,1] neg_lo:[1,0,0] neg_hi:[1,0,0]
	v_mul_f32_e32 v2, v136, v226
	v_mov_b32_e32 v134, v48
	v_mov_b32_e32 v135, v32
	s_waitcnt vmcnt(0)
	v_pk_fma_f32 v[116:117], v[2:3], v[134:135], v[116:117] op_sel_hi:[0,1,1] neg_lo:[1,0,0] neg_hi:[1,0,0]
	v_mov_b32_e32 v134, v64
	v_mov_b32_e32 v135, v16
	v_pk_fma_f32 v[118:119], v[2:3], v[134:135], v[118:119] op_sel_hi:[0,1,1] neg_lo:[1,0,0] neg_hi:[1,0,0]
	v_mul_f32_e32 v2, v136, v228
	v_mov_b32_e32 v134, v49
	v_mov_b32_e32 v135, v33
	v_pk_fma_f32 v[120:121], v[2:3], v[134:135], v[120:121] op_sel_hi:[0,1,1] neg_lo:[1,0,0] neg_hi:[1,0,0]
	v_mov_b32_e32 v134, v65
	v_mov_b32_e32 v135, v17
	v_pk_fma_f32 v[122:123], v[2:3], v[134:135], v[122:123] op_sel_hi:[0,1,1] neg_lo:[1,0,0] neg_hi:[1,0,0]
	v_mul_f32_e32 v2, v136, v230
	v_mov_b32_e32 v134, v50
	v_mov_b32_e32 v135, v34
	v_pk_fma_f32 v[124:125], v[2:3], v[134:135], v[124:125] op_sel_hi:[0,1,1] neg_lo:[1,0,0] neg_hi:[1,0,0]
	v_mov_b32_e32 v134, v66
	v_mov_b32_e32 v135, v18
	v_pk_fma_f32 v[126:127], v[2:3], v[134:135], v[126:127] op_sel_hi:[0,1,1] neg_lo:[1,0,0] neg_hi:[1,0,0]
	v_mul_f32_e32 v2, v136, v232
	v_mov_b32_e32 v134, v51
	v_mov_b32_e32 v135, v35
	v_pk_fma_f32 v[128:129], v[2:3], v[134:135], v[128:129] op_sel_hi:[0,1,1] neg_lo:[1,0,0] neg_hi:[1,0,0]
	v_mov_b32_e32 v134, v67
	v_mov_b32_e32 v135, v19
	v_pk_fma_f32 v[130:131], v[2:3], v[134:135], v[130:131] op_sel_hi:[0,1,1] neg_lo:[1,0,0] neg_hi:[1,0,0]
	s_cbranch_vccz .LBB0_1112
; #define INP(k) launder_p(args.in[k])
; __global__ void __launch_bounds__(NWAVES * 64, 2) mega_fwd(Args args) {
;     ...
;                             } else { const float* subg = INP(10) + l * 256;
;                                 asm volatile("s_waitcnt vmcnt(0)" ::: "memory");
;                                 float sg[8];
; #pragma unroll
;                                 for (int i = 0; i < 8; ++i) sg[i] = subg[(i >> 2) * 128 + (i & 3) * 32 + r32];
;                                 { f32x4 t[16];
; #pragma unroll
;                                   for (int r = 0; r < 16; ++r) t[r] = *(const f32x4*)(sq + r * 4);
;                                   asm volatile("" ::: "memory");
; #pragma unroll
;                                   for (int r = 0; r < 16; ++r) { float ssq = 0.f;
; #pragma unroll
;                                       for (int d0 = 0; d0 < 4; ++d0) ssq += t[r][d0] * t[r][d0] + o[d0][r] * o[d0][r];
; #pragma unroll
;                                       for (int off = 1; off < 32; off <<= 1) ssq += __shfl_xor(ssq, off);
;                                       rli[r] = __builtin_amdgcn_rsqf(ssq * (1.0f / 256.0f) + RMS_EPS) * (1.0f - lam_init); } }
	v_readlane_b32 s8, v252, 35
	v_readlane_b32 s12, v252, 39
	v_readlane_b32 s13, v252, 40
	s_mov_b64 s[0:1], s[12:13]
	v_readlane_b32 s6, v254, 41
	v_and_b32_e32 v2, 31, v238
	v_readlane_b32 s7, v254, 42
	s_add_u32 s0, s0, s6
	s_addc_u32 s1, s1, s7
	s_waitcnt vmcnt(0)
	v_lshlrev_b32_e32 v132, 2, v2
	global_load_dword v245, v132, s[0:1]
	global_load_dword v244, v132, s[0:1] offset:128
	global_load_dword v239, v132, s[0:1] offset:256
	global_load_dword v217, v132, s[0:1] offset:384
	global_load_dword v213, v132, s[0:1] offset:512
	global_load_dword v211, v132, s[0:1] offset:640
	global_load_dword v209, v132, s[0:1] offset:768
	global_load_dword v197, v132, s[0:1] offset:896
	global_load_dwordx4 v[180:183], v[236:237], off offset:-1024
	global_load_dwordx4 v[184:187], v[236:237], off offset:-2048
	global_load_dwordx4 v[188:191], v[236:237], off offset:-3072
	global_load_dwordx4 v[192:195], v[236:237], off offset:-4096
	global_load_dwordx4 v[164:167], v[236:237], off offset:3072
	global_load_dwordx4 v[168:171], v[236:237], off offset:2048
	global_load_dwordx4 v[172:175], v[236:237], off offset:1024
	global_load_dwordx4 v[176:179], v[236:237], off
	s_mov_b64 s[100:101], 0x2000
	v_lshl_add_u64 v[236:237], v[236:237], 0, s[100:101]
	global_load_dwordx4 v[148:151], v[236:237], off offset:-1024
	global_load_dwordx4 v[152:155], v[236:237], off offset:-2048
	global_load_dwordx4 v[156:159], v[236:237], off offset:-3072
	global_load_dwordx4 v[160:163], v[236:237], off offset:-4096
	global_load_dwordx4 v[132:135], v[236:237], off offset:3072
	global_load_dwordx4 v[136:139], v[236:237], off offset:2048
	global_load_dwordx4 v[140:143], v[236:237], off offset:1024
	global_load_dwordx4 v[144:147], v[236:237], off
	s_mov_b32 s100, 0xffffe000
	s_mov_b32 s101, -1
	v_lshl_add_u64 v[236:237], v[236:237], 0, s[100:101]
	v_pk_mul_f32 v[250:251], v[68:69], v[68:69]
	v_readlane_b32 s11, v252, 38
	v_readlane_b32 s0, v254, 48
	v_readlane_b32 s11, v254, 24
	s_mov_b32 s8, 0xe800
	v_readlane_b32 s10, v252, 37
	s_mov_b64 s[12:13], 0x3800
	s_movk_i32 s10, 0x3000
	v_lshlrev_b32_e32 v2, 1, v2
	v_readlane_b32 s9, v252, 36
	v_readlane_b32 s14, v252, 41
	v_readlane_b32 s15, v252, 42
	v_readlane_b32 s16, v252, 43
	v_readlane_b32 s17, v252, 44
	v_readlane_b32 s18, v252, 45
	v_readlane_b32 s19, v252, 46
	v_readlane_b32 s20, v252, 47
	v_readlane_b32 s21, v252, 48
	v_readlane_b32 s22, v252, 49
	v_readlane_b32 s23, v252, 50
	v_lshrrev_b32_e32 v4, 2, v238
	v_lshl_add_u32 v5, s11, 5, v4
	v_add_u32_e32 v5, s0, v5
	v_readlane_b32 s100, v253, 48
	v_readlane_b32 s101, v253, 49
	v_and_b32_e32 v8, 3, v238
	v_lshlrev_b32_e32 v8, 7, v8
	v_mov_b32_e32 v9, 0
	v_mov_b64_e32 v[6:7], s[100:101]
	s_nop 0
	v_mad_i64_i32 v[6:7], s[100:101], v5, s8, v[6:7]
	v_lshl_add_u64 v[6:7], v[6:7], 0, v[8:9]
	v_readlane_b32 s100, v254, 49
	v_lshl_add_u64 v[6:7], v[6:7], 0, s[12:13]
	s_nop 1
	v_mov_b32_e32 v8, s100
	v_lshlrev_b32_e32 v8, 1, v8
	v_lshl_add_u64 v[6:7], v[6:7], 0, v[8:9]
	global_load_dword v10, v[6:7], off
	s_mov_b64 s[100:101], 0xe8000
	v_lshl_add_u64 v[6:7], v[6:7], 0, s[100:101]
	global_load_dword v11, v[6:7], off
	s_waitcnt vmcnt(14)
	v_fma_f32 v192, v192, v192, v250
	v_fmac_f32_e32 v251, v193, v193
	v_add_f32_e32 v215, v192, v251
	v_pk_mul_f32 v[192:193], v[70:71], v[70:71]
	s_nop 0
	v_fma_f32 v192, v194, v194, v192
	v_add_f32_e32 v192, v215, v192
	v_fmac_f32_e32 v193, v195, v195
	v_add_f32_e32 v192, v192, v193
	ds_bpermute_b32 v193, v1, v192
	s_waitcnt lgkmcnt(0)
	v_add_f32_e32 v192, v192, v193
	ds_bpermute_b32 v193, v246, v192
	s_waitcnt lgkmcnt(0)
	v_add_f32_e32 v192, v192, v193
	ds_bpermute_b32 v193, v247, v192
	s_waitcnt lgkmcnt(0)
	v_add_f32_e32 v192, v192, v193
	ds_bpermute_b32 v193, v248, v192
	s_waitcnt lgkmcnt(0)
	v_add_f32_e32 v192, v192, v193
	ds_bpermute_b32 v193, v249, v192
	s_waitcnt lgkmcnt(0)
	v_add_f32_e32 v192, v192, v193
	v_fmamk_f32 v192, v192, 0x3b800000, v221
	v_rsq_f32_e32 v192, v192
	s_nop 0
	v_mul_f32_e32 v215, v205, v192
	v_pk_mul_f32 v[192:193], v[72:73], v[72:73]
	s_nop 0
	v_fma_f32 v188, v188, v188, v192
	v_fmac_f32_e32 v193, v189, v189
	v_add_f32_e32 v192, v188, v193
	v_pk_mul_f32 v[188:189], v[74:75], v[74:75]
	s_nop 0
	v_fma_f32 v188, v190, v190, v188
	v_add_f32_e32 v188, v192, v188
	v_fmac_f32_e32 v189, v191, v191
	v_add_f32_e32 v188, v188, v189
	ds_bpermute_b32 v189, v1, v188
	s_waitcnt lgkmcnt(0)
	v_add_f32_e32 v188, v188, v189
	ds_bpermute_b32 v189, v246, v188
	s_waitcnt lgkmcnt(0)
	v_add_f32_e32 v188, v188, v189
	ds_bpermute_b32 v189, v247, v188
	s_waitcnt lgkmcnt(0)
	v_add_f32_e32 v188, v188, v189
	ds_bpermute_b32 v189, v248, v188
	s_waitcnt lgkmcnt(0)
	v_add_f32_e32 v251, v188, v189
	v_pk_mul_f32 v[188:189], v[76:77], v[76:77]
	ds_bpermute_b32 v223, v249, v251
	v_fma_f32 v184, v184, v184, v188
	v_fmac_f32_e32 v189, v185, v185
	v_add_f32_e32 v188, v184, v189
	v_pk_mul_f32 v[184:185], v[78:79], v[78:79]
	s_nop 0
	v_fma_f32 v184, v186, v186, v184
	v_add_f32_e32 v184, v188, v184
	v_fmac_f32_e32 v185, v187, v187
	v_add_f32_e32 v184, v184, v185
	ds_bpermute_b32 v185, v1, v184
	s_waitcnt lgkmcnt(0)
	v_add_f32_e32 v184, v184, v185
	ds_bpermute_b32 v185, v246, v184
	s_waitcnt lgkmcnt(0)
	v_add_f32_e32 v184, v184, v185
	ds_bpermute_b32 v185, v247, v184
	s_waitcnt lgkmcnt(0)
	v_add_f32_e32 v184, v184, v185
	ds_bpermute_b32 v185, v248, v184
	s_waitcnt lgkmcnt(0)
	v_add_f32_e32 v189, v184, v185
	v_pk_mul_f32 v[184:185], v[80:81], v[80:81]
	ds_bpermute_b32 v191, v249, v189
	v_fma_f32 v180, v180, v180, v184
	v_fmac_f32_e32 v185, v181, v181
	v_add_f32_e32 v184, v180, v185
	v_pk_mul_f32 v[180:181], v[82:83], v[82:83]
	s_nop 0
	v_fma_f32 v180, v182, v182, v180
	v_add_f32_e32 v180, v184, v180
	v_fmac_f32_e32 v181, v183, v183
	v_add_f32_e32 v180, v180, v181
	ds_bpermute_b32 v181, v1, v180
	s_waitcnt lgkmcnt(0)
; __global__ void __launch_bounds__(NWAVES * 64, 2) mega_fwd(Args args) {
;     ...
;                                   for (int r = 0; r < 16; ++r) { float ssq = 0.f;
; #pragma unroll
;                                       for (int d0 = 0; d0 < 4; ++d0) ssq += t[r][d0] * t[r][d0] + o[d0][r] * o[d0][r];
; #pragma unroll
;                                       for (int off = 1; off < 32; off <<= 1) ssq += __shfl_xor(ssq, off);
;                                       rli[r] = __builtin_amdgcn_rsqf(ssq * (1.0f / 256.0f) + RMS_EPS) * (1.0f - lam_init); } }
	v_add_f32_e32 v180, v180, v181
	ds_bpermute_b32 v181, v246, v180
	s_waitcnt lgkmcnt(0)
	v_add_f32_e32 v180, v180, v181
	ds_bpermute_b32 v181, v247, v180
	s_waitcnt lgkmcnt(0)
	v_add_f32_e32 v180, v180, v181
	ds_bpermute_b32 v181, v248, v180
	s_waitcnt lgkmcnt(0)
	v_add_f32_e32 v187, v180, v181
	v_pk_mul_f32 v[180:181], v[84:85], v[84:85]
	ds_bpermute_b32 v188, v249, v187
	s_waitcnt vmcnt(10)
	v_fma_f32 v176, v176, v176, v180
	v_fmac_f32_e32 v181, v177, v177
	v_add_f32_e32 v180, v176, v181
	v_pk_mul_f32 v[176:177], v[86:87], v[86:87]
	s_nop 0
	v_fma_f32 v176, v178, v178, v176
	v_add_f32_e32 v176, v180, v176
	v_fmac_f32_e32 v177, v179, v179
	v_add_f32_e32 v176, v176, v177
	ds_bpermute_b32 v177, v1, v176
	v_pk_mul_f32 v[178:179], v[88:89], v[88:89]
	s_waitcnt lgkmcnt(0)
	v_add_f32_e32 v176, v176, v177
	ds_bpermute_b32 v177, v246, v176
	v_fma_f32 v172, v172, v172, v178
	v_fmac_f32_e32 v179, v173, v173
	s_waitcnt lgkmcnt(0)
	v_add_f32_e32 v176, v176, v177
	ds_bpermute_b32 v177, v247, v176
	s_waitcnt lgkmcnt(0)
	v_add_f32_e32 v176, v176, v177
	ds_bpermute_b32 v177, v248, v176
	s_waitcnt lgkmcnt(0)
	v_add_f32_e32 v176, v176, v177
	v_add_f32_e32 v177, v172, v179
	v_pk_mul_f32 v[172:173], v[90:91], v[90:91]
	ds_bpermute_b32 v186, v249, v176
	v_fma_f32 v172, v174, v174, v172
	v_add_f32_e32 v172, v177, v172
	v_fmac_f32_e32 v173, v175, v175
	v_add_f32_e32 v172, v172, v173
	ds_bpermute_b32 v173, v1, v172
	v_pk_mul_f32 v[174:175], v[92:93], v[92:93]
	s_waitcnt lgkmcnt(0)
	v_add_f32_e32 v172, v172, v173
	ds_bpermute_b32 v173, v246, v172
	v_fma_f32 v168, v168, v168, v174
	v_fmac_f32_e32 v175, v169, v169
	s_waitcnt lgkmcnt(0)
	v_add_f32_e32 v172, v172, v173
	ds_bpermute_b32 v173, v247, v172
	s_waitcnt lgkmcnt(0)
	v_add_f32_e32 v172, v172, v173
	ds_bpermute_b32 v173, v248, v172
	s_waitcnt lgkmcnt(0)
	v_add_f32_e32 v173, v172, v173
	v_add_f32_e32 v172, v168, v175
	v_pk_mul_f32 v[168:169], v[94:95], v[94:95]
	ds_bpermute_b32 v250, v249, v173
	v_fma_f32 v168, v170, v170, v168
	v_add_f32_e32 v168, v172, v168
	v_fmac_f32_e32 v169, v171, v171
	v_add_f32_e32 v168, v168, v169
	ds_bpermute_b32 v169, v1, v168
	s_waitcnt lgkmcnt(0)
	v_add_f32_e32 v168, v168, v169
	ds_bpermute_b32 v169, v246, v168
	s_waitcnt lgkmcnt(0)
	v_add_f32_e32 v168, v168, v169
	ds_bpermute_b32 v169, v247, v168
	s_waitcnt lgkmcnt(0)
	v_add_f32_e32 v168, v168, v169
	ds_bpermute_b32 v169, v248, v168
	s_waitcnt lgkmcnt(0)
	v_add_f32_e32 v174, v168, v169
	v_pk_mul_f32 v[168:169], v[96:97], v[96:97]
	ds_bpermute_b32 v190, v249, v174
	v_fma_f32 v164, v164, v164, v168
	v_fmac_f32_e32 v169, v165, v165
	v_add_f32_e32 v168, v164, v169
	v_pk_mul_f32 v[164:165], v[98:99], v[98:99]
	s_nop 0
	v_fma_f32 v164, v166, v166, v164
	v_add_f32_e32 v164, v168, v164
	v_fmac_f32_e32 v165, v167, v167
	v_add_f32_e32 v164, v164, v165
	ds_bpermute_b32 v165, v1, v164
	s_waitcnt lgkmcnt(0)
	v_add_f32_e32 v164, v164, v165
	ds_bpermute_b32 v165, v246, v164
	s_waitcnt lgkmcnt(0)
	v_add_f32_e32 v164, v164, v165
	ds_bpermute_b32 v165, v247, v164
	s_waitcnt lgkmcnt(0)
	v_add_f32_e32 v164, v164, v165
	ds_bpermute_b32 v165, v248, v164
	s_waitcnt lgkmcnt(0)
	v_add_f32_e32 v175, v164, v165
	v_pk_mul_f32 v[164:165], v[100:101], v[100:101]
	ds_bpermute_b32 v185, v249, v175
	s_waitcnt vmcnt(6)
	v_fma_f32 v160, v160, v160, v164
	v_fmac_f32_e32 v165, v161, v161
	v_add_f32_e32 v164, v160, v165
	v_pk_mul_f32 v[160:161], v[102:103], v[102:103]
	s_nop 0
	v_fma_f32 v160, v162, v162, v160
	v_add_f32_e32 v160, v164, v160
	v_fmac_f32_e32 v161, v163, v163
	v_add_f32_e32 v160, v160, v161
	ds_bpermute_b32 v161, v1, v160
	s_waitcnt lgkmcnt(0)
	v_add_f32_e32 v160, v160, v161
	ds_bpermute_b32 v161, v246, v160
	s_waitcnt lgkmcnt(0)
	v_add_f32_e32 v160, v160, v161
	ds_bpermute_b32 v161, v247, v160
	s_waitcnt lgkmcnt(0)
	v_add_f32_e32 v160, v160, v161
	ds_bpermute_b32 v161, v248, v160
	s_waitcnt lgkmcnt(0)
	v_add_f32_e32 v168, v160, v161
	v_pk_mul_f32 v[160:161], v[104:105], v[104:105]
	ds_bpermute_b32 v180, v249, v168
	v_fma_f32 v156, v156, v156, v160
	v_fmac_f32_e32 v161, v157, v157
	v_add_f32_e32 v160, v156, v161
	v_pk_mul_f32 v[156:157], v[106:107], v[106:107]
	s_nop 0
	v_fma_f32 v156, v158, v158, v156
	v_add_f32_e32 v156, v160, v156
	v_fmac_f32_e32 v157, v159, v159
	v_add_f32_e32 v156, v156, v157
	ds_bpermute_b32 v157, v1, v156
	s_waitcnt lgkmcnt(0)
	v_add_f32_e32 v156, v156, v157
	ds_bpermute_b32 v157, v246, v156
	s_waitcnt lgkmcnt(0)
	v_add_f32_e32 v156, v156, v157
	ds_bpermute_b32 v157, v247, v156
	s_waitcnt lgkmcnt(0)
	v_add_f32_e32 v156, v156, v157
	ds_bpermute_b32 v157, v248, v156
	s_waitcnt lgkmcnt(0)
	v_add_f32_e32 v177, v156, v157
	v_pk_mul_f32 v[156:157], v[108:109], v[108:109]
	ds_bpermute_b32 v184, v249, v177
	v_fma_f32 v152, v152, v152, v156
	v_fmac_f32_e32 v157, v153, v153
	v_add_f32_e32 v156, v152, v157
	v_pk_mul_f32 v[152:153], v[110:111], v[110:111]
	s_nop 0
	v_fma_f32 v152, v154, v154, v152
	v_add_f32_e32 v152, v156, v152
	v_fmac_f32_e32 v153, v155, v155
	v_add_f32_e32 v152, v152, v153
	ds_bpermute_b32 v153, v1, v152
	s_waitcnt lgkmcnt(0)
	v_add_f32_e32 v152, v152, v153
	ds_bpermute_b32 v153, v246, v152
	s_waitcnt lgkmcnt(0)
	v_add_f32_e32 v152, v152, v153
	ds_bpermute_b32 v153, v247, v152
	s_waitcnt lgkmcnt(0)
	v_add_f32_e32 v152, v152, v153
	ds_bpermute_b32 v153, v248, v152
	s_waitcnt lgkmcnt(0)
	v_add_f32_e32 v178, v152, v153
	v_pk_mul_f32 v[152:153], v[112:113], v[112:113]
	ds_bpermute_b32 v183, v249, v178
	v_fma_f32 v148, v148, v148, v152
	v_fmac_f32_e32 v153, v149, v149
	v_add_f32_e32 v152, v148, v153
	v_pk_mul_f32 v[148:149], v[114:115], v[114:115]
	s_nop 0
	v_fma_f32 v148, v150, v150, v148
	v_add_f32_e32 v148, v152, v148
	v_fmac_f32_e32 v149, v151, v151
	v_add_f32_e32 v148, v148, v149
	ds_bpermute_b32 v149, v1, v148
	s_waitcnt lgkmcnt(0)
; __device__ __forceinline__ float bflo(unsigned w) { return __uint_as_float(w << 16); }
; __device__ __forceinline__ float bfhi(unsigned w) { return __uint_as_float(w & 0xffff0000u); }
; __device__ __forceinline__ unsigned pk2(float lo, float hi) { return f2bf(lo) | (f2bf(hi) << 16); }
; __device__ __forceinline__ int crow(int r, int hi) { return (r & 3) + 8 * (r >> 2) + 4 * hi; }
; __global__ void __launch_bounds__(NWAVES * 64, 2) mega_fwd(Args args) {
;     ...
;                                   for (int r = 0; r < 16; ++r) { float ssq = 0.f;
; #pragma unroll
;                                       for (int d0 = 0; d0 < 4; ++d0) ssq += t[r][d0] * t[r][d0] + o[d0][r] * o[d0][r];
; #pragma unroll
;                                       for (int off = 1; off < 32; off <<= 1) ssq += __shfl_xor(ssq, off);
;                                       rli[r] = __builtin_amdgcn_rsqf(ssq * (1.0f / 256.0f) + RMS_EPS) * (1.0f - lam_init); } }
; #pragma unroll
;                                 for (int hv = 0; hv < 2; ++hv)
; #pragma unroll
;                                   for (int rq = 0; rq < 4; ++rq) { unsigned zz[16]; f32x4 t[4];
;                                     int wv_ = wave; asm volatile("" : "+s"(wv_));
; #pragma unroll
;                                     for (int rr = 0; rr < 4; ++rr) { const int r = rq * 4 + rr; const bf16_t* zp = PROJ + (size_t)(b * SEQ + L * 256 + wv_ * 32 + att::crow(r, hi)) * NC + C_ZB + h * 256 + hv * 128 + (r32 & ~1);
; #pragma unroll
;                                         for (int d0 = 0; d0 < 4; ++d0) zz[rr * 4 + d0] = *(const unsigned*)(zp + d0 * 32);
;                                         if (hv == 0) t[rr] = *(const f32x4*)(sq + r * 4); else t[rr] = (f32x4){o[0][r], o[1][r], o[2][r], o[3][r]}; }
;                                     asm volatile("" ::: "memory");
; #pragma unroll
;                                     for (int rr = 0; rr < 4; ++rr) { const int r = rq * 4 + rr; bf16_t* yp = Y + (size_t)(b * SEQ + L * 256 + wv_ * 32 + att::crow(r, hi)) * YS + BW + h * 256 + hv * 128 + r32;
; #pragma unroll
;                                         for (int d0 = 0; d0 < 4; ++d0) { const float val = t[rr][d0] * rli[r] * sg[hv * 4 + d0], vn = __shfl_xor(val, 1);
;                                             if ((r32 & 1) == 0) *(unsigned*)(yp + d0 * 32) = pk2(val * bflo(zz[rr * 4 + d0]), vn * bfhi(zz[rr * 4 + d0])); } } }
	v_add_f32_e32 v148, v148, v149
	ds_bpermute_b32 v149, v246, v148
	s_waitcnt lgkmcnt(0)
	v_add_f32_e32 v148, v148, v149
	ds_bpermute_b32 v149, v247, v148
	s_waitcnt lgkmcnt(0)
	v_add_f32_e32 v148, v148, v149
	ds_bpermute_b32 v149, v248, v148
	s_waitcnt lgkmcnt(0)
	v_add_f32_e32 v179, v148, v149
	v_pk_mul_f32 v[148:149], v[116:117], v[116:117]
	ds_bpermute_b32 v182, v249, v179
	s_waitcnt vmcnt(2)
	v_fma_f32 v144, v144, v144, v148
	v_fmac_f32_e32 v149, v145, v145
	v_add_f32_e32 v148, v144, v149
	v_pk_mul_f32 v[144:145], v[118:119], v[118:119]
	v_mov_b32_e32 v149, v3
	v_fma_f32 v144, v146, v146, v144
	v_add_f32_e32 v144, v148, v144
	v_fmac_f32_e32 v145, v147, v147
	v_add_f32_e32 v144, v144, v145
	ds_bpermute_b32 v145, v1, v144
	s_waitcnt lgkmcnt(0)
	v_add_f32_e32 v144, v144, v145
	ds_bpermute_b32 v145, v246, v144
	s_waitcnt lgkmcnt(0)
	v_add_f32_e32 v144, v144, v145
	ds_bpermute_b32 v145, v247, v144
	s_waitcnt lgkmcnt(0)
	v_add_f32_e32 v144, v144, v145
	ds_bpermute_b32 v145, v248, v144
	s_waitcnt lgkmcnt(0)
	v_add_f32_e32 v172, v144, v145
	v_pk_mul_f32 v[144:145], v[120:121], v[120:121]
	ds_bpermute_b32 v181, v249, v172
	v_fma_f32 v140, v140, v140, v144
	v_fmac_f32_e32 v145, v141, v141
	v_add_f32_e32 v144, v140, v145
	v_pk_mul_f32 v[140:141], v[122:123], v[122:123]
	s_nop 0
	v_fma_f32 v140, v142, v142, v140
	v_add_f32_e32 v140, v144, v140
	v_fmac_f32_e32 v141, v143, v143
	v_add_f32_e32 v140, v140, v141
	ds_bpermute_b32 v141, v1, v140
	s_waitcnt lgkmcnt(0)
	v_add_f32_e32 v140, v140, v141
	ds_bpermute_b32 v141, v246, v140
	s_waitcnt lgkmcnt(0)
	v_add_f32_e32 v140, v140, v141
	ds_bpermute_b32 v141, v247, v140
	s_waitcnt lgkmcnt(0)
	v_add_f32_e32 v140, v140, v141
	ds_bpermute_b32 v141, v248, v140
	s_waitcnt lgkmcnt(0)
	v_add_f32_e32 v166, v140, v141
	v_pk_mul_f32 v[140:141], v[124:125], v[124:125]
	ds_bpermute_b32 v167, v249, v166
	v_fma_f32 v136, v136, v136, v140
	v_fmac_f32_e32 v141, v137, v137
	v_add_f32_e32 v140, v136, v141
	v_pk_mul_f32 v[136:137], v[126:127], v[126:127]
	s_nop 0
	v_fma_f32 v136, v138, v138, v136
	v_add_f32_e32 v136, v140, v136
	v_fmac_f32_e32 v137, v139, v139
	v_add_f32_e32 v136, v136, v137
	ds_bpermute_b32 v137, v1, v136
	s_waitcnt lgkmcnt(0)
	v_add_f32_e32 v136, v136, v137
	ds_bpermute_b32 v137, v246, v136
	s_waitcnt lgkmcnt(0)
	v_add_f32_e32 v136, v136, v137
	ds_bpermute_b32 v137, v247, v136
	s_waitcnt lgkmcnt(0)
	v_add_f32_e32 v136, v136, v137
	ds_bpermute_b32 v137, v248, v136
	s_waitcnt lgkmcnt(0)
	v_add_f32_e32 v163, v136, v137
	v_pk_mul_f32 v[136:137], v[128:129], v[128:129]
	ds_bpermute_b32 v164, v249, v163
	v_fma_f32 v132, v132, v132, v136
	v_fmac_f32_e32 v137, v133, v133
	v_add_f32_e32 v136, v132, v137
	v_pk_mul_f32 v[132:133], v[130:131], v[130:131]
	s_nop 0
	v_fma_f32 v132, v134, v134, v132
	v_add_f32_e32 v132, v136, v132
	v_fmac_f32_e32 v133, v135, v135
	v_add_f32_e32 v132, v132, v133
	ds_bpermute_b32 v133, v1, v132
	v_and_b32_e32 v134, 30, v238
	v_lshlrev_b32_e32 v148, 1, v134
	s_waitcnt lgkmcnt(0)
	v_add_f32_e32 v132, v132, v133
	ds_bpermute_b32 v133, v246, v132
	s_waitcnt lgkmcnt(0)
	v_add_f32_e32 v132, v132, v133
	ds_bpermute_b32 v133, v247, v132
	s_waitcnt lgkmcnt(0)
	v_add_f32_e32 v132, v132, v133
	ds_bpermute_b32 v133, v248, v132
	s_waitcnt lgkmcnt(0)
	v_add_f32_e32 v160, v132, v133
	v_ashrrev_i32_e32 v132, 3, v238
	v_and_b32_e32 v132, -4, v132
	v_add_u32_e32 v162, s0, v132
	s_mov_b32 s0, s11
	v_and_b32_e32 v132, 1, v238
	v_lshl_add_u32 v156, s0, 5, v162
	v_readlane_b32 s0, v253, 48
	v_readlane_b32 s1, v253, 49
	v_cmp_eq_u32_e64 s[6:7], 0, v132
	v_or_b32_e32 v154, 1, v156
	v_mov_b64_e32 v[158:159], s[0:1]
	v_mad_i64_i32 v[132:133], s[0:1], v156, s8, v[158:159]
	v_readlane_b32 s0, v254, 49
	s_lshl_b32 s2, s0, 1
	v_lshl_add_u64 v[132:133], v[132:133], 0, s[2:3]
	v_lshl_add_u64 v[132:133], v[132:133], 0, v[148:149]
	v_mad_i64_i32 v[150:151], s[0:1], v154, s8, v[158:159]
	v_lshl_add_u64 v[134:135], v[132:133], 0, s[12:13]
	v_add_co_u32_e32 v132, vcc, s10, v132
	v_lshl_add_u64 v[150:151], v[150:151], 0, s[2:3]
	s_nop 0
	v_addc_co_u32_e32 v133, vcc, 0, v133, vcc
	v_lshl_add_u64 v[150:151], v[150:151], 0, v[148:149]
	v_lshl_add_u64 v[152:153], v[150:151], 0, s[12:13]
	v_add_co_u32_e32 v150, vcc, s10, v150
	ds_bpermute_b32 v161, v249, v160
	s_nop 0
	v_addc_co_u32_e32 v151, vcc, 0, v151, vcc
	global_load_dword v192, v[132:133], off offset:2048 nt
	global_load_dword v233, v[134:135], off offset:64 nt
	global_load_dword v169, v[134:135], off offset:128 nt
	global_load_dword v155, v[134:135], off offset:192 nt
	s_nop 0
	global_load_dwordx4 v[132:135], v[236:237], off offset:-1024
	global_load_dwordx4 v[136:139], v[236:237], off offset:-2048
	global_load_dwordx4 v[140:143], v[236:237], off offset:-3072
	global_load_dwordx4 v[144:147], v[236:237], off offset:-4096
	global_load_dword v240, v[150:151], off offset:2048 nt
	global_load_dword v249, v[152:153], off offset:64 nt
	global_load_dword v170, v[152:153], off offset:128 nt
	s_nop 0
	global_load_dword v153, v[152:153], off offset:192 nt
	v_or_b32_e32 v152, 2, v156
	v_mad_i64_i32 v[150:151], s[0:1], v152, s8, v[158:159]
	v_lshl_add_u64 v[150:151], v[150:151], 0, s[2:3]
	v_lshl_add_u64 v[150:151], v[150:151], 0, v[148:149]
	v_lshl_add_u64 v[194:195], v[150:151], 0, s[12:13]
	v_add_co_u32_e32 v150, vcc, s10, v150
	v_ashrrev_i32_e32 v157, 31, v156
	s_nop 0
	v_addc_co_u32_e32 v151, vcc, 0, v151, vcc
	global_load_dword v248, v[150:151], off offset:2048 nt
	global_load_dword v247, v[194:195], off offset:64 nt
	global_load_dword v171, v[194:195], off offset:128 nt
	s_nop 0
	global_load_dword v151, v[194:195], off offset:192 nt
	v_or_b32_e32 v150, 3, v156
	v_mad_i64_i32 v[158:159], s[0:1], v150, s8, v[158:159]
	v_lshl_add_u64 v[158:159], v[158:159], 0, s[2:3]
	v_lshl_add_u64 v[158:159], v[158:159], 0, v[148:149]
	v_lshl_add_u64 v[194:195], v[158:159], 0, s[12:13]
	v_add_co_u32_e32 v158, vcc, s10, v158
	v_lshlrev_b64 v[156:157], 13, v[156:157]
	s_nop 0
	v_addc_co_u32_e32 v159, vcc, 0, v159, vcc
	global_load_dword v246, v[158:159], off offset:2048 nt
	global_load_dword v238, v[194:195], off offset:64 nt
	global_load_dword v165, v[194:195], off offset:128 nt
	global_load_dword v149, v[194:195], off offset:192 nt
	v_lshl_add_u64 v[156:157], s[4:5], 0, v[156:157]
	v_lshl_add_u64 v[156:157], v[156:157], 0, v[2:3]
	s_waitcnt vmcnt(12)
	v_mul_f32_e32 v144, v215, v144
	v_mul_f32_e32 v159, v144, v245
	ds_bpermute_b32 v158, v1, v159
	s_and_saveexec_b64 s[0:1], s[6:7]
	s_cbranch_execz .LBB0_857
	v_lshlrev_b32_e32 v193, 16, v192
	v_and_b32_e32 v192, 0xffff0000, v192
	s_waitcnt lgkmcnt(0)
	v_pk_mul_f32 v[158:159], v[158:159], v[192:193]
	s_nop 0
	v_and_b32_sdwa v144, v159, v227 dst_sel:DWORD dst_unused:UNUSED_PAD src0_sel:WORD_1 src1_sel:DWORD
	v_and_b32_sdwa v192, v158, v227 dst_sel:DWORD dst_unused:UNUSED_PAD src0_sel:WORD_1 src1_sel:DWORD
	v_add3_u32 v144, v159, v144, s97
	v_add3_u32 v158, v158, v192, s97
	v_lshrrev_b32_e32 v144, 16, v144
	v_and_or_b32 v144, v158, s66, v144
	global_store_dword v[156:157], v144, off offset:2048

; __device__ __forceinline__ float bflo(unsigned w) { return __uint_as_float(w << 16); }
; __device__ __forceinline__ float bfhi(unsigned w) { return __uint_as_float(w & 0xffff0000u); }
; __device__ __forceinline__ unsigned pk2(float lo, float hi) { return f2bf(lo) | (f2bf(hi) << 16); }
; __device__ __forceinline__ int crow(int r, int hi) { return (r & 3) + 8 * (r >> 2) + 4 * hi; }
; __global__ void __launch_bounds__(NWAVES * 64, 2) mega_fwd(Args args) {
;     ...
;                                       rli[r] = __builtin_amdgcn_rsqf(ssq * (1.0f / 256.0f) + RMS_EPS) * (1.0f - lam_init); } }
; #pragma unroll
;                                 for (int hv = 0; hv < 2; ++hv)
; #pragma unroll
;                                   for (int rq = 0; rq < 4; ++rq) { unsigned zz[16]; f32x4 t[4];
;                                     int wv_ = wave; asm volatile("" : "+s"(wv_));
; #pragma unroll
;                                     for (int rr = 0; rr < 4; ++rr) { const int r = rq * 4 + rr; const bf16_t* zp = PROJ + (size_t)(b * SEQ + L * 256 + wv_ * 32 + att::crow(r, hi)) * NC + C_ZB + h * 256 + hv * 128 + (r32 & ~1);
; #pragma unroll
;                                         for (int d0 = 0; d0 < 4; ++d0) zz[rr * 4 + d0] = *(const unsigned*)(zp + d0 * 32);
;                                         if (hv == 0) t[rr] = *(const f32x4*)(sq + r * 4); else t[rr] = (f32x4){o[0][r], o[1][r], o[2][r], o[3][r]}; }
;                                     asm volatile("" ::: "memory");
; #pragma unroll
;                                     for (int rr = 0; rr < 4; ++rr) { const int r = rq * 4 + rr; bf16_t* yp = Y + (size_t)(b * SEQ + L * 256 + wv_ * 32 + att::crow(r, hi)) * YS + BW + h * 256 + hv * 128 + r32;
; #pragma unroll
;                                         for (int d0 = 0; d0 < 4; ++d0) { const float val = t[rr][d0] * rli[r] * sg[hv * 4 + d0], vn = __shfl_xor(val, 1);
;                                             if ((r32 & 1) == 0) *(unsigned*)(yp + d0 * 32) = pk2(val * bflo(zz[rr * 4 + d0]), vn * bfhi(zz[rr * 4 + d0])); } } }
.LBB0_887:
	s_or_b64 exec, exec, s[0:1]
	s_waitcnt lgkmcnt(0)
	v_add_f32_e32 v132, v176, v186
	v_fmamk_f32 v132, v132, 0x3b800000, v221
	s_mov_b32 s0, s11
	v_rsq_f32_e32 v132, v132
	v_add_u32_e32 v176, 8, v162
	v_lshl_add_u32 v156, s0, 5, v176
	v_readlane_b32 s0, v253, 48
	v_readlane_b32 s1, v253, 49
	s_waitcnt vmcnt(1)
	v_mul_f32_e32 v165, v205, v132
	s_waitcnt vmcnt(0)
	v_mov_b32_e32 v149, v3
	v_mov_b64_e32 v[158:159], s[0:1]
	v_mad_i64_i32 v[132:133], s[0:1], v156, s8, v[158:159]
	v_lshl_add_u64 v[132:133], v[132:133], 0, s[2:3]
	v_or_b32_e32 v154, 1, v156
	v_lshl_add_u64 v[132:133], v[132:133], 0, v[148:149]
	v_mad_i64_i32 v[150:151], s[0:1], v154, s8, v[158:159]
	v_lshl_add_u64 v[134:135], v[132:133], 0, s[12:13]
	v_add_co_u32_e32 v132, vcc, s10, v132
	v_lshl_add_u64 v[150:151], v[150:151], 0, s[2:3]
	s_nop 0
	v_addc_co_u32_e32 v133, vcc, 0, v133, vcc
	v_lshl_add_u64 v[150:151], v[150:151], 0, v[148:149]
	v_lshl_add_u64 v[152:153], v[150:151], 0, s[12:13]
	v_add_co_u32_e32 v150, vcc, s10, v150
	global_load_dword v246, v[132:133], off offset:2048 nt
	global_load_dword v240, v[134:135], off offset:64 nt
	global_load_dword v238, v[134:135], off offset:128 nt
	global_load_dword v155, v[134:135], off offset:192 nt
	s_nop 0
	global_load_dwordx4 v[132:135], v[236:237], off offset:3072
	global_load_dwordx4 v[136:139], v[236:237], off offset:2048
	global_load_dwordx4 v[140:143], v[236:237], off offset:1024
	global_load_dwordx4 v[144:147], v[236:237], off
	v_addc_co_u32_e32 v151, vcc, 0, v151, vcc
	global_load_dword v233, v[150:151], off offset:2048 nt
	global_load_dword v223, v[152:153], off offset:64 nt
	global_load_dword v193, v[152:153], off offset:128 nt
	s_nop 0
	global_load_dword v153, v[152:153], off offset:192 nt
	v_or_b32_e32 v152, 2, v156
	v_mad_i64_i32 v[150:151], s[0:1], v152, s8, v[158:159]
	v_lshl_add_u64 v[150:151], v[150:151], 0, s[2:3]
	v_lshl_add_u64 v[150:151], v[150:151], 0, v[148:149]
	v_lshl_add_u64 v[186:187], v[150:151], 0, s[12:13]
	v_add_co_u32_e32 v150, vcc, s10, v150
	v_ashrrev_i32_e32 v157, 31, v156
	s_nop 0
	v_addc_co_u32_e32 v151, vcc, 0, v151, vcc
	global_load_dword v192, v[150:151], off offset:2048 nt
	global_load_dword v191, v[186:187], off offset:64 nt
	global_load_dword v189, v[186:187], off offset:128 nt
	s_nop 0
	global_load_dword v151, v[186:187], off offset:192 nt
	v_or_b32_e32 v150, 3, v156
	v_mad_i64_i32 v[158:159], s[0:1], v150, s8, v[158:159]
	v_lshl_add_u64 v[158:159], v[158:159], 0, s[2:3]
	v_lshl_add_u64 v[158:159], v[158:159], 0, v[148:149]
	v_lshl_add_u64 v[194:195], v[158:159], 0, s[12:13]
	v_add_co_u32_e32 v158, vcc, s10, v158
	v_lshlrev_b64 v[156:157], 13, v[156:157]
	s_nop 0
	v_addc_co_u32_e32 v159, vcc, 0, v159, vcc
	global_load_dword v188, v[158:159], off offset:2048 nt
	global_load_dword v187, v[194:195], off offset:64 nt
	global_load_dword v186, v[194:195], off offset:128 nt
	global_load_dword v149, v[194:195], off offset:192 nt
	v_lshl_add_u64 v[156:157], s[4:5], 0, v[156:157]
	v_lshl_add_u64 v[156:157], v[156:157], 0, v[2:3]
	s_waitcnt vmcnt(12)
	v_mul_f32_e32 v144, v165, v144
	v_mul_f32_e32 v159, v144, v245
	ds_bpermute_b32 v158, v1, v159
	s_and_saveexec_b64 s[0:1], s[6:7]
	s_cbranch_execz .LBB0_889
	v_lshlrev_b32_e32 v195, 16, v246
	v_and_b32_e32 v194, 0xffff0000, v246
	s_waitcnt lgkmcnt(0)
	v_pk_mul_f32 v[158:159], v[158:159], v[194:195]
	s_nop 0
	v_and_b32_sdwa v144, v159, v227 dst_sel:DWORD dst_unused:UNUSED_PAD src0_sel:WORD_1 src1_sel:DWORD
	v_and_b32_sdwa v194, v158, v227 dst_sel:DWORD dst_unused:UNUSED_PAD src0_sel:WORD_1 src1_sel:DWORD
	v_add3_u32 v144, v159, v144, s97
	v_add3_u32 v158, v158, v194, s97
	v_lshrrev_b32_e32 v144, 16, v144
	v_and_or_b32 v144, v158, s66, v144
	global_store_dword v[156:157], v144, off offset:2048

; __device__ __forceinline__ float bflo(unsigned w) { return __uint_as_float(w << 16); }
; __device__ __forceinline__ float bfhi(unsigned w) { return __uint_as_float(w & 0xffff0000u); }
; __device__ __forceinline__ unsigned pk2(float lo, float hi) { return f2bf(lo) | (f2bf(hi) << 16); }
; __device__ __forceinline__ int crow(int r, int hi) { return (r & 3) + 8 * (r >> 2) + 4 * hi; }
; __global__ void __launch_bounds__(NWAVES * 64, 2) mega_fwd(Args args) {
;     ...
;                                       rli[r] = __builtin_amdgcn_rsqf(ssq * (1.0f / 256.0f) + RMS_EPS) * (1.0f - lam_init); } }
; #pragma unroll
;                                 for (int hv = 0; hv < 2; ++hv)
; #pragma unroll
;                                   for (int rq = 0; rq < 4; ++rq) { unsigned zz[16]; f32x4 t[4];
;                                     int wv_ = wave; asm volatile("" : "+s"(wv_));
; #pragma unroll
;                                     for (int rr = 0; rr < 4; ++rr) { const int r = rq * 4 + rr; const bf16_t* zp = PROJ + (size_t)(b * SEQ + L * 256 + wv_ * 32 + att::crow(r, hi)) * NC + C_ZB + h * 256 + hv * 128 + (r32 & ~1);
; #pragma unroll
;                                         for (int d0 = 0; d0 < 4; ++d0) zz[rr * 4 + d0] = *(const unsigned*)(zp + d0 * 32);
;                                         if (hv == 0) t[rr] = *(const f32x4*)(sq + r * 4); else t[rr] = (f32x4){o[0][r], o[1][r], o[2][r], o[3][r]}; }
;                                     asm volatile("" ::: "memory");
; #pragma unroll
;                                     for (int rr = 0; rr < 4; ++rr) { const int r = rq * 4 + rr; bf16_t* yp = Y + (size_t)(b * SEQ + L * 256 + wv_ * 32 + att::crow(r, hi)) * YS + BW + h * 256 + hv * 128 + r32;
; #pragma unroll
;                                         for (int d0 = 0; d0 < 4; ++d0) { const float val = t[rr][d0] * rli[r] * sg[hv * 4 + d0], vn = __shfl_xor(val, 1);
;                                             if ((r32 & 1) == 0) *(unsigned*)(yp + d0 * 32) = pk2(val * bflo(zz[rr * 4 + d0]), vn * bfhi(zz[rr * 4 + d0])); } } }
.LBB0_919:
	s_or_b64 exec, exec, s[0:1]
	s_waitcnt lgkmcnt(0)
	v_add_f32_e32 v132, v168, v180
	v_fmamk_f32 v132, v132, 0x3b800000, v221
	s_mov_b32 s0, s11
	v_rsq_f32_e32 v132, v132
	v_add_u32_e32 v180, 16, v162
	v_lshl_add_u32 v156, s0, 5, v180
	v_readlane_b32 s0, v253, 48
	v_readlane_b32 s1, v253, 49
	v_mul_f32_e32 v168, v205, v132
	s_waitcnt vmcnt(0)
	v_mov_b32_e32 v149, v3
	v_mov_b64_e32 v[158:159], s[0:1]
	v_mad_i64_i32 v[132:133], s[0:1], v156, s8, v[158:159]
	v_lshl_add_u64 v[132:133], v[132:133], 0, s[2:3]
	v_or_b32_e32 v154, 1, v156
	v_lshl_add_u64 v[132:133], v[132:133], 0, v[148:149]
	v_mad_i64_i32 v[150:151], s[0:1], v154, s8, v[158:159]
	v_lshl_add_u64 v[134:135], v[132:133], 0, s[12:13]
	v_add_co_u32_e32 v132, vcc, s10, v132
	v_lshl_add_u64 v[150:151], v[150:151], 0, s[2:3]
	s_nop 0
	v_addc_co_u32_e32 v133, vcc, 0, v133, vcc
	v_lshl_add_u64 v[150:151], v[150:151], 0, v[148:149]
	v_lshl_add_u64 v[152:153], v[150:151], 0, s[12:13]
	v_add_co_u32_e32 v150, vcc, s10, v150
	global_load_dword v238, v[132:133], off offset:2048 nt
	global_load_dword v233, v[134:135], off offset:64 nt
	global_load_dword v223, v[134:135], off offset:128 nt
	global_load_dword v155, v[134:135], off offset:192 nt
	s_nop 0
	s_mov_b64 s[100:101], 0x2000
	v_lshl_add_u64 v[236:237], v[236:237], 0, s[100:101]
	global_load_dwordx4 v[132:135], v[236:237], off offset:-1024
	global_load_dwordx4 v[136:139], v[236:237], off offset:-2048
	global_load_dwordx4 v[140:143], v[236:237], off offset:-3072
	global_load_dwordx4 v[144:147], v[236:237], off offset:-4096
	s_mov_b32 s100, 0xffffe000
	s_mov_b32 s101, -1
	v_lshl_add_u64 v[236:237], v[236:237], 0, s[100:101]
	v_addc_co_u32_e32 v151, vcc, 0, v151, vcc
	global_load_dword v193, v[150:151], off offset:2048 nt
	global_load_dword v192, v[152:153], off offset:64 nt
	global_load_dword v191, v[152:153], off offset:128 nt
	s_nop 0
	global_load_dword v153, v[152:153], off offset:192 nt
	v_or_b32_e32 v152, 2, v156
	v_mad_i64_i32 v[150:151], s[0:1], v152, s8, v[158:159]
	v_lshl_add_u64 v[150:151], v[150:151], 0, s[2:3]
	v_lshl_add_u64 v[150:151], v[150:151], 0, v[148:149]
	v_lshl_add_u64 v[186:187], v[150:151], 0, s[12:13]
	v_add_co_u32_e32 v150, vcc, s10, v150
	v_ashrrev_i32_e32 v157, 31, v156
	s_nop 0
	v_addc_co_u32_e32 v151, vcc, 0, v151, vcc
	global_load_dword v190, v[150:151], off offset:2048 nt
	global_load_dword v189, v[186:187], off offset:64 nt
	global_load_dword v188, v[186:187], off offset:128 nt
	s_nop 0
	global_load_dword v151, v[186:187], off offset:192 nt
	v_or_b32_e32 v150, 3, v156
	v_mad_i64_i32 v[158:159], s[0:1], v150, s8, v[158:159]
	v_lshl_add_u64 v[158:159], v[158:159], 0, s[2:3]
	v_lshl_add_u64 v[158:159], v[158:159], 0, v[148:149]
	v_lshl_add_u64 v[194:195], v[158:159], 0, s[12:13]
	v_add_co_u32_e32 v158, vcc, s10, v158
	v_lshlrev_b64 v[156:157], 13, v[156:157]
	s_nop 0
	v_addc_co_u32_e32 v159, vcc, 0, v159, vcc
	global_load_dword v187, v[158:159], off offset:2048 nt
	global_load_dword v186, v[194:195], off offset:64 nt
	global_load_dword v185, v[194:195], off offset:128 nt
	global_load_dword v149, v[194:195], off offset:192 nt
	v_lshl_add_u64 v[156:157], s[4:5], 0, v[156:157]
	v_lshl_add_u64 v[156:157], v[156:157], 0, v[2:3]
	s_waitcnt vmcnt(12)
	v_mul_f32_e32 v144, v168, v144
	v_mul_f32_e32 v159, v144, v245
	ds_bpermute_b32 v158, v1, v159
	s_and_saveexec_b64 s[0:1], s[6:7]
	s_cbranch_execz .LBB0_921
	v_lshlrev_b32_e32 v195, 16, v238
	v_and_b32_e32 v194, 0xffff0000, v238
	s_waitcnt lgkmcnt(0)
	v_pk_mul_f32 v[158:159], v[158:159], v[194:195]
	s_nop 0
	v_and_b32_sdwa v144, v159, v227 dst_sel:DWORD dst_unused:UNUSED_PAD src0_sel:WORD_1 src1_sel:DWORD
	v_and_b32_sdwa v194, v158, v227 dst_sel:DWORD dst_unused:UNUSED_PAD src0_sel:WORD_1 src1_sel:DWORD
	v_add3_u32 v144, v159, v144, s97
	v_add3_u32 v158, v158, v194, s97
	v_lshrrev_b32_e32 v144, 16, v144
	v_and_or_b32 v144, v158, s66, v144
	global_store_dword v[156:157], v144, off offset:2048

; __device__ __forceinline__ float bflo(unsigned w) { return __uint_as_float(w << 16); }
; __device__ __forceinline__ float bfhi(unsigned w) { return __uint_as_float(w & 0xffff0000u); }
; __device__ __forceinline__ unsigned pk2(float lo, float hi) { return f2bf(lo) | (f2bf(hi) << 16); }
; __device__ __forceinline__ int crow(int r, int hi) { return (r & 3) + 8 * (r >> 2) + 4 * hi; }
; __global__ void __launch_bounds__(NWAVES * 64, 2) mega_fwd(Args args) {
;     ...
;                                       rli[r] = __builtin_amdgcn_rsqf(ssq * (1.0f / 256.0f) + RMS_EPS) * (1.0f - lam_init); } }
; #pragma unroll
;                                 for (int hv = 0; hv < 2; ++hv)
; #pragma unroll
;                                   for (int rq = 0; rq < 4; ++rq) { unsigned zz[16]; f32x4 t[4];
;                                     int wv_ = wave; asm volatile("" : "+s"(wv_));
; #pragma unroll
;                                     for (int rr = 0; rr < 4; ++rr) { const int r = rq * 4 + rr; const bf16_t* zp = PROJ + (size_t)(b * SEQ + L * 256 + wv_ * 32 + att::crow(r, hi)) * NC + C_ZB + h * 256 + hv * 128 + (r32 & ~1);
; #pragma unroll
;                                         for (int d0 = 0; d0 < 4; ++d0) zz[rr * 4 + d0] = *(const unsigned*)(zp + d0 * 32);
;                                         if (hv == 0) t[rr] = *(const f32x4*)(sq + r * 4); else t[rr] = (f32x4){o[0][r], o[1][r], o[2][r], o[3][r]}; }
;                                     asm volatile("" ::: "memory");
; #pragma unroll
;                                     for (int rr = 0; rr < 4; ++rr) { const int r = rq * 4 + rr; bf16_t* yp = Y + (size_t)(b * SEQ + L * 256 + wv_ * 32 + att::crow(r, hi)) * YS + BW + h * 256 + hv * 128 + r32;
; #pragma unroll
;                                         for (int d0 = 0; d0 < 4; ++d0) { const float val = t[rr][d0] * rli[r] * sg[hv * 4 + d0], vn = __shfl_xor(val, 1);
;                                             if ((r32 & 1) == 0) *(unsigned*)(yp + d0 * 32) = pk2(val * bflo(zz[rr * 4 + d0]), vn * bfhi(zz[rr * 4 + d0])); } } }
.LBB0_951:
	s_or_b64 exec, exec, s[0:1]
	s_waitcnt lgkmcnt(0)
	v_add_f32_e32 v132, v172, v181
	v_fmamk_f32 v132, v132, 0x3b800000, v221
	s_mov_b32 s0, s11
	v_rsq_f32_e32 v132, v132
	v_add_u32_e32 v181, 24, v162
	v_lshl_add_u32 v156, s0, 5, v181
	v_readlane_b32 s0, v253, 48
	v_readlane_b32 s1, v253, 49
	v_mul_f32_e32 v172, v205, v132
	s_waitcnt vmcnt(0)
	v_mov_b32_e32 v149, v3
	v_mov_b64_e32 v[158:159], s[0:1]
	v_mad_i64_i32 v[132:133], s[0:1], v156, s8, v[158:159]
	v_lshl_add_u64 v[132:133], v[132:133], 0, s[2:3]
	v_or_b32_e32 v154, 1, v156
	v_lshl_add_u64 v[132:133], v[132:133], 0, v[148:149]
	v_mad_i64_i32 v[150:151], s[0:1], v154, s8, v[158:159]
	v_lshl_add_u64 v[134:135], v[132:133], 0, s[12:13]
	v_add_co_u32_e32 v132, vcc, s10, v132
	v_lshl_add_u64 v[150:151], v[150:151], 0, s[2:3]
	s_nop 0
	v_addc_co_u32_e32 v133, vcc, 0, v133, vcc
	v_lshl_add_u64 v[150:151], v[150:151], 0, v[148:149]
	v_lshl_add_u64 v[152:153], v[150:151], 0, s[12:13]
	v_add_co_u32_e32 v150, vcc, s10, v150
	global_load_dword v193, v[132:133], off offset:2048 nt
	global_load_dword v192, v[134:135], off offset:64 nt
	global_load_dword v191, v[134:135], off offset:128 nt
	global_load_dword v155, v[134:135], off offset:192 nt
	s_nop 0
	s_mov_b64 s[100:101], 0x2000
	v_lshl_add_u64 v[236:237], v[236:237], 0, s[100:101]
	global_load_dwordx4 v[132:135], v[236:237], off offset:3072
	global_load_dwordx4 v[136:139], v[236:237], off offset:2048
	global_load_dwordx4 v[140:143], v[236:237], off offset:1024
	global_load_dwordx4 v[144:147], v[236:237], off
	s_mov_b32 s100, 0xffffe000
	s_mov_b32 s101, -1
	v_lshl_add_u64 v[236:237], v[236:237], 0, s[100:101]
	v_addc_co_u32_e32 v151, vcc, 0, v151, vcc
	global_load_dword v190, v[150:151], off offset:2048 nt
	global_load_dword v189, v[152:153], off offset:64 nt
	global_load_dword v188, v[152:153], off offset:128 nt
	s_nop 0
	global_load_dword v153, v[152:153], off offset:192 nt
	v_or_b32_e32 v152, 2, v156
	v_mad_i64_i32 v[150:151], s[0:1], v152, s8, v[158:159]
	v_lshl_add_u64 v[150:151], v[150:151], 0, s[2:3]
	v_lshl_add_u64 v[150:151], v[150:151], 0, v[148:149]
	v_lshl_add_u64 v[182:183], v[150:151], 0, s[12:13]
	v_add_co_u32_e32 v150, vcc, s10, v150
	v_ashrrev_i32_e32 v157, 31, v156
	s_nop 0
	v_addc_co_u32_e32 v151, vcc, 0, v151, vcc
	global_load_dword v187, v[150:151], off offset:2048 nt
	global_load_dword v186, v[182:183], off offset:64 nt
	global_load_dword v185, v[182:183], off offset:128 nt
	s_nop 0
	global_load_dword v151, v[182:183], off offset:192 nt
	v_or_b32_e32 v150, 3, v156
	v_mad_i64_i32 v[158:159], s[0:1], v150, s8, v[158:159]
	v_lshl_add_u64 v[158:159], v[158:159], 0, s[2:3]
	v_lshl_add_u64 v[158:159], v[158:159], 0, v[148:149]
	v_lshl_add_u64 v[194:195], v[158:159], 0, s[12:13]
	v_add_co_u32_e32 v158, vcc, s10, v158
	v_lshlrev_b64 v[156:157], 13, v[156:157]
	s_nop 0
	v_addc_co_u32_e32 v159, vcc, 0, v159, vcc
	global_load_dword v184, v[158:159], off offset:2048 nt
	global_load_dword v183, v[194:195], off offset:64 nt
	global_load_dword v182, v[194:195], off offset:128 nt
	global_load_dword v149, v[194:195], off offset:192 nt
	v_lshl_add_u64 v[156:157], s[4:5], 0, v[156:157]
	v_lshl_add_u64 v[156:157], v[156:157], 0, v[2:3]
	s_waitcnt vmcnt(12)
	v_mul_f32_e32 v144, v172, v144
	v_mul_f32_e32 v159, v144, v245
	ds_bpermute_b32 v158, v1, v159
	s_and_saveexec_b64 s[0:1], s[6:7]
	s_cbranch_execz .LBB0_953
	v_lshlrev_b32_e32 v195, 16, v193
	v_and_b32_e32 v194, 0xffff0000, v193
	s_waitcnt lgkmcnt(0)
	v_pk_mul_f32 v[158:159], v[158:159], v[194:195]
	s_nop 0
	v_and_b32_sdwa v144, v159, v227 dst_sel:DWORD dst_unused:UNUSED_PAD src0_sel:WORD_1 src1_sel:DWORD
	v_and_b32_sdwa v193, v158, v227 dst_sel:DWORD dst_unused:UNUSED_PAD src0_sel:WORD_1 src1_sel:DWORD
	v_add3_u32 v144, v159, v144, s97
	v_add3_u32 v158, v158, v193, s97
	v_lshrrev_b32_e32 v144, 16, v144
	v_and_or_b32 v144, v158, s66, v144
	global_store_dword v[156:157], v144, off offset:2048

; __device__ __forceinline__ float bflo(unsigned w) { return __uint_as_float(w << 16); }
; __device__ __forceinline__ float bfhi(unsigned w) { return __uint_as_float(w & 0xffff0000u); }
; __device__ __forceinline__ unsigned pk2(float lo, float hi) { return f2bf(lo) | (f2bf(hi) << 16); }
; __device__ __forceinline__ int crow(int r, int hi) { return (r & 3) + 8 * (r >> 2) + 4 * hi; }
; __global__ void __launch_bounds__(NWAVES * 64, 2) mega_fwd(Args args) {
;     ...
;                                   for (int rq = 0; rq < 4; ++rq) { unsigned zz[16]; f32x4 t[4];
;                                     int wv_ = wave; asm volatile("" : "+s"(wv_));
; #pragma unroll
;                                     for (int rr = 0; rr < 4; ++rr) { const int r = rq * 4 + rr; const bf16_t* zp = PROJ + (size_t)(b * SEQ + L * 256 + wv_ * 32 + att::crow(r, hi)) * NC + C_ZB + h * 256 + hv * 128 + (r32 & ~1);
; #pragma unroll
;                                         for (int d0 = 0; d0 < 4; ++d0) zz[rr * 4 + d0] = *(const unsigned*)(zp + d0 * 32);
;                                         if (hv == 0) t[rr] = *(const f32x4*)(sq + r * 4); else t[rr] = (f32x4){o[0][r], o[1][r], o[2][r], o[3][r]}; }
;                                     asm volatile("" ::: "memory");
; #pragma unroll
;                                     for (int rr = 0; rr < 4; ++rr) { const int r = rq * 4 + rr; bf16_t* yp = Y + (size_t)(b * SEQ + L * 256 + wv_ * 32 + att::crow(r, hi)) * YS + BW + h * 256 + hv * 128 + r32;
; #pragma unroll
;                                         for (int d0 = 0; d0 < 4; ++d0) { const float val = t[rr][d0] * rli[r] * sg[hv * 4 + d0], vn = __shfl_xor(val, 1);
;                                             if ((r32 & 1) == 0) *(unsigned*)(yp + d0 * 32) = pk2(val * bflo(zz[rr * 4 + d0]), vn * bfhi(zz[rr * 4 + d0])); } } }
.LBB0_983:
	s_or_b64 exec, exec, s[0:1]
	s_mov_b32 s0, s11
	s_mov_b32 s2, 0xe800
	v_lshl_add_u32 v138, s0, 5, v162
	v_readlane_b32 s0, v254, 61
	v_readlane_b32 s1, v254, 62
	s_waitcnt vmcnt(0)
	v_mov_b32_e32 v149, v3
	v_or_b32_e32 v136, 1, v138
	v_mov_b64_e32 v[140:141], s[0:1]
	s_waitcnt lgkmcnt(0)
	v_mad_i64_i32 v[132:133], s[0:1], v138, s2, v[140:141]
	v_lshl_add_u64 v[132:133], v[132:133], 0, v[148:149]
	v_lshl_add_u64 v[134:135], v[132:133], 0, s[14:15]
	v_add_co_u32_e32 v132, vcc, 0x3000, v132
	v_ashrrev_i32_e32 v139, 31, v138
	s_nop 0
	v_addc_co_u32_e32 v133, vcc, 0, v133, vcc
	global_load_dword v159, v[132:133], off offset:2304 nt
	global_load_dword v158, v[134:135], off offset:64 nt
	global_load_dword v157, v[134:135], off offset:128 nt
	global_load_dword v137, v[134:135], off offset:192 nt
	v_mad_i64_i32 v[132:133], s[0:1], v136, s2, v[140:141]
	v_lshl_add_u64 v[132:133], v[132:133], 0, v[148:149]
	v_lshl_add_u64 v[134:135], v[132:133], 0, s[14:15]
	v_add_co_u32_e32 v132, vcc, 0x3000, v132
	s_nop 1
	v_addc_co_u32_e32 v133, vcc, 0, v133, vcc
	global_load_dword v155, v[132:133], off offset:2304 nt
	global_load_dword v154, v[134:135], off offset:64 nt
	global_load_dword v153, v[134:135], off offset:128 nt
	s_nop 0
	global_load_dword v135, v[134:135], off offset:192 nt
	v_or_b32_e32 v134, 2, v138
	v_mad_i64_i32 v[132:133], s[0:1], v134, s2, v[140:141]
	v_lshl_add_u64 v[132:133], v[132:133], 0, v[148:149]
	v_lshl_add_u64 v[146:147], v[132:133], 0, s[14:15]
	v_add_co_u32_e32 v132, vcc, 0x3000, v132
	s_nop 1
	v_addc_co_u32_e32 v133, vcc, 0, v133, vcc
	global_load_dword v152, v[132:133], off offset:2304 nt
	global_load_dword v151, v[146:147], off offset:64 nt
	global_load_dword v150, v[146:147], off offset:128 nt
	s_nop 0
	global_load_dword v133, v[146:147], off offset:192 nt
	v_or_b32_e32 v132, 3, v138
	v_mad_i64_i32 v[140:141], s[0:1], v132, s2, v[140:141]
	v_lshl_add_u64 v[140:141], v[140:141], 0, v[148:149]
	v_lshl_add_u64 v[160:161], v[140:141], 0, s[14:15]
	v_add_co_u32_e32 v140, vcc, 0x3000, v140
	v_lshlrev_b64 v[138:139], 13, v[138:139]
	s_nop 0
	v_addc_co_u32_e32 v141, vcc, 0, v141, vcc
	global_load_dword v147, v[140:141], off offset:2304 nt
	global_load_dword v146, v[160:161], off offset:64 nt
	global_load_dword v145, v[160:161], off offset:128 nt
	global_load_dword v143, v[160:161], off offset:192 nt
	v_mul_f32_e32 v140, v215, v68
	v_mul_f32_e32 v141, v140, v213
	ds_bpermute_b32 v140, v1, v141
	v_lshl_add_u64 v[138:139], s[4:5], 0, v[138:139]
	v_lshl_add_u64 v[138:139], v[138:139], 0, v[2:3]
	s_and_saveexec_b64 s[0:1], s[6:7]
	s_cbranch_execz .LBB0_985
	s_waitcnt vmcnt(15)
	v_lshlrev_b32_e32 v161, 16, v159
	v_and_b32_e32 v160, 0xffff0000, v159
	s_waitcnt lgkmcnt(0)
	v_pk_mul_f32 v[140:141], v[140:141], v[160:161]
	s_nop 0
	v_and_b32_sdwa v149, v141, v227 dst_sel:DWORD dst_unused:UNUSED_PAD src0_sel:WORD_1 src1_sel:DWORD
	v_and_b32_sdwa v159, v140, v227 dst_sel:DWORD dst_unused:UNUSED_PAD src0_sel:WORD_1 src1_sel:DWORD
	v_add3_u32 v141, v141, v149, s97
	v_add3_u32 v140, v140, v159, s97
	v_lshrrev_b32_e32 v141, 16, v141
	v_and_or_b32 v140, v140, s66, v141
	global_store_dword v[138:139], v140, off offset:2304

; __device__ __forceinline__ float bflo(unsigned w) { return __uint_as_float(w << 16); }
; __device__ __forceinline__ float bfhi(unsigned w) { return __uint_as_float(w & 0xffff0000u); }
; __device__ __forceinline__ unsigned pk2(float lo, float hi) { return f2bf(lo) | (f2bf(hi) << 16); }
; __device__ __forceinline__ int crow(int r, int hi) { return (r & 3) + 8 * (r >> 2) + 4 * hi; }
; __global__ void __launch_bounds__(NWAVES * 64, 2) mega_fwd(Args args) {
;     ...
;                                   for (int rq = 0; rq < 4; ++rq) { unsigned zz[16]; f32x4 t[4];
;                                     int wv_ = wave; asm volatile("" : "+s"(wv_));
; #pragma unroll
;                                     for (int rr = 0; rr < 4; ++rr) { const int r = rq * 4 + rr; const bf16_t* zp = PROJ + (size_t)(b * SEQ + L * 256 + wv_ * 32 + att::crow(r, hi)) * NC + C_ZB + h * 256 + hv * 128 + (r32 & ~1);
; #pragma unroll
;                                         for (int d0 = 0; d0 < 4; ++d0) zz[rr * 4 + d0] = *(const unsigned*)(zp + d0 * 32);
;                                         if (hv == 0) t[rr] = *(const f32x4*)(sq + r * 4); else t[rr] = (f32x4){o[0][r], o[1][r], o[2][r], o[3][r]}; }
;                                     asm volatile("" ::: "memory");
; #pragma unroll
;                                     for (int rr = 0; rr < 4; ++rr) { const int r = rq * 4 + rr; bf16_t* yp = Y + (size_t)(b * SEQ + L * 256 + wv_ * 32 + att::crow(r, hi)) * YS + BW + h * 256 + hv * 128 + r32;
; #pragma unroll
;                                         for (int d0 = 0; d0 < 4; ++d0) { const float val = t[rr][d0] * rli[r] * sg[hv * 4 + d0], vn = __shfl_xor(val, 1);
;                                             if ((r32 & 1) == 0) *(unsigned*)(yp + d0 * 32) = pk2(val * bflo(zz[rr * 4 + d0]), vn * bfhi(zz[rr * 4 + d0])); } } }
.LBB0_1015:
	s_or_b64 exec, exec, s[0:1]
	s_mov_b32 s0, s11
	v_mov_b32_e32 v149, v3
	v_lshl_add_u32 v138, s0, 5, v176
	v_readlane_b32 s0, v254, 61
	v_readlane_b32 s1, v254, 62
	v_or_b32_e32 v136, 1, v138
	v_ashrrev_i32_e32 v139, 31, v138
	v_mov_b64_e32 v[140:141], s[0:1]
	v_mad_i64_i32 v[132:133], s[0:1], v138, s2, v[140:141]
	v_lshl_add_u64 v[132:133], v[132:133], 0, v[148:149]
	s_waitcnt lgkmcnt(0)
	v_lshl_add_u64 v[134:135], v[132:133], 0, s[14:15]
	v_add_co_u32_e32 v132, vcc, 0x3000, v132
	s_nop 1
	v_addc_co_u32_e32 v133, vcc, 0, v133, vcc
	global_load_dword v159, v[132:133], off offset:2304 nt
	global_load_dword v158, v[134:135], off offset:64 nt
	global_load_dword v157, v[134:135], off offset:128 nt
	global_load_dword v137, v[134:135], off offset:192 nt
	v_mad_i64_i32 v[132:133], s[0:1], v136, s2, v[140:141]
	v_lshl_add_u64 v[132:133], v[132:133], 0, v[148:149]
	v_lshl_add_u64 v[134:135], v[132:133], 0, s[14:15]
	v_add_co_u32_e32 v132, vcc, 0x3000, v132
	s_nop 1
	v_addc_co_u32_e32 v133, vcc, 0, v133, vcc
	global_load_dword v155, v[132:133], off offset:2304 nt
	global_load_dword v154, v[134:135], off offset:64 nt
	global_load_dword v153, v[134:135], off offset:128 nt
	s_nop 0
	global_load_dword v135, v[134:135], off offset:192 nt
	v_or_b32_e32 v134, 2, v138
	v_mad_i64_i32 v[132:133], s[0:1], v134, s2, v[140:141]
	v_lshl_add_u64 v[132:133], v[132:133], 0, v[148:149]
	s_waitcnt vmcnt(10)
	v_lshl_add_u64 v[146:147], v[132:133], 0, s[14:15]
	v_add_co_u32_e32 v132, vcc, 0x3000, v132
	s_nop 1
	v_addc_co_u32_e32 v133, vcc, 0, v133, vcc
	global_load_dword v152, v[132:133], off offset:2304 nt
	global_load_dword v151, v[146:147], off offset:64 nt
	global_load_dword v150, v[146:147], off offset:128 nt
	s_nop 0
	global_load_dword v133, v[146:147], off offset:192 nt
	v_or_b32_e32 v132, 3, v138
	v_mad_i64_i32 v[140:141], s[0:1], v132, s2, v[140:141]
	v_lshl_add_u64 v[140:141], v[140:141], 0, v[148:149]
	v_lshl_add_u64 v[160:161], v[140:141], 0, s[14:15]
	v_add_co_u32_e32 v140, vcc, 0x3000, v140
	v_lshlrev_b64 v[138:139], 13, v[138:139]
	s_nop 0
	v_addc_co_u32_e32 v141, vcc, 0, v141, vcc
	global_load_dword v147, v[140:141], off offset:2304 nt
	global_load_dword v146, v[160:161], off offset:64 nt
	global_load_dword v145, v[160:161], off offset:128 nt
	global_load_dword v143, v[160:161], off offset:192 nt
	v_mul_f32_e32 v140, v165, v84
	v_mul_f32_e32 v141, v140, v213
	ds_bpermute_b32 v140, v1, v141
	v_lshl_add_u64 v[138:139], s[4:5], 0, v[138:139]
	v_lshl_add_u64 v[138:139], v[138:139], 0, v[2:3]
	s_and_saveexec_b64 s[0:1], s[6:7]
	s_cbranch_execz .LBB0_1017
	s_waitcnt vmcnt(15)
	v_lshlrev_b32_e32 v161, 16, v159
	v_and_b32_e32 v160, 0xffff0000, v159
	s_waitcnt lgkmcnt(0)
	v_pk_mul_f32 v[140:141], v[140:141], v[160:161]
	s_nop 0
	v_and_b32_sdwa v149, v141, v227 dst_sel:DWORD dst_unused:UNUSED_PAD src0_sel:WORD_1 src1_sel:DWORD
	v_and_b32_sdwa v159, v140, v227 dst_sel:DWORD dst_unused:UNUSED_PAD src0_sel:WORD_1 src1_sel:DWORD
	v_add3_u32 v141, v141, v149, s97
	v_add3_u32 v140, v140, v159, s97
	v_lshrrev_b32_e32 v141, 16, v141
	v_and_or_b32 v140, v140, s66, v141
	global_store_dword v[138:139], v140, off offset:2304

; __device__ __forceinline__ float bflo(unsigned w) { return __uint_as_float(w << 16); }
; __device__ __forceinline__ float bfhi(unsigned w) { return __uint_as_float(w & 0xffff0000u); }
; __device__ __forceinline__ unsigned pk2(float lo, float hi) { return f2bf(lo) | (f2bf(hi) << 16); }
; __device__ __forceinline__ int crow(int r, int hi) { return (r & 3) + 8 * (r >> 2) + 4 * hi; }
; __global__ void __launch_bounds__(NWAVES * 64, 2) mega_fwd(Args args) {
;     ...
;                                   for (int rq = 0; rq < 4; ++rq) { unsigned zz[16]; f32x4 t[4];
;                                     int wv_ = wave; asm volatile("" : "+s"(wv_));
; #pragma unroll
;                                     for (int rr = 0; rr < 4; ++rr) { const int r = rq * 4 + rr; const bf16_t* zp = PROJ + (size_t)(b * SEQ + L * 256 + wv_ * 32 + att::crow(r, hi)) * NC + C_ZB + h * 256 + hv * 128 + (r32 & ~1);
; #pragma unroll
;                                         for (int d0 = 0; d0 < 4; ++d0) zz[rr * 4 + d0] = *(const unsigned*)(zp + d0 * 32);
;                                         if (hv == 0) t[rr] = *(const f32x4*)(sq + r * 4); else t[rr] = (f32x4){o[0][r], o[1][r], o[2][r], o[3][r]}; }
;                                     asm volatile("" ::: "memory");
; #pragma unroll
;                                     for (int rr = 0; rr < 4; ++rr) { const int r = rq * 4 + rr; bf16_t* yp = Y + (size_t)(b * SEQ + L * 256 + wv_ * 32 + att::crow(r, hi)) * YS + BW + h * 256 + hv * 128 + r32;
; #pragma unroll
;                                         for (int d0 = 0; d0 < 4; ++d0) { const float val = t[rr][d0] * rli[r] * sg[hv * 4 + d0], vn = __shfl_xor(val, 1);
;                                             if ((r32 & 1) == 0) *(unsigned*)(yp + d0 * 32) = pk2(val * bflo(zz[rr * 4 + d0]), vn * bfhi(zz[rr * 4 + d0])); } } }
.LBB0_1047:
	s_or_b64 exec, exec, s[0:1]
	s_mov_b32 s0, s11
	v_mov_b32_e32 v149, v3
	v_lshl_add_u32 v138, s0, 5, v180
	v_readlane_b32 s0, v254, 61
	v_readlane_b32 s1, v254, 62
	v_or_b32_e32 v136, 1, v138
	v_ashrrev_i32_e32 v139, 31, v138
	v_mov_b64_e32 v[140:141], s[0:1]
	v_mad_i64_i32 v[132:133], s[0:1], v138, s2, v[140:141]
	v_lshl_add_u64 v[132:133], v[132:133], 0, v[148:149]
	s_waitcnt lgkmcnt(0)
	v_lshl_add_u64 v[134:135], v[132:133], 0, s[14:15]
	v_add_co_u32_e32 v132, vcc, 0x3000, v132
	s_nop 1
	v_addc_co_u32_e32 v133, vcc, 0, v133, vcc
	global_load_dword v159, v[132:133], off offset:2304 nt
	global_load_dword v158, v[134:135], off offset:64 nt
	global_load_dword v157, v[134:135], off offset:128 nt
	global_load_dword v137, v[134:135], off offset:192 nt
	v_mad_i64_i32 v[132:133], s[0:1], v136, s2, v[140:141]
	v_lshl_add_u64 v[132:133], v[132:133], 0, v[148:149]
	v_lshl_add_u64 v[134:135], v[132:133], 0, s[14:15]
	v_add_co_u32_e32 v132, vcc, 0x3000, v132
	s_nop 1
	v_addc_co_u32_e32 v133, vcc, 0, v133, vcc
	global_load_dword v155, v[132:133], off offset:2304 nt
	global_load_dword v154, v[134:135], off offset:64 nt
	global_load_dword v153, v[134:135], off offset:128 nt
	s_nop 0
	global_load_dword v135, v[134:135], off offset:192 nt
	v_or_b32_e32 v134, 2, v138
	v_mad_i64_i32 v[132:133], s[0:1], v134, s2, v[140:141]
	v_lshl_add_u64 v[132:133], v[132:133], 0, v[148:149]
	s_waitcnt vmcnt(10)
	v_lshl_add_u64 v[146:147], v[132:133], 0, s[14:15]
	v_add_co_u32_e32 v132, vcc, 0x3000, v132
	s_nop 1
	v_addc_co_u32_e32 v133, vcc, 0, v133, vcc
	global_load_dword v152, v[132:133], off offset:2304 nt
	global_load_dword v151, v[146:147], off offset:64 nt
	global_load_dword v150, v[146:147], off offset:128 nt
	s_nop 0
	global_load_dword v133, v[146:147], off offset:192 nt
	v_or_b32_e32 v132, 3, v138
	v_mad_i64_i32 v[140:141], s[0:1], v132, s2, v[140:141]
	v_lshl_add_u64 v[140:141], v[140:141], 0, v[148:149]
	v_lshl_add_u64 v[160:161], v[140:141], 0, s[14:15]
	v_add_co_u32_e32 v140, vcc, 0x3000, v140
	v_lshlrev_b64 v[138:139], 13, v[138:139]
	s_nop 0
	v_addc_co_u32_e32 v141, vcc, 0, v141, vcc
	global_load_dword v147, v[140:141], off offset:2304 nt
	global_load_dword v146, v[160:161], off offset:64 nt
	global_load_dword v145, v[160:161], off offset:128 nt
	global_load_dword v143, v[160:161], off offset:192 nt
	v_mul_f32_e32 v140, v168, v100
	v_mul_f32_e32 v141, v140, v213
	ds_bpermute_b32 v140, v1, v141
	v_lshl_add_u64 v[138:139], s[4:5], 0, v[138:139]
	v_lshl_add_u64 v[138:139], v[138:139], 0, v[2:3]
	s_and_saveexec_b64 s[0:1], s[6:7]
	s_cbranch_execz .LBB0_1049
	s_waitcnt vmcnt(15)
	v_lshlrev_b32_e32 v161, 16, v159
	v_and_b32_e32 v160, 0xffff0000, v159
	s_waitcnt lgkmcnt(0)
	v_pk_mul_f32 v[140:141], v[140:141], v[160:161]
	s_nop 0
	v_and_b32_sdwa v149, v141, v227 dst_sel:DWORD dst_unused:UNUSED_PAD src0_sel:WORD_1 src1_sel:DWORD
	v_and_b32_sdwa v159, v140, v227 dst_sel:DWORD dst_unused:UNUSED_PAD src0_sel:WORD_1 src1_sel:DWORD
	v_add3_u32 v141, v141, v149, s97
	v_add3_u32 v140, v140, v159, s97
	v_lshrrev_b32_e32 v141, 16, v141
	v_and_or_b32 v140, v140, s66, v141
	global_store_dword v[138:139], v140, off offset:2304

; __device__ __forceinline__ float bflo(unsigned w) { return __uint_as_float(w << 16); }
; __device__ __forceinline__ float bfhi(unsigned w) { return __uint_as_float(w & 0xffff0000u); }
; __device__ __forceinline__ unsigned pk2(float lo, float hi) { return f2bf(lo) | (f2bf(hi) << 16); }
; __device__ __forceinline__ int crow(int r, int hi) { return (r & 3) + 8 * (r >> 2) + 4 * hi; }
; __global__ void __launch_bounds__(NWAVES * 64, 2) mega_fwd(Args args) {
;     ...
;                                   for (int rq = 0; rq < 4; ++rq) { unsigned zz[16]; f32x4 t[4];
;                                     int wv_ = wave; asm volatile("" : "+s"(wv_));
; #pragma unroll
;                                     for (int rr = 0; rr < 4; ++rr) { const int r = rq * 4 + rr; const bf16_t* zp = PROJ + (size_t)(b * SEQ + L * 256 + wv_ * 32 + att::crow(r, hi)) * NC + C_ZB + h * 256 + hv * 128 + (r32 & ~1);
; #pragma unroll
;                                         for (int d0 = 0; d0 < 4; ++d0) zz[rr * 4 + d0] = *(const unsigned*)(zp + d0 * 32);
;                                         if (hv == 0) t[rr] = *(const f32x4*)(sq + r * 4); else t[rr] = (f32x4){o[0][r], o[1][r], o[2][r], o[3][r]}; }
;                                     asm volatile("" ::: "memory");
; #pragma unroll
;                                     for (int rr = 0; rr < 4; ++rr) { const int r = rq * 4 + rr; bf16_t* yp = Y + (size_t)(b * SEQ + L * 256 + wv_ * 32 + att::crow(r, hi)) * YS + BW + h * 256 + hv * 128 + r32;
; #pragma unroll
;                                         for (int d0 = 0; d0 < 4; ++d0) { const float val = t[rr][d0] * rli[r] * sg[hv * 4 + d0], vn = __shfl_xor(val, 1);
;                                             if ((r32 & 1) == 0) *(unsigned*)(yp + d0 * 32) = pk2(val * bflo(zz[rr * 4 + d0]), vn * bfhi(zz[rr * 4 + d0])); } } }
.LBB0_1079:
	s_or_b64 exec, exec, s[0:1]
	s_mov_b32 s0, s11
	v_mov_b32_e32 v149, v3
	v_lshl_add_u32 v138, s0, 5, v181
	v_readlane_b32 s0, v254, 61
	v_readlane_b32 s1, v254, 62
	v_or_b32_e32 v136, 1, v138
	v_ashrrev_i32_e32 v139, 31, v138
	v_mov_b64_e32 v[140:141], s[0:1]
	v_mad_i64_i32 v[132:133], s[0:1], v138, s2, v[140:141]
	v_lshl_add_u64 v[132:133], v[132:133], 0, v[148:149]
	s_waitcnt lgkmcnt(0)
	v_lshl_add_u64 v[134:135], v[132:133], 0, s[14:15]
	v_add_co_u32_e32 v132, vcc, 0x3000, v132
	s_nop 1
	v_addc_co_u32_e32 v133, vcc, 0, v133, vcc
	global_load_dword v159, v[132:133], off offset:2304 nt
	global_load_dword v158, v[134:135], off offset:64 nt
	global_load_dword v157, v[134:135], off offset:128 nt
	global_load_dword v137, v[134:135], off offset:192 nt
	v_mad_i64_i32 v[132:133], s[0:1], v136, s2, v[140:141]
	v_lshl_add_u64 v[132:133], v[132:133], 0, v[148:149]
	v_lshl_add_u64 v[134:135], v[132:133], 0, s[14:15]
	v_add_co_u32_e32 v132, vcc, 0x3000, v132
	s_nop 1
	v_addc_co_u32_e32 v133, vcc, 0, v133, vcc
	global_load_dword v155, v[132:133], off offset:2304 nt
	global_load_dword v154, v[134:135], off offset:64 nt
	global_load_dword v153, v[134:135], off offset:128 nt
	s_nop 0
	global_load_dword v135, v[134:135], off offset:192 nt
	v_or_b32_e32 v134, 2, v138
	v_mad_i64_i32 v[132:133], s[0:1], v134, s2, v[140:141]
	v_lshl_add_u64 v[132:133], v[132:133], 0, v[148:149]
	s_waitcnt vmcnt(10)
	v_lshl_add_u64 v[146:147], v[132:133], 0, s[14:15]
	v_add_co_u32_e32 v132, vcc, 0x3000, v132
	s_nop 1
	v_addc_co_u32_e32 v133, vcc, 0, v133, vcc
	global_load_dword v152, v[132:133], off offset:2304 nt
	global_load_dword v151, v[146:147], off offset:64 nt
	global_load_dword v150, v[146:147], off offset:128 nt
	s_nop 0
	global_load_dword v133, v[146:147], off offset:192 nt
	v_or_b32_e32 v132, 3, v138
	v_mad_i64_i32 v[140:141], s[0:1], v132, s2, v[140:141]
	v_lshl_add_u64 v[140:141], v[140:141], 0, v[148:149]
	v_lshl_add_u64 v[148:149], v[140:141], 0, s[14:15]
	v_add_co_u32_e32 v140, vcc, 0x3000, v140
	v_lshlrev_b64 v[138:139], 13, v[138:139]
	s_nop 0
	v_addc_co_u32_e32 v141, vcc, 0, v141, vcc
	global_load_dword v147, v[140:141], off offset:2304 nt
	global_load_dword v146, v[148:149], off offset:64 nt
	global_load_dword v145, v[148:149], off offset:128 nt
	global_load_dword v143, v[148:149], off offset:192 nt
	v_mul_f32_e32 v140, v172, v116
	v_mul_f32_e32 v141, v140, v213
	ds_bpermute_b32 v140, v1, v141
	v_lshl_add_u64 v[138:139], s[4:5], 0, v[138:139]
	v_lshl_add_u64 v[138:139], v[138:139], 0, v[2:3]
	s_and_saveexec_b64 s[0:1], s[6:7]
	s_cbranch_execz .LBB0_1081
	s_waitcnt vmcnt(15)
	v_lshlrev_b32_e32 v149, 16, v159
	v_and_b32_e32 v148, 0xffff0000, v159
	s_waitcnt lgkmcnt(0)
	v_pk_mul_f32 v[140:141], v[140:141], v[148:149]
	s_nop 0
	v_and_b32_sdwa v148, v141, v227 dst_sel:DWORD dst_unused:UNUSED_PAD src0_sel:WORD_1 src1_sel:DWORD
	v_and_b32_sdwa v149, v140, v227 dst_sel:DWORD dst_unused:UNUSED_PAD src0_sel:WORD_1 src1_sel:DWORD
	v_add3_u32 v141, v141, v148, s97
	v_add3_u32 v140, v140, v149, s97
	v_lshrrev_b32_e32 v141, 16, v141
	v_and_or_b32 v140, v140, s66, v141
	global_store_dword v[138:139], v140, off offset:2304

; #define LAS __attribute__((address_space(3)))
; __device__ __forceinline__ void stage_load(u32x4 (&v)[16], const bf16_t* src, int row_stride, int wave, int lane) {
;     const bf16_t* p = src + (size_t)(wave * 2 + (lane >> 5)) * row_stride + (lane & 31) * 8;
; #pragma unroll
;     for (int i = 0; i < 16; ++i) v[i] = *(const u32x4*)(p + (size_t)(16 * i) * row_stride);
; }
; __device__ __forceinline__ void unit(const bf16_t* proj, const bf16_t* mk, const bf16_t* mvt, bf16_t* Y3, int un, LAS unsigned char* lds) {
;     int tid_l = threadIdx.x; asm volatile("" : "+v"(tid_l));
;     const int tid = tid_l, wave = __builtin_amdgcn_readfirstlane(tid >> 6), lane = tid & 63, r32 = lane & 31, hi = lane >> 5;
;     const int tk = un * 8 + wave, rb = tk & 63, h = (tk >> 6) & 3, b = tk >> 8, bt0 = b * SEQ + rb * 32;
;     u32x4 st[16]; att::bf16x8 qr[16];
;     stage_load(st, mk + (size_t)(b * MEML) * 2048 + h * 256, 2048, wave, lane);
;     const bf16_t* qp = proj + (size_t)(bt0 + r32) * NC + C_QM + h * 256 + hi * 8;
; #pragma unroll
;     for (int d0 = 0; d0 < 16; ++d0) qr[d0] = *(const att::bf16x8*)(qp + d0 * 16);
;     asm volatile("" ::: "memory");
;     stage_store(st, lds, wave, lane);
.LBB0_1117:
	s_andn2_b64 vcc, exec, s[0:1]
	s_cbranch_vccnz .LBB0_1375
	v_mov_b32_e32 v220, v0
	s_mov_b32 s11, 0xe800
	v_readfirstlane_b32 s0, v220
	s_ashr_i32 s6, s0, 6
	v_readlane_b32 s0, v254, 47
	s_lshl_b32 s0, s0, 3
	s_add_i32 s0, s0, s6
	s_addk_i32 s0, 0xf400
	s_ashr_i32 s8, s0, 8
	s_lshl_b32 s2, s0, 5
	s_and_b32 s4, s0, 0xffffff00
	s_lshl_b32 s1, s8, 11
	s_and_b32 s2, s2, 0x7e0
	s_ashr_i32 s5, s4, 31
	s_or_b32 s1, s1, s2
	s_lshl_b64 s[4:5], s[4:5], 12
	v_readlane_b32 s2, v253, 59
	s_add_u32 s4, s2, s4
	v_readlane_b32 s2, v253, 60
	s_addc_u32 s5, s2, s5
	s_lshl_b32 s0, s0, 2
	s_and_b32 s0, s0, 0x300
	s_lshl_b32 s2, s0, 1
	s_add_u32 s4, s4, s2
	v_bfe_u32 v200, v220, 5, 1
	s_addc_u32 s5, s5, 0
	s_lshl_b32 s6, s6, 1
	v_or_b32_e32 v198, s6, v200
	v_ashrrev_i32_e32 v199, 31, v198
	v_lshlrev_b64 v[4:5], 12, v[198:199]
	v_lshlrev_b32_e32 v2, 4, v220
	v_lshl_add_u64 v[4:5], s[4:5], 0, v[4:5]
	v_and_b32_e32 v2, 0x1f0, v2
	v_lshl_add_u64 v[60:61], v[4:5], 0, v[2:3]
	v_add_co_u32_e32 v8, vcc, s84, v60
	s_mov_b32 s4, 0x20000
	s_nop 0
	v_addc_co_u32_e32 v9, vcc, 0, v61, vcc
	s_waitcnt lgkmcnt(0)
	global_load_dwordx4 v[4:7], v[60:61], off
	s_nop 0
	global_load_dwordx4 v[8:11], v[8:9], off
	v_add_co_u32_e32 v12, vcc, s4, v60
	s_mov_b32 s4, 0x30000
	s_nop 0
	v_addc_co_u32_e32 v13, vcc, 0, v61, vcc
	v_add_co_u32_e32 v16, vcc, s4, v60
	s_mov_b32 s4, 0x40000
	s_nop 0
	v_addc_co_u32_e32 v17, vcc, 0, v61, vcc
	v_add_co_u32_e32 v20, vcc, s4, v60
	s_mov_b32 s4, 0x50000
	s_nop 0
	v_addc_co_u32_e32 v21, vcc, 0, v61, vcc
	v_add_co_u32_e32 v24, vcc, s4, v60
	s_mov_b32 s4, 0x60000
	s_nop 0
	v_addc_co_u32_e32 v25, vcc, 0, v61, vcc
	v_add_co_u32_e32 v28, vcc, s4, v60
	s_mov_b32 s4, 0x70000
	s_nop 0
	v_addc_co_u32_e32 v29, vcc, 0, v61, vcc
	v_add_co_u32_e32 v32, vcc, s4, v60
	s_mov_b32 s4, 0x80000
	s_nop 0
	v_addc_co_u32_e32 v33, vcc, 0, v61, vcc
	v_add_co_u32_e32 v36, vcc, s4, v60
	s_mov_b32 s4, 0x90000
	s_nop 0
	v_addc_co_u32_e32 v37, vcc, 0, v61, vcc
	v_add_co_u32_e32 v40, vcc, s4, v60
	s_mov_b32 s4, 0xa0000
	s_nop 0
	v_addc_co_u32_e32 v41, vcc, 0, v61, vcc
	v_add_co_u32_e32 v44, vcc, s4, v60
	s_mov_b32 s4, 0xb0000
	s_nop 0
	v_addc_co_u32_e32 v45, vcc, 0, v61, vcc
	v_add_co_u32_e32 v48, vcc, s4, v60
	s_mov_b32 s4, 0xc0000
	s_nop 0
	v_addc_co_u32_e32 v49, vcc, 0, v61, vcc
	v_add_co_u32_e32 v52, vcc, s4, v60
	s_mov_b32 s4, 0xd0000
	s_nop 0
	v_addc_co_u32_e32 v53, vcc, 0, v61, vcc
	v_add_co_u32_e32 v56, vcc, s4, v60
	s_mov_b32 s4, 0xe0000
	s_nop 0
	v_addc_co_u32_e32 v57, vcc, 0, v61, vcc
	v_add_co_u32_e32 v62, vcc, s4, v60
	s_mov_b32 s4, 0xf0000
	s_nop 0
	v_addc_co_u32_e32 v63, vcc, 0, v61, vcc
	v_add_co_u32_e32 v64, vcc, s4, v60
	global_load_dwordx4 v[12:15], v[12:13], off
	s_nop 0
	global_load_dwordx4 v[16:19], v[16:17], off
	v_addc_co_u32_e32 v65, vcc, 0, v61, vcc
	global_load_dwordx4 v[20:23], v[20:21], off
	s_nop 0
	global_load_dwordx4 v[24:27], v[24:25], off
	s_nop 0
	global_load_dwordx4 v[28:31], v[28:29], off
	s_nop 0
	global_load_dwordx4 v[32:35], v[32:33], off
	s_nop 0
	global_load_dwordx4 v[36:39], v[36:37], off
	s_nop 0
	global_load_dwordx4 v[40:43], v[40:41], off
	s_nop 0
	global_load_dwordx4 v[44:47], v[44:45], off
	s_nop 0
	global_load_dwordx4 v[48:51], v[48:49], off
	s_nop 0
	global_load_dwordx4 v[52:55], v[52:53], off
	s_nop 0
	global_load_dwordx4 v[56:59], v[56:57], off
	s_nop 0
	global_load_dwordx4 v[60:63], v[62:63], off
	s_nop 0
	global_load_dwordx4 v[64:67], v[64:65], off
	v_readlane_b32 s4, v253, 48
	s_waitcnt vmcnt(16)
	v_and_b32_e32 v1, 31, v220
	v_readlane_b32 s5, v253, 49
	v_or_b32_e32 v68, s1, v1
	v_lshlrev_b32_e32 v70, 4, v200
	v_mov_b64_e32 v[196:197], s[4:5]
	v_mad_i64_i32 v[68:69], s[4:5], v68, s11, v[196:197]
	v_lshl_add_u64 v[68:69], v[68:69], 0, s[2:3]
	v_mov_b32_e32 v71, v3
	v_lshl_add_u64 v[68:69], v[68:69], 0, v[70:71]
	s_mov_b64 s[4:5], 0x5800
	v_lshl_add_u64 v[70:71], v[68:69], 0, s[4:5]
	s_movk_i32 s4, 0x5000
	v_add_co_u32_e32 v68, vcc, s4, v68
	v_or_b32_e32 v209, 2, v200
	s_nop 0
	v_addc_co_u32_e32 v69, vcc, 0, v69, vcc
	global_load_dwordx4 v[188:191], v[70:71], off offset:32
	global_load_dwordx4 v[184:187], v[70:71], off offset:64
	global_load_dwordx4 v[180:183], v[70:71], off offset:96
	global_load_dwordx4 v[176:179], v[70:71], off offset:128
	global_load_dwordx4 v[172:175], v[70:71], off offset:160
	global_load_dwordx4 v[168:171], v[70:71], off offset:192
	global_load_dwordx4 v[164:167], v[70:71], off offset:224
	global_load_dwordx4 v[160:163], v[70:71], off offset:256
	global_load_dwordx4 v[156:159], v[70:71], off offset:288
	global_load_dwordx4 v[152:155], v[70:71], off offset:320
	global_load_dwordx4 v[148:151], v[70:71], off offset:352
	global_load_dwordx4 v[144:147], v[70:71], off offset:384
	global_load_dwordx4 v[140:143], v[70:71], off offset:416
	global_load_dwordx4 v[136:139], v[70:71], off offset:448
	global_load_dwordx4 v[116:119], v[68:69], off offset:2048
	global_load_dwordx4 v[132:135], v[70:71], off offset:480
	v_bitop3_b32 v69, s6, v220, v200 bitop3:0x36
	v_lshlrev_b32_e32 v69, 4, v69
	v_lshlrev_b32_e32 v68, 9, v198
	v_and_b32_e32 v69, 0x1f0, v69
	v_add3_u32 v222, 0, v68, v69
	s_waitcnt vmcnt(31)
; #define LAS __attribute__((address_space(3)))
; __device__ __forceinline__ void stage_store(const u32x4 (&v)[16], LAS unsigned char* lds, int wave, int lane) {
;     const int c = lane & 31, r0 = wave * 2 + (lane >> 5);
; #pragma unroll
;     for (int i = 0; i < 16; ++i) { const int r = r0 + 16 * i; *(LAS u32x4*)(lds + r * 512 + ((c ^ (r & 31)) << 4)) = v[i]; }
; }
; __device__ __forceinline__ void unit(const bf16_t* proj, const bf16_t* mk, const bf16_t* mvt, bf16_t* Y3, int un, LAS unsigned char* lds) {
;     int tid_l = threadIdx.x; asm volatile("" : "+v"(tid_l));
;     const int tid = tid_l, wave = __builtin_amdgcn_readfirstlane(tid >> 6), lane = tid & 63, r32 = lane & 31, hi = lane >> 5;
;     const int tk = un * 8 + wave, rb = tk & 63, h = (tk >> 6) & 3, b = tk >> 8, bt0 = b * SEQ + rb * 32;
;     u32x4 st[16]; att::bf16x8 qr[16];
;     stage_load(st, mk + (size_t)(b * MEML) * 2048 + h * 256, 2048, wave, lane);
;     const bf16_t* qp = proj + (size_t)(bt0 + r32) * NC + C_QM + h * 256 + hi * 8;
; #pragma unroll
;     for (int d0 = 0; d0 < 16; ++d0) qr[d0] = *(const att::bf16x8*)(qp + d0 * 16);
;     asm volatile("" ::: "memory");
;     stage_store(st, lds, wave, lane);
;     __syncthreads();
;     att::f32x16 s[8];
; #pragma unroll
;     for (int kb = 0; kb < 8; ++kb) { s[kb] = att::f32x16{};
; #pragma unroll
;         for (int q2 = 0; q2 < 8; ++q2) { att::bf16x8 kf[2]; int rv = r32; asm volatile("" : "+v"(rv));
; #pragma unroll
;             for (int i = 0; i < 2; ++i) kf[i] = frag(lds, kb * 32 + rv, 2 * (q2 * 2 + i) + hi);
;             asm volatile("" ::: "memory");
; #pragma unroll
;             for (int i = 0; i < 2; ++i) s[kb] = __builtin_amdgcn_mfma_f32_32x32x16_bf16(kf[i], qr[q2 * 2 + i], s[kb], 0, 0, 0); } }
	ds_write_b128 v222, v[4:7]
	v_add_u32_e32 v4, 16, v198
	v_lshlrev_b32_e32 v5, 9, v4
	v_xor_b32_e32 v4, v4, v220
	v_lshlrev_b32_e32 v4, 4, v4
	v_and_b32_e32 v4, 0x1f0, v4
	v_add3_u32 v224, 0, v5, v4
	v_add_u32_e32 v4, 48, v198
	v_lshlrev_b32_e32 v5, 9, v4
	v_xor_b32_e32 v4, v4, v220
	v_lshlrev_b32_e32 v4, 4, v4
	v_and_b32_e32 v4, 0x1f0, v4
	v_add3_u32 v226, 0, v5, v4
	v_add_u32_e32 v4, 0x50, v198
	v_lshlrev_b32_e32 v5, 9, v4
	v_xor_b32_e32 v4, v4, v220
	v_lshlrev_b32_e32 v4, 4, v4
	v_and_b32_e32 v4, 0x1f0, v4
	v_add3_u32 v228, 0, v5, v4
	v_add_u32_e32 v4, 0x70, v198
	v_lshlrev_b32_e32 v5, 9, v4
	v_xor_b32_e32 v4, v4, v220
	v_lshlrev_b32_e32 v4, 4, v4
	v_and_b32_e32 v4, 0x1f0, v4
	v_add3_u32 v230, 0, v5, v4
	v_add_u32_e32 v4, 0x90, v198
	v_lshlrev_b32_e32 v5, 9, v4
	v_xor_b32_e32 v4, v4, v220
	v_lshlrev_b32_e32 v4, 4, v4
	v_and_b32_e32 v4, 0x1f0, v4
	v_add3_u32 v240, 0, v5, v4
	v_add_u32_e32 v4, 0xb0, v198
	v_lshlrev_b32_e32 v5, 9, v4
	v_xor_b32_e32 v4, v4, v220
	v_lshlrev_b32_e32 v4, 4, v4
	v_and_b32_e32 v4, 0x1f0, v4
	v_add3_u32 v250, 0, v5, v4
	v_add_u32_e32 v4, 0xd0, v198
	v_lshlrev_b32_e32 v5, 9, v4
	v_xor_b32_e32 v4, v4, v220
	v_lshlrev_b32_e32 v4, 4, v4
	v_and_b32_e32 v4, 0x1f0, v4
	v_add3_u32 v194, 0, v5, v4
	v_add_u32_e32 v4, 0xf0, v198
	v_lshlrev_b32_e32 v5, 9, v4
	v_xor_b32_e32 v4, v4, v220
	v_lshlrev_b32_e32 v4, 4, v4
	v_and_b32_e32 v4, 0x1f0, v4
	s_waitcnt vmcnt(30)
	ds_write_b128 v224, v[8:11]
	s_waitcnt vmcnt(29)
	ds_write_b128 v222, v[12:15] offset:16384
	v_add_u32_e32 v223, 0x10000, v222
	v_add_u32_e32 v245, 0x14000, v222
	v_add_u32_e32 v251, 0x18000, v222
	v_add_u32_e32 v195, 0x1c000, v222
	v_add3_u32 v244, 0, v5, v4
	v_mov_b32_e32 v8, v1
	s_waitcnt vmcnt(28)
	ds_write_b128 v226, v[16:19]
	s_waitcnt vmcnt(27)
	ds_write_b128 v222, v[20:23] offset:32768
	s_waitcnt vmcnt(26)
	ds_write_b128 v228, v[24:27]
	s_waitcnt vmcnt(25)
	ds_write_b128 v222, v[28:31] offset:49152
	s_waitcnt vmcnt(24)
	ds_write_b128 v230, v[32:35]
	s_waitcnt vmcnt(23)
	ds_write_b128 v223, v[36:39]
	s_waitcnt vmcnt(22)
	ds_write_b128 v240, v[40:43]
	s_waitcnt vmcnt(21)
	ds_write_b128 v245, v[44:47]
	s_waitcnt vmcnt(20)
	ds_write_b128 v250, v[48:51]
	s_waitcnt vmcnt(19)
	ds_write_b128 v251, v[52:55]
	s_waitcnt vmcnt(18)
	ds_write_b128 v194, v[56:59]
	s_waitcnt vmcnt(17)
	ds_write_b128 v195, v[60:63]
	s_waitcnt vmcnt(16)
	ds_write_b128 v244, v[64:67]
	s_waitcnt lgkmcnt(0)
	s_barrier
	v_mov_b32_e32 v24, v1
	v_lshl_add_u32 v9, v8, 9, 0
	v_bitop3_b32 v4, v8, v200, 31 bitop3:0x6c
	v_lshl_add_u32 v4, v4, 4, v9
	ds_read_b128 v[4:7], v4
	v_bitop3_b32 v8, v8, v209, 31 bitop3:0x6c
	v_lshl_add_u32 v20, v8, 4, v9
	ds_read_b128 v[20:23], v20
	s_waitcnt vmcnt(1) lgkmcnt(1)
	v_mfma_f32_32x32x16_bf16 v[4:19], v[4:7], v[116:119], 0
	v_or_b32_e32 v218, 4, v200
	v_or_b32_e32 v214, 6, v200
	v_lshl_add_u32 v25, v24, 9, 0
	v_or_b32_e32 v217, 8, v200
	v_or_b32_e32 v206, 10, v200
	s_waitcnt lgkmcnt(0)
	v_mfma_f32_32x32x16_bf16 v[4:19], v[20:23], v[188:191], v[4:19]
	v_bitop3_b32 v20, v24, v218, 31 bitop3:0x6c
	v_lshl_add_u32 v20, v20, 4, v25
	ds_read_b128 v[20:23], v20
	v_bitop3_b32 v24, v24, v214, 31 bitop3:0x6c
	v_lshl_add_u32 v24, v24, 4, v25
	v_or_b32_e32 v216, 12, v200
	v_or_b32_e32 v211, 14, v200
	s_waitcnt lgkmcnt(0)
	v_mfma_f32_32x32x16_bf16 v[4:19], v[20:23], v[184:187], v[4:19]
	ds_read_b128 v[20:23], v24
	v_mov_b32_e32 v24, v1
	v_or_b32_e32 v215, 16, v200
	v_lshl_add_u32 v25, v24, 9, 0
	v_or_b32_e32 v202, 18, v200
	s_waitcnt lgkmcnt(0)
	v_mfma_f32_32x32x16_bf16 v[4:19], v[20:23], v[180:183], v[4:19]
	v_bitop3_b32 v20, v24, v217, 31 bitop3:0x6c
	v_lshl_add_u32 v20, v20, 4, v25
	ds_read_b128 v[20:23], v20
	v_bitop3_b32 v24, v24, v206, 31 bitop3:0x6c
	v_lshl_add_u32 v24, v24, 4, v25
	v_or_b32_e32 v213, 20, v200
	v_or_b32_e32 v208, 22, v200
	s_waitcnt lgkmcnt(0)
	v_mfma_f32_32x32x16_bf16 v[4:19], v[20:23], v[176:179], v[4:19]
	ds_read_b128 v[20:23], v24
	v_mov_b32_e32 v24, v1
	v_or_b32_e32 v212, 24, v200
	v_lshl_add_u32 v25, v24, 9, 0
	v_or_b32_e32 v201, 26, v200
	s_waitcnt lgkmcnt(0)
	v_mfma_f32_32x32x16_bf16 v[4:19], v[20:23], v[172:175], v[4:19]
	v_bitop3_b32 v20, v24, v216, 31 bitop3:0x6c
	v_lshl_add_u32 v20, v20, 4, v25
	ds_read_b128 v[20:23], v20
	v_bitop3_b32 v24, v24, v211, 31 bitop3:0x6c
	v_lshl_add_u32 v24, v24, 4, v25
	v_or_b32_e32 v210, 28, v200
	v_or_b32_e32 v204, 30, v200
	s_waitcnt lgkmcnt(0)
	v_mfma_f32_32x32x16_bf16 v[4:19], v[20:23], v[168:171], v[4:19]
	ds_read_b128 v[20:23], v24
	v_mov_b32_e32 v24, v1
	v_mov_b32_e32 v40, v1
	v_lshl_add_u32 v25, v24, 9, 0
	v_mov_b32_e32 v56, v1
	s_waitcnt lgkmcnt(0)
	v_mfma_f32_32x32x16_bf16 v[4:19], v[20:23], v[164:167], v[4:19]
	v_bitop3_b32 v20, v24, v215, 31 bitop3:0x6c
	v_lshl_add_u32 v20, v20, 4, v25
	ds_read_b128 v[20:23], v20
	v_bitop3_b32 v24, v24, v202, 31 bitop3:0x6c
	v_lshl_add_u32 v24, v24, 4, v25
	v_mov_b32_e32 v72, v1
	s_add_i32 s7, 0, 0x10000
	s_waitcnt lgkmcnt(0)
	v_mfma_f32_32x32x16_bf16 v[4:19], v[20:23], v[160:163], v[4:19]
	ds_read_b128 v[20:23], v24
	v_mov_b32_e32 v24, v1
	v_mov_b32_e32 v88, v1
	v_lshl_add_u32 v25, v24, 9, 0
	s_add_i32 s6, 0, 0x14000
	s_waitcnt lgkmcnt(0)
	v_mfma_f32_32x32x16_bf16 v[4:19], v[20:23], v[156:159], v[4:19]
	v_bitop3_b32 v20, v24, v213, 31 bitop3:0x6c
	v_lshl_add_u32 v20, v20, 4, v25
	ds_read_b128 v[20:23], v20
	v_bitop3_b32 v24, v24, v208, 31 bitop3:0x6c
	v_lshl_add_u32 v24, v24, 4, v25
	v_mov_b32_e32 v104, v1
	s_add_i32 s5, 0, 0x18000
	s_waitcnt lgkmcnt(0)
	v_mfma_f32_32x32x16_bf16 v[4:19], v[20:23], v[152:155], v[4:19]
	ds_read_b128 v[20:23], v24
	v_mov_b32_e32 v24, v1
	v_mov_b32_e32 v124, v1
	v_lshl_add_u32 v25, v24, 9, 0
	s_add_i32 s4, 0, 0x1c000
	s_waitcnt lgkmcnt(0)
; __device__ __forceinline__ void unit(const bf16_t* proj, const bf16_t* mk, const bf16_t* mvt, bf16_t* Y3, int un, LAS unsigned char* lds) {
;     ...
;     att::f32x16 s[8];
; #pragma unroll
;     for (int kb = 0; kb < 8; ++kb) { s[kb] = att::f32x16{};
; #pragma unroll
;         for (int q2 = 0; q2 < 8; ++q2) { att::bf16x8 kf[2]; int rv = r32; asm volatile("" : "+v"(rv));
; #pragma unroll
;             for (int i = 0; i < 2; ++i) kf[i] = frag(lds, kb * 32 + rv, 2 * (q2 * 2 + i) + hi);
;             asm volatile("" ::: "memory");
; #pragma unroll
;             for (int i = 0; i < 2; ++i) s[kb] = __builtin_amdgcn_mfma_f32_32x32x16_bf16(kf[i], qr[q2 * 2 + i], s[kb], 0, 0, 0); } }
	v_mfma_f32_32x32x16_bf16 v[4:19], v[20:23], v[148:151], v[4:19]
	v_bitop3_b32 v20, v24, v212, 31 bitop3:0x6c
	v_lshl_add_u32 v20, v20, 4, v25
	ds_read_b128 v[20:23], v20
	v_bitop3_b32 v24, v24, v201, 31 bitop3:0x6c
	v_lshl_add_u32 v24, v24, 4, v25
	s_mov_b32 s9, 0xff800000
	s_lshl_b32 s8, s8, 10
	s_waitcnt lgkmcnt(0)
	v_mfma_f32_32x32x16_bf16 v[4:19], v[20:23], v[144:147], v[4:19]
	ds_read_b128 v[20:23], v24
	v_mov_b32_e32 v24, v1
	s_or_b32 s8, s8, s0
	v_lshl_add_u32 v25, v24, 9, 0
	v_readlane_b32 s10, v254, 33
	s_waitcnt lgkmcnt(0)
	v_mfma_f32_32x32x16_bf16 v[4:19], v[20:23], v[140:143], v[4:19]
	v_bitop3_b32 v20, v24, v210, 31 bitop3:0x6c
	v_lshl_add_u32 v20, v20, 4, v25
	ds_read_b128 v[20:23], v20
	v_bitop3_b32 v24, v24, v204, 31 bitop3:0x6c
	v_lshl_add_u32 v24, v24, 4, v25
	s_mov_b64 s[12:13], 0x6000
	s_waitcnt lgkmcnt(0)
	v_mfma_f32_32x32x16_bf16 v[4:19], v[20:23], v[136:139], v[4:19]
	ds_read_b128 v[20:23], v24
	v_mov_b32_e32 v24, v1
	s_nop 0
	v_lshl_add_u32 v25, v24, 9, 0
	s_waitcnt vmcnt(0) lgkmcnt(0)
	v_mfma_f32_32x32x16_bf16 v[4:19], v[20:23], v[132:135], v[4:19]
	v_bitop3_b32 v20, v24, v200, 31 bitop3:0x6c
	v_lshl_add_u32 v20, v20, 4, v25
	ds_read_b128 v[20:23], v20 offset:16384
	v_bitop3_b32 v24, v24, v209, 31 bitop3:0x6c
	v_lshl_add_u32 v36, v24, 4, v25
	ds_read_b128 v[36:39], v36 offset:16384
	s_waitcnt lgkmcnt(1)
	v_mfma_f32_32x32x16_bf16 v[20:35], v[20:23], v[116:119], 0
	s_nop 0
	v_lshl_add_u32 v41, v40, 9, 0
	s_waitcnt lgkmcnt(0)
	v_mfma_f32_32x32x16_bf16 v[20:35], v[36:39], v[188:191], v[20:35]
	v_bitop3_b32 v36, v40, v218, 31 bitop3:0x6c
	v_lshl_add_u32 v36, v36, 4, v41
	ds_read_b128 v[36:39], v36 offset:16384
	v_bitop3_b32 v40, v40, v214, 31 bitop3:0x6c
	v_lshl_add_u32 v40, v40, 4, v41
	s_waitcnt lgkmcnt(0)
	v_mfma_f32_32x32x16_bf16 v[20:35], v[36:39], v[184:187], v[20:35]
	ds_read_b128 v[36:39], v40 offset:16384
	v_mov_b32_e32 v40, v1
	s_nop 0
	v_lshl_add_u32 v41, v40, 9, 0
	s_waitcnt lgkmcnt(0)
	v_mfma_f32_32x32x16_bf16 v[20:35], v[36:39], v[180:183], v[20:35]
	v_bitop3_b32 v36, v40, v217, 31 bitop3:0x6c
	v_lshl_add_u32 v36, v36, 4, v41
	ds_read_b128 v[36:39], v36 offset:16384
	v_bitop3_b32 v40, v40, v206, 31 bitop3:0x6c
	v_lshl_add_u32 v40, v40, 4, v41
	s_waitcnt lgkmcnt(0)
	v_mfma_f32_32x32x16_bf16 v[20:35], v[36:39], v[176:179], v[20:35]
	ds_read_b128 v[36:39], v40 offset:16384
	v_mov_b32_e32 v40, v1
	s_nop 0
	v_lshl_add_u32 v41, v40, 9, 0
	s_waitcnt lgkmcnt(0)
	v_mfma_f32_32x32x16_bf16 v[20:35], v[36:39], v[172:175], v[20:35]
	v_bitop3_b32 v36, v40, v216, 31 bitop3:0x6c
	v_lshl_add_u32 v36, v36, 4, v41
	ds_read_b128 v[36:39], v36 offset:16384
	v_bitop3_b32 v40, v40, v211, 31 bitop3:0x6c
	v_lshl_add_u32 v40, v40, 4, v41
	s_waitcnt lgkmcnt(0)
	v_mfma_f32_32x32x16_bf16 v[20:35], v[36:39], v[168:171], v[20:35]
	ds_read_b128 v[36:39], v40 offset:16384
	v_mov_b32_e32 v40, v1
	s_nop 0
	v_lshl_add_u32 v41, v40, 9, 0
	s_waitcnt lgkmcnt(0)
	v_mfma_f32_32x32x16_bf16 v[20:35], v[36:39], v[164:167], v[20:35]
	v_bitop3_b32 v36, v40, v215, 31 bitop3:0x6c
	v_lshl_add_u32 v36, v36, 4, v41
	ds_read_b128 v[36:39], v36 offset:16384
	v_bitop3_b32 v40, v40, v202, 31 bitop3:0x6c
	v_lshl_add_u32 v40, v40, 4, v41
	s_waitcnt lgkmcnt(0)
	v_mfma_f32_32x32x16_bf16 v[20:35], v[36:39], v[160:163], v[20:35]
	ds_read_b128 v[36:39], v40 offset:16384
	v_mov_b32_e32 v40, v1
	s_nop 0
	v_lshl_add_u32 v41, v40, 9, 0
	s_waitcnt lgkmcnt(0)
	v_mfma_f32_32x32x16_bf16 v[20:35], v[36:39], v[156:159], v[20:35]
	v_bitop3_b32 v36, v40, v213, 31 bitop3:0x6c
	v_lshl_add_u32 v36, v36, 4, v41
	ds_read_b128 v[36:39], v36 offset:16384
	v_bitop3_b32 v40, v40, v208, 31 bitop3:0x6c
	v_lshl_add_u32 v40, v40, 4, v41
	s_waitcnt lgkmcnt(0)
	v_mfma_f32_32x32x16_bf16 v[20:35], v[36:39], v[152:155], v[20:35]
	ds_read_b128 v[36:39], v40 offset:16384
	v_mov_b32_e32 v40, v1
	s_nop 0
	v_lshl_add_u32 v41, v40, 9, 0
	s_waitcnt lgkmcnt(0)
	v_mfma_f32_32x32x16_bf16 v[20:35], v[36:39], v[148:151], v[20:35]
	v_bitop3_b32 v36, v40, v212, 31 bitop3:0x6c
	v_lshl_add_u32 v36, v36, 4, v41
	ds_read_b128 v[36:39], v36 offset:16384
	v_bitop3_b32 v40, v40, v201, 31 bitop3:0x6c
	v_lshl_add_u32 v40, v40, 4, v41
	s_waitcnt lgkmcnt(0)
	v_mfma_f32_32x32x16_bf16 v[20:35], v[36:39], v[144:147], v[20:35]
	ds_read_b128 v[36:39], v40 offset:16384
	v_mov_b32_e32 v40, v1
	s_nop 0
	v_lshl_add_u32 v41, v40, 9, 0
	s_waitcnt lgkmcnt(0)
	v_mfma_f32_32x32x16_bf16 v[20:35], v[36:39], v[140:143], v[20:35]
	v_bitop3_b32 v36, v40, v210, 31 bitop3:0x6c
	v_lshl_add_u32 v36, v36, 4, v41
	ds_read_b128 v[36:39], v36 offset:16384
	v_bitop3_b32 v40, v40, v204, 31 bitop3:0x6c
	v_lshl_add_u32 v40, v40, 4, v41
	s_waitcnt lgkmcnt(0)
	v_mfma_f32_32x32x16_bf16 v[20:35], v[36:39], v[136:139], v[20:35]
	ds_read_b128 v[36:39], v40 offset:16384
	v_mov_b32_e32 v40, v1
	s_nop 0
	v_lshl_add_u32 v41, v40, 9, 0
	s_waitcnt lgkmcnt(0)
	v_mfma_f32_32x32x16_bf16 v[20:35], v[36:39], v[132:135], v[20:35]
	v_bitop3_b32 v36, v40, v200, 31 bitop3:0x6c
	v_lshl_add_u32 v36, v36, 4, v41
	ds_read_b128 v[36:39], v36 offset:32768
	v_bitop3_b32 v40, v40, v209, 31 bitop3:0x6c
	v_lshl_add_u32 v52, v40, 4, v41
	ds_read_b128 v[52:55], v52 offset:32768
	s_waitcnt lgkmcnt(1)
	v_mfma_f32_32x32x16_bf16 v[36:51], v[36:39], v[116:119], 0
	s_nop 0
	v_lshl_add_u32 v57, v56, 9, 0
	s_waitcnt lgkmcnt(0)
	v_mfma_f32_32x32x16_bf16 v[36:51], v[52:55], v[188:191], v[36:51]
	v_bitop3_b32 v52, v56, v218, 31 bitop3:0x6c
	v_lshl_add_u32 v52, v52, 4, v57
	ds_read_b128 v[52:55], v52 offset:32768
	v_bitop3_b32 v56, v56, v214, 31 bitop3:0x6c
	v_lshl_add_u32 v56, v56, 4, v57
	s_waitcnt lgkmcnt(0)
; __device__ __forceinline__ void unit(const bf16_t* proj, const bf16_t* mk, const bf16_t* mvt, bf16_t* Y3, int un, LAS unsigned char* lds) {
;     ...
;     att::f32x16 s[8];
; #pragma unroll
;     for (int kb = 0; kb < 8; ++kb) { s[kb] = att::f32x16{};
; #pragma unroll
;         for (int q2 = 0; q2 < 8; ++q2) { att::bf16x8 kf[2]; int rv = r32; asm volatile("" : "+v"(rv));
; #pragma unroll
;             for (int i = 0; i < 2; ++i) kf[i] = frag(lds, kb * 32 + rv, 2 * (q2 * 2 + i) + hi);
;             asm volatile("" ::: "memory");
; #pragma unroll
;             for (int i = 0; i < 2; ++i) s[kb] = __builtin_amdgcn_mfma_f32_32x32x16_bf16(kf[i], qr[q2 * 2 + i], s[kb], 0, 0, 0); } }
	v_mfma_f32_32x32x16_bf16 v[36:51], v[52:55], v[184:187], v[36:51]
	ds_read_b128 v[52:55], v56 offset:32768
	v_mov_b32_e32 v56, v1
	s_nop 0
	v_lshl_add_u32 v57, v56, 9, 0
	s_waitcnt lgkmcnt(0)
	v_mfma_f32_32x32x16_bf16 v[36:51], v[52:55], v[180:183], v[36:51]
	v_bitop3_b32 v52, v56, v217, 31 bitop3:0x6c
	v_lshl_add_u32 v52, v52, 4, v57
	ds_read_b128 v[52:55], v52 offset:32768
	v_bitop3_b32 v56, v56, v206, 31 bitop3:0x6c
	v_lshl_add_u32 v56, v56, 4, v57
	s_waitcnt lgkmcnt(0)
	v_mfma_f32_32x32x16_bf16 v[36:51], v[52:55], v[176:179], v[36:51]
	ds_read_b128 v[52:55], v56 offset:32768
	v_mov_b32_e32 v56, v1
	s_nop 0
	v_lshl_add_u32 v57, v56, 9, 0
	s_waitcnt lgkmcnt(0)
	v_mfma_f32_32x32x16_bf16 v[36:51], v[52:55], v[172:175], v[36:51]
	v_bitop3_b32 v52, v56, v216, 31 bitop3:0x6c
	v_lshl_add_u32 v52, v52, 4, v57
	ds_read_b128 v[52:55], v52 offset:32768
	v_bitop3_b32 v56, v56, v211, 31 bitop3:0x6c
	v_lshl_add_u32 v56, v56, 4, v57
	s_waitcnt lgkmcnt(0)
	v_mfma_f32_32x32x16_bf16 v[36:51], v[52:55], v[168:171], v[36:51]
	ds_read_b128 v[52:55], v56 offset:32768
	v_mov_b32_e32 v56, v1
	s_nop 0
	v_lshl_add_u32 v57, v56, 9, 0
	s_waitcnt lgkmcnt(0)
	v_mfma_f32_32x32x16_bf16 v[36:51], v[52:55], v[164:167], v[36:51]
	v_bitop3_b32 v52, v56, v215, 31 bitop3:0x6c
	v_lshl_add_u32 v52, v52, 4, v57
	ds_read_b128 v[52:55], v52 offset:32768
	v_bitop3_b32 v56, v56, v202, 31 bitop3:0x6c
	v_lshl_add_u32 v56, v56, 4, v57
	s_waitcnt lgkmcnt(0)
	v_mfma_f32_32x32x16_bf16 v[36:51], v[52:55], v[160:163], v[36:51]
	ds_read_b128 v[52:55], v56 offset:32768
	v_mov_b32_e32 v56, v1
	s_nop 0
	v_lshl_add_u32 v57, v56, 9, 0
	s_waitcnt lgkmcnt(0)
	v_mfma_f32_32x32x16_bf16 v[36:51], v[52:55], v[156:159], v[36:51]
	v_bitop3_b32 v52, v56, v213, 31 bitop3:0x6c
	v_lshl_add_u32 v52, v52, 4, v57
	ds_read_b128 v[52:55], v52 offset:32768
	v_bitop3_b32 v56, v56, v208, 31 bitop3:0x6c
	v_lshl_add_u32 v56, v56, 4, v57
	s_waitcnt lgkmcnt(0)
	v_mfma_f32_32x32x16_bf16 v[36:51], v[52:55], v[152:155], v[36:51]
	ds_read_b128 v[52:55], v56 offset:32768
	v_mov_b32_e32 v56, v1
	s_nop 0
	v_lshl_add_u32 v57, v56, 9, 0
	s_waitcnt lgkmcnt(0)
	v_mfma_f32_32x32x16_bf16 v[36:51], v[52:55], v[148:151], v[36:51]
	v_bitop3_b32 v52, v56, v212, 31 bitop3:0x6c
	v_lshl_add_u32 v52, v52, 4, v57
	ds_read_b128 v[52:55], v52 offset:32768
	v_bitop3_b32 v56, v56, v201, 31 bitop3:0x6c
	v_lshl_add_u32 v56, v56, 4, v57
	s_waitcnt lgkmcnt(0)
	v_mfma_f32_32x32x16_bf16 v[36:51], v[52:55], v[144:147], v[36:51]
	ds_read_b128 v[52:55], v56 offset:32768
	v_mov_b32_e32 v56, v1
	s_nop 0
	v_lshl_add_u32 v57, v56, 9, 0
	s_waitcnt lgkmcnt(0)
	v_mfma_f32_32x32x16_bf16 v[36:51], v[52:55], v[140:143], v[36:51]
	v_bitop3_b32 v52, v56, v210, 31 bitop3:0x6c
	v_lshl_add_u32 v52, v52, 4, v57
	ds_read_b128 v[52:55], v52 offset:32768
	v_bitop3_b32 v56, v56, v204, 31 bitop3:0x6c
	v_lshl_add_u32 v56, v56, 4, v57
	s_waitcnt lgkmcnt(0)
	v_mfma_f32_32x32x16_bf16 v[36:51], v[52:55], v[136:139], v[36:51]
	ds_read_b128 v[52:55], v56 offset:32768
	v_mov_b32_e32 v56, v1
	s_nop 0
	v_lshl_add_u32 v57, v56, 9, 0
	s_waitcnt lgkmcnt(0)
	v_mfma_f32_32x32x16_bf16 v[36:51], v[52:55], v[132:135], v[36:51]
	v_bitop3_b32 v52, v56, v200, 31 bitop3:0x6c
	v_lshl_add_u32 v52, v52, 4, v57
	ds_read_b128 v[52:55], v52 offset:49152
	v_bitop3_b32 v56, v56, v209, 31 bitop3:0x6c
	v_lshl_add_u32 v68, v56, 4, v57
	ds_read_b128 v[68:71], v68 offset:49152
	s_waitcnt lgkmcnt(1)
	v_mfma_f32_32x32x16_bf16 v[52:67], v[52:55], v[116:119], 0
	s_nop 0
	v_lshl_add_u32 v73, v72, 9, 0
	s_waitcnt lgkmcnt(0)
	v_mfma_f32_32x32x16_bf16 v[52:67], v[68:71], v[188:191], v[52:67]
	v_bitop3_b32 v68, v72, v218, 31 bitop3:0x6c
	v_lshl_add_u32 v68, v68, 4, v73
	ds_read_b128 v[68:71], v68 offset:49152
	v_bitop3_b32 v72, v72, v214, 31 bitop3:0x6c
	v_lshl_add_u32 v72, v72, 4, v73
	s_waitcnt lgkmcnt(0)
	v_mfma_f32_32x32x16_bf16 v[52:67], v[68:71], v[184:187], v[52:67]
	ds_read_b128 v[68:71], v72 offset:49152
	v_mov_b32_e32 v72, v1
	s_nop 0
	v_lshl_add_u32 v73, v72, 9, 0
	s_waitcnt lgkmcnt(0)
	v_mfma_f32_32x32x16_bf16 v[52:67], v[68:71], v[180:183], v[52:67]
	v_bitop3_b32 v68, v72, v217, 31 bitop3:0x6c
	v_lshl_add_u32 v68, v68, 4, v73
	ds_read_b128 v[68:71], v68 offset:49152
	v_bitop3_b32 v72, v72, v206, 31 bitop3:0x6c
	v_lshl_add_u32 v72, v72, 4, v73
	s_waitcnt lgkmcnt(0)
	v_mfma_f32_32x32x16_bf16 v[52:67], v[68:71], v[176:179], v[52:67]
	ds_read_b128 v[68:71], v72 offset:49152
	v_mov_b32_e32 v72, v1
	s_nop 0
	v_lshl_add_u32 v73, v72, 9, 0
	s_waitcnt lgkmcnt(0)
	v_mfma_f32_32x32x16_bf16 v[52:67], v[68:71], v[172:175], v[52:67]
	v_bitop3_b32 v68, v72, v216, 31 bitop3:0x6c
	v_lshl_add_u32 v68, v68, 4, v73
	ds_read_b128 v[68:71], v68 offset:49152
	v_bitop3_b32 v72, v72, v211, 31 bitop3:0x6c
	v_lshl_add_u32 v72, v72, 4, v73
	s_waitcnt lgkmcnt(0)
	v_mfma_f32_32x32x16_bf16 v[52:67], v[68:71], v[168:171], v[52:67]
	ds_read_b128 v[68:71], v72 offset:49152
	v_mov_b32_e32 v72, v1
	s_nop 0
	v_lshl_add_u32 v73, v72, 9, 0
	s_waitcnt lgkmcnt(0)
	v_mfma_f32_32x32x16_bf16 v[52:67], v[68:71], v[164:167], v[52:67]
	v_bitop3_b32 v68, v72, v215, 31 bitop3:0x6c
	v_lshl_add_u32 v68, v68, 4, v73
	ds_read_b128 v[68:71], v68 offset:49152
	v_bitop3_b32 v72, v72, v202, 31 bitop3:0x6c
	v_lshl_add_u32 v72, v72, 4, v73
	s_waitcnt lgkmcnt(0)
	v_mfma_f32_32x32x16_bf16 v[52:67], v[68:71], v[160:163], v[52:67]
	ds_read_b128 v[68:71], v72 offset:49152
	v_mov_b32_e32 v72, v1
	s_nop 0
	v_lshl_add_u32 v73, v72, 9, 0
	s_waitcnt lgkmcnt(0)
	v_mfma_f32_32x32x16_bf16 v[52:67], v[68:71], v[156:159], v[52:67]
	v_bitop3_b32 v68, v72, v213, 31 bitop3:0x6c
	v_lshl_add_u32 v68, v68, 4, v73
	ds_read_b128 v[68:71], v68 offset:49152
	v_bitop3_b32 v72, v72, v208, 31 bitop3:0x6c
	v_lshl_add_u32 v72, v72, 4, v73
	s_waitcnt lgkmcnt(0)
; __device__ __forceinline__ void unit(const bf16_t* proj, const bf16_t* mk, const bf16_t* mvt, bf16_t* Y3, int un, LAS unsigned char* lds) {
;     ...
;     att::f32x16 s[8];
; #pragma unroll
;     for (int kb = 0; kb < 8; ++kb) { s[kb] = att::f32x16{};
; #pragma unroll
;         for (int q2 = 0; q2 < 8; ++q2) { att::bf16x8 kf[2]; int rv = r32; asm volatile("" : "+v"(rv));
; #pragma unroll
;             for (int i = 0; i < 2; ++i) kf[i] = frag(lds, kb * 32 + rv, 2 * (q2 * 2 + i) + hi);
;             asm volatile("" ::: "memory");
; #pragma unroll
;             for (int i = 0; i < 2; ++i) s[kb] = __builtin_amdgcn_mfma_f32_32x32x16_bf16(kf[i], qr[q2 * 2 + i], s[kb], 0, 0, 0); } }
	v_mfma_f32_32x32x16_bf16 v[52:67], v[68:71], v[152:155], v[52:67]
	ds_read_b128 v[68:71], v72 offset:49152
	v_mov_b32_e32 v72, v1
	s_nop 0
	v_lshl_add_u32 v73, v72, 9, 0
	s_waitcnt lgkmcnt(0)
	v_mfma_f32_32x32x16_bf16 v[52:67], v[68:71], v[148:151], v[52:67]
	v_bitop3_b32 v68, v72, v212, 31 bitop3:0x6c
	v_lshl_add_u32 v68, v68, 4, v73
	ds_read_b128 v[68:71], v68 offset:49152
	v_bitop3_b32 v72, v72, v201, 31 bitop3:0x6c
	v_lshl_add_u32 v72, v72, 4, v73
	s_waitcnt lgkmcnt(0)
	v_mfma_f32_32x32x16_bf16 v[52:67], v[68:71], v[144:147], v[52:67]
	ds_read_b128 v[68:71], v72 offset:49152
	v_mov_b32_e32 v72, v1
	s_nop 0
	v_lshl_add_u32 v73, v72, 9, 0
	s_waitcnt lgkmcnt(0)
	v_mfma_f32_32x32x16_bf16 v[52:67], v[68:71], v[140:143], v[52:67]
	v_bitop3_b32 v68, v72, v210, 31 bitop3:0x6c
	v_lshl_add_u32 v68, v68, 4, v73
	ds_read_b128 v[68:71], v68 offset:49152
	v_bitop3_b32 v72, v72, v204, 31 bitop3:0x6c
	v_lshl_add_u32 v72, v72, 4, v73
	s_waitcnt lgkmcnt(0)
	v_mfma_f32_32x32x16_bf16 v[52:67], v[68:71], v[136:139], v[52:67]
	ds_read_b128 v[68:71], v72 offset:49152
	v_mov_b32_e32 v72, v1
	s_nop 0
	v_lshl_add_u32 v73, v72, 9, s7
	s_waitcnt lgkmcnt(0)
	v_mfma_f32_32x32x16_bf16 v[52:67], v[68:71], v[132:135], v[52:67]
	v_bitop3_b32 v68, v72, v200, 31 bitop3:0x6c
	v_lshl_add_u32 v68, v68, 4, v73
	ds_read_b128 v[68:71], v68
	v_bitop3_b32 v72, v72, v209, 31 bitop3:0x6c
	v_lshl_add_u32 v84, v72, 4, v73
	ds_read_b128 v[84:87], v84
	s_waitcnt lgkmcnt(1)
	v_mfma_f32_32x32x16_bf16 v[68:83], v[68:71], v[116:119], 0
	s_nop 0
	v_lshl_add_u32 v89, v88, 9, s7
	s_waitcnt lgkmcnt(0)
	v_mfma_f32_32x32x16_bf16 v[68:83], v[84:87], v[188:191], v[68:83]
	v_bitop3_b32 v84, v88, v218, 31 bitop3:0x6c
	v_lshl_add_u32 v84, v84, 4, v89
	ds_read_b128 v[84:87], v84
	v_bitop3_b32 v88, v88, v214, 31 bitop3:0x6c
	v_lshl_add_u32 v88, v88, 4, v89
	s_waitcnt lgkmcnt(0)
	v_mfma_f32_32x32x16_bf16 v[68:83], v[84:87], v[184:187], v[68:83]
	ds_read_b128 v[84:87], v88
	v_mov_b32_e32 v88, v1
	s_nop 0
	v_lshl_add_u32 v89, v88, 9, s7
	s_waitcnt lgkmcnt(0)
	v_mfma_f32_32x32x16_bf16 v[68:83], v[84:87], v[180:183], v[68:83]
	v_bitop3_b32 v84, v88, v217, 31 bitop3:0x6c
	v_lshl_add_u32 v84, v84, 4, v89
	ds_read_b128 v[84:87], v84
	v_bitop3_b32 v88, v88, v206, 31 bitop3:0x6c
	v_lshl_add_u32 v88, v88, 4, v89
	s_waitcnt lgkmcnt(0)
	v_mfma_f32_32x32x16_bf16 v[68:83], v[84:87], v[176:179], v[68:83]
	ds_read_b128 v[84:87], v88
	v_mov_b32_e32 v88, v1
	s_nop 0
	v_lshl_add_u32 v89, v88, 9, s7
	s_waitcnt lgkmcnt(0)
	v_mfma_f32_32x32x16_bf16 v[68:83], v[84:87], v[172:175], v[68:83]
	v_bitop3_b32 v84, v88, v216, 31 bitop3:0x6c
	v_lshl_add_u32 v84, v84, 4, v89
	ds_read_b128 v[84:87], v84
	v_bitop3_b32 v88, v88, v211, 31 bitop3:0x6c
	v_lshl_add_u32 v88, v88, 4, v89
	s_waitcnt lgkmcnt(0)
	v_mfma_f32_32x32x16_bf16 v[68:83], v[84:87], v[168:171], v[68:83]
	ds_read_b128 v[84:87], v88
	v_mov_b32_e32 v88, v1
	s_nop 0
	v_lshl_add_u32 v89, v88, 9, s7
	s_waitcnt lgkmcnt(0)
	v_mfma_f32_32x32x16_bf16 v[68:83], v[84:87], v[164:167], v[68:83]
	v_bitop3_b32 v84, v88, v215, 31 bitop3:0x6c
	v_lshl_add_u32 v84, v84, 4, v89
	ds_read_b128 v[84:87], v84
	v_bitop3_b32 v88, v88, v202, 31 bitop3:0x6c
	v_lshl_add_u32 v88, v88, 4, v89
	s_waitcnt lgkmcnt(0)
	v_mfma_f32_32x32x16_bf16 v[68:83], v[84:87], v[160:163], v[68:83]
	ds_read_b128 v[84:87], v88
	v_mov_b32_e32 v88, v1
	s_nop 0
	v_lshl_add_u32 v89, v88, 9, s7
	s_waitcnt lgkmcnt(0)
	v_mfma_f32_32x32x16_bf16 v[68:83], v[84:87], v[156:159], v[68:83]
	v_bitop3_b32 v84, v88, v213, 31 bitop3:0x6c
	v_lshl_add_u32 v84, v84, 4, v89
	ds_read_b128 v[84:87], v84
	v_bitop3_b32 v88, v88, v208, 31 bitop3:0x6c
	v_lshl_add_u32 v88, v88, 4, v89
	s_waitcnt lgkmcnt(0)
	v_mfma_f32_32x32x16_bf16 v[68:83], v[84:87], v[152:155], v[68:83]
	ds_read_b128 v[84:87], v88
	v_mov_b32_e32 v88, v1
	s_nop 0
	v_lshl_add_u32 v89, v88, 9, s7
	s_waitcnt lgkmcnt(0)
	v_mfma_f32_32x32x16_bf16 v[68:83], v[84:87], v[148:151], v[68:83]
	v_bitop3_b32 v84, v88, v212, 31 bitop3:0x6c
	v_lshl_add_u32 v84, v84, 4, v89
	ds_read_b128 v[84:87], v84
	v_bitop3_b32 v88, v88, v201, 31 bitop3:0x6c
	v_lshl_add_u32 v88, v88, 4, v89
	s_waitcnt lgkmcnt(0)
	v_mfma_f32_32x32x16_bf16 v[68:83], v[84:87], v[144:147], v[68:83]
	ds_read_b128 v[84:87], v88
	v_mov_b32_e32 v88, v1
	s_nop 0
	v_lshl_add_u32 v89, v88, 9, s7
	s_waitcnt lgkmcnt(0)
	v_mfma_f32_32x32x16_bf16 v[68:83], v[84:87], v[140:143], v[68:83]
	v_bitop3_b32 v84, v88, v210, 31 bitop3:0x6c
	v_lshl_add_u32 v84, v84, 4, v89
	ds_read_b128 v[84:87], v84
	v_bitop3_b32 v88, v88, v204, 31 bitop3:0x6c
	v_lshl_add_u32 v88, v88, 4, v89
	s_waitcnt lgkmcnt(0)
	v_mfma_f32_32x32x16_bf16 v[68:83], v[84:87], v[136:139], v[68:83]
	ds_read_b128 v[84:87], v88
	v_mov_b32_e32 v88, v1
	s_nop 0
	v_lshl_add_u32 v89, v88, 9, s6
	s_waitcnt lgkmcnt(0)
	v_mfma_f32_32x32x16_bf16 v[68:83], v[84:87], v[132:135], v[68:83]
	v_bitop3_b32 v84, v88, v200, 31 bitop3:0x6c
	v_lshl_add_u32 v84, v84, 4, v89
	ds_read_b128 v[84:87], v84
	v_bitop3_b32 v88, v88, v209, 31 bitop3:0x6c
	v_lshl_add_u32 v100, v88, 4, v89
	ds_read_b128 v[100:103], v100
	s_waitcnt lgkmcnt(1)
	v_mfma_f32_32x32x16_bf16 v[84:99], v[84:87], v[116:119], 0
	s_nop 0
	v_lshl_add_u32 v105, v104, 9, s6
	s_waitcnt lgkmcnt(0)
	v_mfma_f32_32x32x16_bf16 v[84:99], v[100:103], v[188:191], v[84:99]
	v_bitop3_b32 v100, v104, v218, 31 bitop3:0x6c
	v_lshl_add_u32 v100, v100, 4, v105
	ds_read_b128 v[100:103], v100
	v_bitop3_b32 v104, v104, v214, 31 bitop3:0x6c
	v_lshl_add_u32 v104, v104, 4, v105
	s_waitcnt lgkmcnt(0)
	v_mfma_f32_32x32x16_bf16 v[84:99], v[100:103], v[184:187], v[84:99]
	ds_read_b128 v[100:103], v104
	v_mov_b32_e32 v104, v1
	s_nop 0
	v_lshl_add_u32 v105, v104, 9, s6
	s_waitcnt lgkmcnt(0)
; __device__ __forceinline__ void unit(const bf16_t* proj, const bf16_t* mk, const bf16_t* mvt, bf16_t* Y3, int un, LAS unsigned char* lds) {
;     ...
;     att::f32x16 s[8];
; #pragma unroll
;     for (int kb = 0; kb < 8; ++kb) { s[kb] = att::f32x16{};
; #pragma unroll
;         for (int q2 = 0; q2 < 8; ++q2) { att::bf16x8 kf[2]; int rv = r32; asm volatile("" : "+v"(rv));
; #pragma unroll
;             for (int i = 0; i < 2; ++i) kf[i] = frag(lds, kb * 32 + rv, 2 * (q2 * 2 + i) + hi);
;             asm volatile("" ::: "memory");
; #pragma unroll
;             for (int i = 0; i < 2; ++i) s[kb] = __builtin_amdgcn_mfma_f32_32x32x16_bf16(kf[i], qr[q2 * 2 + i], s[kb], 0, 0, 0); } }
	v_mfma_f32_32x32x16_bf16 v[84:99], v[100:103], v[180:183], v[84:99]
	v_bitop3_b32 v100, v104, v217, 31 bitop3:0x6c
	v_lshl_add_u32 v100, v100, 4, v105
	ds_read_b128 v[100:103], v100
	v_bitop3_b32 v104, v104, v206, 31 bitop3:0x6c
	v_lshl_add_u32 v104, v104, 4, v105
	s_waitcnt lgkmcnt(0)
	v_mfma_f32_32x32x16_bf16 v[84:99], v[100:103], v[176:179], v[84:99]
	ds_read_b128 v[100:103], v104
	v_mov_b32_e32 v104, v1
	s_nop 0
	v_lshl_add_u32 v105, v104, 9, s6
	s_waitcnt lgkmcnt(0)
	v_mfma_f32_32x32x16_bf16 v[84:99], v[100:103], v[172:175], v[84:99]
	v_bitop3_b32 v100, v104, v216, 31 bitop3:0x6c
	v_lshl_add_u32 v100, v100, 4, v105
	ds_read_b128 v[100:103], v100
	v_bitop3_b32 v104, v104, v211, 31 bitop3:0x6c
	v_lshl_add_u32 v104, v104, 4, v105
	s_waitcnt lgkmcnt(0)
	v_mfma_f32_32x32x16_bf16 v[84:99], v[100:103], v[168:171], v[84:99]
	ds_read_b128 v[100:103], v104
	v_mov_b32_e32 v104, v1
	s_nop 0
	v_lshl_add_u32 v105, v104, 9, s6
	s_waitcnt lgkmcnt(0)
	v_mfma_f32_32x32x16_bf16 v[84:99], v[100:103], v[164:167], v[84:99]
	v_bitop3_b32 v100, v104, v215, 31 bitop3:0x6c
	v_lshl_add_u32 v100, v100, 4, v105
	ds_read_b128 v[100:103], v100
	v_bitop3_b32 v104, v104, v202, 31 bitop3:0x6c
	v_lshl_add_u32 v104, v104, 4, v105
	s_waitcnt lgkmcnt(0)
	v_mfma_f32_32x32x16_bf16 v[84:99], v[100:103], v[160:163], v[84:99]
	ds_read_b128 v[100:103], v104
	v_mov_b32_e32 v104, v1
	s_nop 0
	v_lshl_add_u32 v105, v104, 9, s6
	s_waitcnt lgkmcnt(0)
	v_mfma_f32_32x32x16_bf16 v[84:99], v[100:103], v[156:159], v[84:99]
	v_bitop3_b32 v100, v104, v213, 31 bitop3:0x6c
	v_lshl_add_u32 v100, v100, 4, v105
	ds_read_b128 v[100:103], v100
	v_bitop3_b32 v104, v104, v208, 31 bitop3:0x6c
	v_lshl_add_u32 v104, v104, 4, v105
	s_waitcnt lgkmcnt(0)
	v_mfma_f32_32x32x16_bf16 v[84:99], v[100:103], v[152:155], v[84:99]
	ds_read_b128 v[100:103], v104
	v_mov_b32_e32 v104, v1
	s_nop 0
	v_lshl_add_u32 v105, v104, 9, s6
	s_waitcnt lgkmcnt(0)
	v_mfma_f32_32x32x16_bf16 v[84:99], v[100:103], v[148:151], v[84:99]
	v_bitop3_b32 v100, v104, v212, 31 bitop3:0x6c
	v_lshl_add_u32 v100, v100, 4, v105
	ds_read_b128 v[100:103], v100
	v_bitop3_b32 v104, v104, v201, 31 bitop3:0x6c
	v_lshl_add_u32 v104, v104, 4, v105
	s_waitcnt lgkmcnt(0)
	v_mfma_f32_32x32x16_bf16 v[84:99], v[100:103], v[144:147], v[84:99]
	ds_read_b128 v[100:103], v104
	v_mov_b32_e32 v104, v1
	s_nop 0
	v_lshl_add_u32 v105, v104, 9, s6
	s_waitcnt lgkmcnt(0)
	v_mfma_f32_32x32x16_bf16 v[84:99], v[100:103], v[140:143], v[84:99]
	v_bitop3_b32 v100, v104, v210, 31 bitop3:0x6c
	v_lshl_add_u32 v100, v100, 4, v105
	ds_read_b128 v[100:103], v100
	v_bitop3_b32 v104, v104, v204, 31 bitop3:0x6c
	v_lshl_add_u32 v104, v104, 4, v105
	s_waitcnt lgkmcnt(0)
	v_mfma_f32_32x32x16_bf16 v[84:99], v[100:103], v[136:139], v[84:99]
	ds_read_b128 v[100:103], v104
	v_mov_b32_e32 v104, v1
	s_nop 0
	v_lshl_add_u32 v105, v104, 9, s5
	s_waitcnt lgkmcnt(0)
	v_mfma_f32_32x32x16_bf16 v[84:99], v[100:103], v[132:135], v[84:99]
	v_bitop3_b32 v100, v104, v200, 31 bitop3:0x6c
	v_lshl_add_u32 v100, v100, 4, v105
	ds_read_b128 v[100:103], v100
	v_bitop3_b32 v104, v104, v209, 31 bitop3:0x6c
	v_lshl_add_u32 v120, v104, 4, v105
	ds_read_b128 v[120:123], v120
	s_waitcnt lgkmcnt(1)
	v_mfma_f32_32x32x16_bf16 v[100:115], v[100:103], v[116:119], 0
	s_nop 0
	v_lshl_add_u32 v125, v124, 9, s5
	s_waitcnt lgkmcnt(0)
	v_mfma_f32_32x32x16_bf16 v[100:115], v[120:123], v[188:191], v[100:115]
	v_bitop3_b32 v120, v124, v218, 31 bitop3:0x6c
	v_lshl_add_u32 v120, v120, 4, v125
	ds_read_b128 v[120:123], v120
	v_bitop3_b32 v124, v124, v214, 31 bitop3:0x6c
	v_lshl_add_u32 v124, v124, 4, v125
	s_waitcnt lgkmcnt(0)
	v_mfma_f32_32x32x16_bf16 v[100:115], v[120:123], v[184:187], v[100:115]
	ds_read_b128 v[120:123], v124
	v_mov_b32_e32 v124, v1
	s_nop 0
	v_lshl_add_u32 v125, v124, 9, s5
	s_waitcnt lgkmcnt(0)
	v_mfma_f32_32x32x16_bf16 v[100:115], v[120:123], v[180:183], v[100:115]
	v_bitop3_b32 v120, v124, v217, 31 bitop3:0x6c
	v_lshl_add_u32 v120, v120, 4, v125
	ds_read_b128 v[120:123], v120
	v_bitop3_b32 v124, v124, v206, 31 bitop3:0x6c
	v_lshl_add_u32 v124, v124, 4, v125
	s_waitcnt lgkmcnt(0)
	v_mfma_f32_32x32x16_bf16 v[100:115], v[120:123], v[176:179], v[100:115]
	ds_read_b128 v[120:123], v124
	v_mov_b32_e32 v124, v1
	s_nop 0
	v_lshl_add_u32 v125, v124, 9, s5
	s_waitcnt lgkmcnt(0)
	v_mfma_f32_32x32x16_bf16 v[100:115], v[120:123], v[172:175], v[100:115]
	v_bitop3_b32 v120, v124, v216, 31 bitop3:0x6c
	v_lshl_add_u32 v120, v120, 4, v125
	ds_read_b128 v[120:123], v120
	v_bitop3_b32 v124, v124, v211, 31 bitop3:0x6c
	v_lshl_add_u32 v124, v124, 4, v125
	s_waitcnt lgkmcnt(0)
	v_mfma_f32_32x32x16_bf16 v[100:115], v[120:123], v[168:171], v[100:115]
	ds_read_b128 v[120:123], v124
	v_mov_b32_e32 v124, v1
	s_nop 0
	v_lshl_add_u32 v125, v124, 9, s5
	s_waitcnt lgkmcnt(0)
	v_mfma_f32_32x32x16_bf16 v[100:115], v[120:123], v[164:167], v[100:115]
	v_bitop3_b32 v120, v124, v215, 31 bitop3:0x6c
	v_lshl_add_u32 v120, v120, 4, v125
	ds_read_b128 v[120:123], v120
	v_bitop3_b32 v124, v124, v202, 31 bitop3:0x6c
	v_lshl_add_u32 v124, v124, 4, v125
	s_waitcnt lgkmcnt(0)
	v_mfma_f32_32x32x16_bf16 v[100:115], v[120:123], v[160:163], v[100:115]
	ds_read_b128 v[120:123], v124
	v_mov_b32_e32 v124, v1
	s_nop 0
	v_lshl_add_u32 v125, v124, 9, s5
	s_waitcnt lgkmcnt(0)
	v_mfma_f32_32x32x16_bf16 v[100:115], v[120:123], v[156:159], v[100:115]
	v_bitop3_b32 v120, v124, v213, 31 bitop3:0x6c
	v_lshl_add_u32 v120, v120, 4, v125
	ds_read_b128 v[120:123], v120
	v_bitop3_b32 v124, v124, v208, 31 bitop3:0x6c
	v_lshl_add_u32 v124, v124, 4, v125
	s_waitcnt lgkmcnt(0)
	v_mfma_f32_32x32x16_bf16 v[100:115], v[120:123], v[152:155], v[100:115]
	ds_read_b128 v[120:123], v124
	v_mov_b32_e32 v124, v1
	s_nop 0
	v_lshl_add_u32 v125, v124, 9, s5
	s_waitcnt lgkmcnt(0)
; __device__ __forceinline__ void unit(const bf16_t* proj, const bf16_t* mk, const bf16_t* mvt, bf16_t* Y3, int un, LAS unsigned char* lds) {
;     ...
;     att::f32x16 s[8];
; #pragma unroll
;     for (int kb = 0; kb < 8; ++kb) { s[kb] = att::f32x16{};
; #pragma unroll
;         for (int q2 = 0; q2 < 8; ++q2) { att::bf16x8 kf[2]; int rv = r32; asm volatile("" : "+v"(rv));
; #pragma unroll
;             for (int i = 0; i < 2; ++i) kf[i] = frag(lds, kb * 32 + rv, 2 * (q2 * 2 + i) + hi);
;             asm volatile("" ::: "memory");
; #pragma unroll
;             for (int i = 0; i < 2; ++i) s[kb] = __builtin_amdgcn_mfma_f32_32x32x16_bf16(kf[i], qr[q2 * 2 + i], s[kb], 0, 0, 0); } }
;     constexpr float C = 0.0625f * att::LOG2E;
;     float mx = -__builtin_inff();
; #pragma unroll
;     for (int kb = 0; kb < 8; ++kb)
; #pragma unroll
;         for (int r = 0; r < 16; ++r) mx = fmaxf(mx, s[kb][r]);
	v_mfma_f32_32x32x16_bf16 v[100:115], v[120:123], v[148:151], v[100:115]
	v_bitop3_b32 v120, v124, v212, 31 bitop3:0x6c
	v_lshl_add_u32 v120, v120, 4, v125
	ds_read_b128 v[120:123], v120
	v_bitop3_b32 v124, v124, v201, 31 bitop3:0x6c
	v_lshl_add_u32 v124, v124, 4, v125
	s_waitcnt lgkmcnt(0)
	v_mfma_f32_32x32x16_bf16 v[100:115], v[120:123], v[144:147], v[100:115]
	ds_read_b128 v[120:123], v124
	v_mov_b32_e32 v124, v1
	s_nop 0
	v_lshl_add_u32 v125, v124, 9, s5
	s_waitcnt lgkmcnt(0)
	v_mfma_f32_32x32x16_bf16 v[100:115], v[120:123], v[140:143], v[100:115]
	v_bitop3_b32 v120, v124, v210, 31 bitop3:0x6c
	v_lshl_add_u32 v120, v120, 4, v125
	ds_read_b128 v[120:123], v120
	v_bitop3_b32 v124, v124, v204, 31 bitop3:0x6c
	v_lshl_add_u32 v124, v124, 4, v125
	s_waitcnt lgkmcnt(0)
	v_mfma_f32_32x32x16_bf16 v[100:115], v[120:123], v[136:139], v[100:115]
	ds_read_b128 v[120:123], v124
	v_mov_b32_e32 v124, v1
	s_nop 0
	v_lshl_add_u32 v125, v124, 9, s4
	s_waitcnt lgkmcnt(0)
	v_mfma_f32_32x32x16_bf16 v[100:115], v[120:123], v[132:135], v[100:115]
	v_bitop3_b32 v120, v124, v200, 31 bitop3:0x6c
	v_lshl_add_u32 v120, v120, 4, v125
	ds_read_b128 v[120:123], v120
	v_bitop3_b32 v124, v124, v209, 31 bitop3:0x6c
	v_lshl_add_u32 v192, v124, 4, v125
	ds_read_b128 v[246:249], v192
	v_mov_b32_e32 v192, v1
	s_waitcnt lgkmcnt(1)
	v_mfma_f32_32x32x16_bf16 v[116:131], v[120:123], v[116:119], 0
	s_nop 0
	v_lshl_add_u32 v193, v192, 9, s4
	s_waitcnt lgkmcnt(0)
	v_mfma_f32_32x32x16_bf16 v[116:131], v[246:249], v[188:191], v[116:131]
	v_bitop3_b32 v188, v192, v218, 31 bitop3:0x6c
	v_lshl_add_u32 v188, v188, 4, v193
	ds_read_b128 v[188:191], v188
	v_bitop3_b32 v192, v192, v214, 31 bitop3:0x6c
	v_lshl_add_u32 v192, v192, 4, v193
	s_waitcnt lgkmcnt(0)
	v_mfma_f32_32x32x16_bf16 v[116:131], v[188:191], v[184:187], v[116:131]
	ds_read_b128 v[184:187], v192
	s_waitcnt lgkmcnt(0)
	v_mfma_f32_32x32x16_bf16 v[116:131], v[184:187], v[180:183], v[116:131]
	v_mov_b32_e32 v184, v1
	s_nop 0
	v_lshl_add_u32 v185, v184, 9, s4
	v_bitop3_b32 v180, v184, v217, 31 bitop3:0x6c
	v_lshl_add_u32 v180, v180, 4, v185
	ds_read_b128 v[180:183], v180
	v_bitop3_b32 v184, v184, v206, 31 bitop3:0x6c
	v_lshl_add_u32 v184, v184, 4, v185
	s_waitcnt lgkmcnt(0)
	v_mfma_f32_32x32x16_bf16 v[116:131], v[180:183], v[176:179], v[116:131]
	ds_read_b128 v[176:179], v184
	v_mov_b32_e32 v180, v1
	s_waitcnt lgkmcnt(0)
	v_mfma_f32_32x32x16_bf16 v[116:131], v[176:179], v[172:175], v[116:131]
	v_lshl_add_u32 v176, v180, 9, s4
	v_bitop3_b32 v172, v180, v216, 31 bitop3:0x6c
	v_lshl_add_u32 v172, v172, 4, v176
	ds_read_b128 v[172:175], v172
	v_bitop3_b32 v177, v180, v211, 31 bitop3:0x6c
	v_lshl_add_u32 v176, v177, 4, v176
	ds_read_b128 v[176:179], v176
	s_waitcnt lgkmcnt(1)
	v_mfma_f32_32x32x16_bf16 v[116:131], v[172:175], v[168:171], v[116:131]
	v_mov_b32_e32 v172, v1
	s_nop 0
	v_lshl_add_u32 v173, v172, 9, s4
	v_bitop3_b32 v168, v172, v215, 31 bitop3:0x6c
	v_lshl_add_u32 v168, v168, 4, v173
	ds_read_b128 v[168:171], v168
	s_waitcnt lgkmcnt(1)
	v_mfma_f32_32x32x16_bf16 v[116:131], v[176:179], v[164:167], v[116:131]
	v_bitop3_b32 v164, v172, v202, 31 bitop3:0x6c
	v_lshl_add_u32 v164, v164, 4, v173
	ds_read_b128 v[164:167], v164
	v_mov_b32_e32 v172, v1
	s_waitcnt lgkmcnt(1)
	v_mfma_f32_32x32x16_bf16 v[116:131], v[168:171], v[160:163], v[116:131]
	v_lshl_add_u32 v173, v172, 9, s4
	v_bitop3_b32 v160, v172, v213, 31 bitop3:0x6c
	v_bitop3_b32 v161, v172, v208, 31 bitop3:0x6c
	v_lshl_add_u32 v160, v160, 4, v173
	v_lshl_add_u32 v168, v161, 4, v173
	ds_read_b128 v[160:163], v160
	ds_read_b128 v[168:171], v168
	s_waitcnt lgkmcnt(2)
	v_mfma_f32_32x32x16_bf16 v[116:131], v[164:167], v[156:159], v[116:131]
	v_mov_b32_e32 v156, v1
	v_max3_f32 v164, v4, s9, v5
	v_lshl_add_u32 v157, v156, 9, s4
	v_bitop3_b32 v158, v156, v212, 31 bitop3:0x6c
	v_bitop3_b32 v156, v156, v201, 31 bitop3:0x6c
	v_lshl_add_u32 v158, v158, 4, v157
	s_waitcnt lgkmcnt(1)
	v_mfma_f32_32x32x16_bf16 v[116:131], v[160:163], v[152:155], v[116:131]
	v_lshl_add_u32 v156, v156, 4, v157
	ds_read_b128 v[152:155], v158
	ds_read_b128 v[156:159], v156
	v_mov_b32_e32 v160, v1
	s_ashr_i32 s9, s8, 31
	v_lshl_add_u32 v161, v160, 9, s4
	s_waitcnt lgkmcnt(2)
	v_mfma_f32_32x32x16_bf16 v[116:131], v[168:171], v[148:151], v[116:131]
	v_bitop3_b32 v162, v160, v210, 31 bitop3:0x6c
	v_bitop3_b32 v149, v160, v204, 31 bitop3:0x6c
	v_lshl_add_u32 v148, v162, 4, v161
	v_lshl_add_u32 v160, v149, 4, v161
	ds_read_b128 v[148:151], v148
	ds_read_b128 v[160:163], v160
	s_lshl_b64 s[8:9], s[8:9], 9
	s_add_u32 s8, s10, s8
	s_waitcnt lgkmcnt(3)
	v_mfma_f32_32x32x16_bf16 v[116:131], v[152:155], v[144:147], v[116:131]
	v_max3_f32 v144, v164, v6, v7
	v_max3_f32 v144, v144, v8, v9
	v_max3_f32 v144, v144, v10, v11
	v_max3_f32 v144, v144, v12, v13
	v_max3_f32 v144, v144, v14, v15
	v_max3_f32 v144, v144, v16, v17
	v_max3_f32 v144, v144, v18, v19
	s_waitcnt lgkmcnt(2)
	v_mfma_f32_32x32x16_bf16 v[116:131], v[156:159], v[140:143], v[116:131]
	v_max3_f32 v140, v144, v20, v21
	v_max3_f32 v140, v140, v22, v23
	v_max3_f32 v140, v140, v24, v25
	v_max3_f32 v140, v140, v26, v27
	v_max3_f32 v140, v140, v28, v29
	v_max3_f32 v140, v140, v30, v31
	v_max3_f32 v140, v140, v32, v33
	s_waitcnt lgkmcnt(1)
	v_mfma_f32_32x32x16_bf16 v[116:131], v[148:151], v[136:139], v[116:131]
	v_max3_f32 v136, v140, v34, v35
	v_max3_f32 v136, v136, v36, v37
	v_max3_f32 v136, v136, v38, v39
	v_max3_f32 v136, v136, v40, v41
	v_max3_f32 v136, v136, v42, v43
	v_max3_f32 v136, v136, v44, v45
	v_max3_f32 v136, v136, v46, v47
	s_waitcnt lgkmcnt(0)
; __device__ __forceinline__ void unit(const bf16_t* proj, const bf16_t* mk, const bf16_t* mvt, bf16_t* Y3, int un, LAS unsigned char* lds) {
;     ...
;     float mx = -__builtin_inff();
; #pragma unroll
;     for (int kb = 0; kb < 8; ++kb)
; #pragma unroll
;         for (int r = 0; r < 16; ++r) mx = fmaxf(mx, s[kb][r]);
;     { auto rr = __builtin_amdgcn_permlane32_swap(__float_as_uint(mx), __float_as_uint(mx), false, false); mx = fmaxf(__uint_as_float(rr[0]), __uint_as_float(rr[1])); }
;     float l = 0.f; const float mc = mx * C;
; #pragma unroll
;     for (int kb = 0; kb < 8; ++kb)
; #pragma unroll
;         for (int r = 0; r < 16; ++r) { s[kb][r] = __builtin_amdgcn_exp2f(fmaf(s[kb][r], C, -mc)); l += s[kb][r]; }
	v_mfma_f32_32x32x16_bf16 v[116:131], v[160:163], v[132:135], v[116:131]
	v_max3_f32 v132, v136, v48, v49
	v_max3_f32 v132, v132, v50, v51
	v_max3_f32 v132, v132, v52, v53
	v_max3_f32 v132, v132, v54, v55
	v_max3_f32 v132, v132, v56, v57
	v_max3_f32 v132, v132, v58, v59
	v_max3_f32 v132, v132, v60, v61
	v_max3_f32 v132, v132, v62, v63
	v_max3_f32 v132, v132, v64, v65
	v_max3_f32 v132, v132, v66, v67
	v_max3_f32 v132, v132, v68, v69
	v_max3_f32 v132, v132, v70, v71
	v_max3_f32 v132, v132, v72, v73
	v_max3_f32 v132, v132, v74, v75
	v_max3_f32 v132, v132, v76, v77
	v_max3_f32 v132, v132, v78, v79
	v_max3_f32 v132, v132, v80, v81
	v_max3_f32 v132, v132, v82, v83
	v_max3_f32 v132, v132, v84, v85
	v_max3_f32 v132, v132, v86, v87
	v_max3_f32 v132, v132, v88, v89
	v_max3_f32 v132, v132, v90, v91
	v_max3_f32 v132, v132, v92, v93
	v_max3_f32 v132, v132, v94, v95
	v_max3_f32 v132, v132, v96, v97
	v_max3_f32 v132, v132, v98, v99
	v_max3_f32 v132, v132, v100, v101
	v_max3_f32 v132, v132, v102, v103
	v_max3_f32 v132, v132, v104, v105
	v_max3_f32 v132, v132, v106, v107
	v_max3_f32 v132, v132, v108, v109
	v_max3_f32 v132, v132, v110, v111
	v_max3_f32 v132, v132, v112, v113
	v_max3_f32 v132, v132, v114, v115
	v_max3_f32 v132, v132, v116, v117
	v_max3_f32 v132, v132, v118, v119
	v_max3_f32 v132, v132, v120, v121
	v_max3_f32 v132, v132, v122, v123
	v_max3_f32 v132, v132, v124, v125
	v_max3_f32 v132, v132, v126, v127
	v_max3_f32 v132, v132, v128, v129
	v_max3_f32 v132, v132, v130, v131
	v_mov_b32_e32 v133, v132
	s_nop 1
	v_permlane32_swap_b32_e32 v132, v133
	v_max_f32_e32 v133, v133, v133
	v_max_f32_e32 v132, v132, v132
	v_max_f32_e32 v132, v132, v133
	v_mul_f32_e32 v158, 0xbdb8aa3b, v132
	v_fmamk_f32 v4, v4, 0x3db8aa3b, v158
	v_exp_f32_e32 v159, v4
	v_fmamk_f32 v4, v5, 0x3db8aa3b, v158
	v_exp_f32_e32 v160, v4
	v_fmamk_f32 v4, v6, 0x3db8aa3b, v158
	v_exp_f32_e32 v161, v4
	v_fmamk_f32 v4, v7, 0x3db8aa3b, v158
	v_exp_f32_e32 v162, v4
	v_fmamk_f32 v5, v8, 0x3db8aa3b, v158
	v_add_f32_e32 v4, 0, v159
	v_exp_f32_e32 v163, v5
	v_fmamk_f32 v5, v9, 0x3db8aa3b, v158
	v_add_f32_e32 v4, v160, v4
	v_exp_f32_e32 v164, v5
	v_fmamk_f32 v5, v10, 0x3db8aa3b, v158
	v_add_f32_e32 v4, v161, v4
	v_exp_f32_e32 v165, v5
	v_fmamk_f32 v5, v11, 0x3db8aa3b, v158
	v_add_f32_e32 v4, v162, v4
	v_exp_f32_e32 v166, v5
	v_fmamk_f32 v5, v12, 0x3db8aa3b, v158
	v_add_f32_e32 v4, v163, v4
	v_exp_f32_e32 v167, v5
	v_fmamk_f32 v5, v13, 0x3db8aa3b, v158
	v_add_f32_e32 v4, v164, v4
	v_exp_f32_e32 v168, v5
	v_fmamk_f32 v5, v14, 0x3db8aa3b, v158
	v_add_f32_e32 v4, v165, v4
	v_exp_f32_e32 v169, v5
	v_fmamk_f32 v5, v15, 0x3db8aa3b, v158
	v_add_f32_e32 v4, v166, v4
	v_exp_f32_e32 v170, v5
	v_fmamk_f32 v5, v16, 0x3db8aa3b, v158
	v_add_f32_e32 v4, v167, v4
	v_exp_f32_e32 v171, v5
	v_fmamk_f32 v5, v17, 0x3db8aa3b, v158
	v_add_f32_e32 v4, v168, v4
	v_exp_f32_e32 v172, v5
	v_fmamk_f32 v5, v18, 0x3db8aa3b, v158
	v_add_f32_e32 v4, v169, v4
	v_exp_f32_e32 v173, v5
	v_fmamk_f32 v5, v19, 0x3db8aa3b, v158
	v_add_f32_e32 v4, v170, v4
	v_exp_f32_e32 v174, v5
	v_fmamk_f32 v5, v20, 0x3db8aa3b, v158
	v_add_f32_e32 v4, v171, v4
	v_exp_f32_e32 v175, v5
	v_fmamk_f32 v5, v21, 0x3db8aa3b, v158
	v_add_f32_e32 v4, v172, v4
	v_exp_f32_e32 v176, v5
	v_fmamk_f32 v5, v22, 0x3db8aa3b, v158
	v_add_f32_e32 v4, v173, v4
	v_exp_f32_e32 v177, v5
	v_fmamk_f32 v5, v23, 0x3db8aa3b, v158
	v_add_f32_e32 v4, v174, v4
	v_exp_f32_e32 v178, v5
	v_fmamk_f32 v5, v24, 0x3db8aa3b, v158
	v_add_f32_e32 v4, v175, v4
	v_exp_f32_e32 v24, v5
	v_fmamk_f32 v5, v25, 0x3db8aa3b, v158
	v_add_f32_e32 v4, v176, v4
	v_exp_f32_e32 v25, v5
	v_fmamk_f32 v5, v26, 0x3db8aa3b, v158
	v_add_f32_e32 v4, v177, v4
	v_exp_f32_e32 v26, v5
	v_fmamk_f32 v5, v27, 0x3db8aa3b, v158
	v_add_f32_e32 v4, v178, v4
	v_exp_f32_e32 v27, v5
	v_fmamk_f32 v5, v28, 0x3db8aa3b, v158
	v_add_f32_e32 v4, v24, v4
	v_exp_f32_e32 v179, v5
	v_fmamk_f32 v5, v29, 0x3db8aa3b, v158
	v_add_f32_e32 v4, v25, v4
	v_exp_f32_e32 v180, v5
	v_fmamk_f32 v5, v30, 0x3db8aa3b, v158
	v_add_f32_e32 v4, v26, v4
	v_exp_f32_e32 v181, v5
	v_fmamk_f32 v5, v31, 0x3db8aa3b, v158
	v_add_f32_e32 v4, v27, v4
	v_exp_f32_e32 v182, v5
	v_fmamk_f32 v5, v32, 0x3db8aa3b, v158
	v_add_f32_e32 v4, v179, v4
	v_exp_f32_e32 v32, v5
	v_fmamk_f32 v5, v33, 0x3db8aa3b, v158
	v_add_f32_e32 v4, v180, v4
	v_exp_f32_e32 v33, v5
	v_fmamk_f32 v5, v34, 0x3db8aa3b, v158
	v_add_f32_e32 v4, v181, v4
	v_exp_f32_e32 v34, v5
	v_fmamk_f32 v5, v35, 0x3db8aa3b, v158
	v_add_f32_e32 v4, v182, v4
	v_exp_f32_e32 v35, v5
	v_fmamk_f32 v5, v36, 0x3db8aa3b, v158
	v_add_f32_e32 v4, v32, v4
	v_exp_f32_e32 v183, v5
	v_fmamk_f32 v5, v37, 0x3db8aa3b, v158
	v_add_f32_e32 v4, v33, v4
	v_exp_f32_e32 v184, v5
	v_fmamk_f32 v5, v38, 0x3db8aa3b, v158
	v_add_f32_e32 v4, v34, v4
	v_exp_f32_e32 v185, v5
	v_fmamk_f32 v5, v39, 0x3db8aa3b, v158
	v_add_f32_e32 v4, v35, v4
	v_exp_f32_e32 v186, v5
	v_fmamk_f32 v5, v40, 0x3db8aa3b, v158
	v_add_f32_e32 v4, v183, v4
	v_exp_f32_e32 v40, v5
	v_fmamk_f32 v5, v41, 0x3db8aa3b, v158
	v_add_f32_e32 v4, v184, v4
	v_exp_f32_e32 v41, v5
	v_fmamk_f32 v5, v42, 0x3db8aa3b, v158
	v_add_f32_e32 v4, v185, v4
	v_exp_f32_e32 v42, v5
	v_fmamk_f32 v5, v43, 0x3db8aa3b, v158
	v_add_f32_e32 v4, v186, v4
	v_exp_f32_e32 v43, v5
	v_fmamk_f32 v5, v44, 0x3db8aa3b, v158
	v_add_f32_e32 v4, v40, v4
	v_exp_f32_e32 v187, v5
	v_fmamk_f32 v5, v45, 0x3db8aa3b, v158
	v_add_f32_e32 v4, v41, v4
	v_exp_f32_e32 v188, v5
	v_fmamk_f32 v5, v46, 0x3db8aa3b, v158
	v_add_f32_e32 v4, v42, v4
	v_exp_f32_e32 v189, v5
	v_fmamk_f32 v5, v47, 0x3db8aa3b, v158
	v_add_f32_e32 v4, v43, v4
	v_exp_f32_e32 v190, v5
	v_fmamk_f32 v5, v48, 0x3db8aa3b, v158
	v_add_f32_e32 v4, v187, v4
	v_exp_f32_e32 v48, v5
; __device__ __forceinline__ void stage_load(u32x4 (&v)[16], const bf16_t* src, int row_stride, int wave, int lane) {
;     const bf16_t* p = src + (size_t)(wave * 2 + (lane >> 5)) * row_stride + (lane & 31) * 8;
; #pragma unroll
;     for (int i = 0; i < 16; ++i) v[i] = *(const u32x4*)(p + (size_t)(16 * i) * row_stride);
; __device__ __forceinline__ void unit(const bf16_t* proj, const bf16_t* mk, const bf16_t* mvt, bf16_t* Y3, int un, LAS unsigned char* lds) {
;     ...
;     for (int kb = 0; kb < 8; ++kb)
; #pragma unroll
;         for (int r = 0; r < 16; ++r) { s[kb][r] = __builtin_amdgcn_exp2f(fmaf(s[kb][r], C, -mc)); l += s[kb][r]; }
;     { auto rr = __builtin_amdgcn_permlane32_swap(__float_as_uint(l), __float_as_uint(l), false, false); l = __uint_as_float(rr[0]) + __uint_as_float(rr[1]); }
;     const float linv = 1.0f / l;
;     att::bf16x8 pa[16];
;     ...
; #pragma unroll
;     for (int kb = 0; kb < 8; ++kb) { MEM_PK4(s[kb], 0, pa[2 * kb]); MEM_PK4(s[kb], 8, pa[2 * kb + 1]); }
	v_fmamk_f32 v5, v49, 0x3db8aa3b, v158
	v_add_f32_e32 v4, v188, v4
	v_exp_f32_e32 v49, v5
	v_fmamk_f32 v5, v50, 0x3db8aa3b, v158
	v_add_f32_e32 v4, v189, v4
	v_exp_f32_e32 v50, v5
	v_fmamk_f32 v5, v51, 0x3db8aa3b, v158
	v_add_f32_e32 v4, v190, v4
	v_exp_f32_e32 v51, v5
	v_fmamk_f32 v5, v52, 0x3db8aa3b, v158
	v_add_f32_e32 v4, v48, v4
	v_exp_f32_e32 v52, v5
	v_fmamk_f32 v5, v53, 0x3db8aa3b, v158
	v_add_f32_e32 v4, v49, v4
	v_exp_f32_e32 v53, v5
	v_fmamk_f32 v5, v54, 0x3db8aa3b, v158
	v_add_f32_e32 v4, v50, v4
	v_exp_f32_e32 v54, v5
	v_fmamk_f32 v5, v55, 0x3db8aa3b, v158
	v_add_f32_e32 v4, v51, v4
	v_exp_f32_e32 v55, v5
	v_fmamk_f32 v5, v56, 0x3db8aa3b, v158
	v_add_f32_e32 v4, v52, v4
	v_exp_f32_e32 v56, v5
	v_fmamk_f32 v5, v57, 0x3db8aa3b, v158
	v_add_f32_e32 v4, v53, v4
	v_exp_f32_e32 v57, v5
	v_fmamk_f32 v5, v58, 0x3db8aa3b, v158
	v_add_f32_e32 v4, v54, v4
	v_exp_f32_e32 v58, v5
	v_fmamk_f32 v5, v59, 0x3db8aa3b, v158
	v_add_f32_e32 v4, v55, v4
	v_exp_f32_e32 v59, v5
	v_add_f32_e32 v4, v56, v4
	v_add_f32_e32 v4, v57, v4
	v_add_f32_e32 v4, v58, v4
	v_add_f32_e32 v134, v59, v4
	v_fmamk_f32 v4, v60, 0x3db8aa3b, v158
	v_exp_f32_e32 v136, v4
	v_fmamk_f32 v4, v61, 0x3db8aa3b, v158
	v_exp_f32_e32 v17, v4
	v_fmamk_f32 v4, v62, 0x3db8aa3b, v158
	v_exp_f32_e32 v133, v4
	v_fmamk_f32 v4, v63, 0x3db8aa3b, v158
	v_exp_f32_e32 v15, v4
	v_fmamk_f32 v4, v64, 0x3db8aa3b, v158
	v_exp_f32_e32 v19, v4
	v_fmamk_f32 v4, v65, 0x3db8aa3b, v158
	v_exp_f32_e32 v14, v4
	v_fmamk_f32 v4, v66, 0x3db8aa3b, v158
	v_exp_f32_e32 v18, v4
	v_fmamk_f32 v4, v67, 0x3db8aa3b, v158
	v_exp_f32_e32 v6, v4
	v_fmamk_f32 v4, v68, 0x3db8aa3b, v158
	v_exp_f32_e32 v7, v4
	v_fmamk_f32 v4, v69, 0x3db8aa3b, v158
	v_exp_f32_e32 v8, v4
	v_fmamk_f32 v4, v70, 0x3db8aa3b, v158
	v_exp_f32_e32 v9, v4
	v_fmamk_f32 v4, v71, 0x3db8aa3b, v158
	v_exp_f32_e32 v10, v4
	v_fmamk_f32 v4, v72, 0x3db8aa3b, v158
	v_exp_f32_e32 v11, v4
	v_fmamk_f32 v4, v73, 0x3db8aa3b, v158
	v_exp_f32_e32 v12, v4
	v_fmamk_f32 v4, v74, 0x3db8aa3b, v158
	v_exp_f32_e32 v13, v4
	v_fmamk_f32 v4, v75, 0x3db8aa3b, v158
	v_exp_f32_e32 v16, v4
	v_fmamk_f32 v4, v76, 0x3db8aa3b, v158
	v_exp_f32_e32 v132, v4
	v_fmamk_f32 v4, v77, 0x3db8aa3b, v158
	v_exp_f32_e32 v135, v4
	v_fmamk_f32 v4, v78, 0x3db8aa3b, v158
	v_exp_f32_e32 v137, v4
	v_fmamk_f32 v4, v79, 0x3db8aa3b, v158
	v_exp_f32_e32 v138, v4
	v_fmamk_f32 v4, v80, 0x3db8aa3b, v158
	v_exp_f32_e32 v139, v4
	v_fmamk_f32 v4, v81, 0x3db8aa3b, v158
	v_exp_f32_e32 v140, v4
	v_fmamk_f32 v4, v82, 0x3db8aa3b, v158
	v_exp_f32_e32 v141, v4
	v_fmamk_f32 v4, v83, 0x3db8aa3b, v158
	v_exp_f32_e32 v142, v4
	v_fmamk_f32 v4, v84, 0x3db8aa3b, v158
	v_exp_f32_e32 v84, v4
	v_fmamk_f32 v4, v85, 0x3db8aa3b, v158
	v_exp_f32_e32 v143, v4
	v_fmamk_f32 v4, v86, 0x3db8aa3b, v158
	v_exp_f32_e32 v86, v4
	v_fmamk_f32 v4, v87, 0x3db8aa3b, v158
	v_exp_f32_e32 v144, v4
	v_fmamk_f32 v4, v88, 0x3db8aa3b, v158
	v_exp_f32_e32 v88, v4
	v_fmamk_f32 v4, v89, 0x3db8aa3b, v158
	v_exp_f32_e32 v145, v4
	v_fmamk_f32 v4, v90, 0x3db8aa3b, v158
	v_exp_f32_e32 v90, v4
	v_fmamk_f32 v4, v91, 0x3db8aa3b, v158
	v_exp_f32_e32 v146, v4
	v_fmamk_f32 v4, v92, 0x3db8aa3b, v158
	v_exp_f32_e32 v92, v4
	v_fmamk_f32 v4, v93, 0x3db8aa3b, v158
	v_exp_f32_e32 v147, v4
	v_fmamk_f32 v4, v94, 0x3db8aa3b, v158
	v_exp_f32_e32 v94, v4
	v_fmamk_f32 v4, v95, 0x3db8aa3b, v158
	v_exp_f32_e32 v149, v4
	v_fmamk_f32 v4, v96, 0x3db8aa3b, v158
	v_exp_f32_e32 v96, v4
	v_fmamk_f32 v4, v97, 0x3db8aa3b, v158
	v_exp_f32_e32 v150, v4
	v_fmamk_f32 v4, v98, 0x3db8aa3b, v158
	v_exp_f32_e32 v98, v4
	v_fmamk_f32 v4, v99, 0x3db8aa3b, v158
	v_exp_f32_e32 v151, v4
	v_fmamk_f32 v4, v100, 0x3db8aa3b, v158
	v_exp_f32_e32 v100, v4
	v_fmamk_f32 v4, v101, 0x3db8aa3b, v158
	v_exp_f32_e32 v152, v4
	v_fmamk_f32 v4, v102, 0x3db8aa3b, v158
	v_exp_f32_e32 v102, v4
	v_fmamk_f32 v4, v103, 0x3db8aa3b, v158
	v_exp_f32_e32 v153, v4
	v_fmamk_f32 v4, v104, 0x3db8aa3b, v158
	v_exp_f32_e32 v104, v4
	v_fmamk_f32 v4, v105, 0x3db8aa3b, v158
	v_exp_f32_e32 v154, v4
	v_fmamk_f32 v4, v106, 0x3db8aa3b, v158
	v_exp_f32_e32 v106, v4
	v_fmamk_f32 v4, v107, 0x3db8aa3b, v158
	v_exp_f32_e32 v155, v4
	v_fmamk_f32 v4, v108, 0x3db8aa3b, v158
	v_fmamk_f32 v20, v115, 0x3db8aa3b, v158
	v_exp_f32_e32 v108, v4
	v_fmamk_f32 v4, v109, 0x3db8aa3b, v158
	v_exp_f32_e32 v97, v20
	v_fmamk_f32 v20, v116, 0x3db8aa3b, v158
	v_exp_f32_e32 v156, v4
	v_fmamk_f32 v4, v110, 0x3db8aa3b, v158
	v_exp_f32_e32 v101, v20
	v_fmamk_f32 v20, v117, 0x3db8aa3b, v158
	v_exp_f32_e32 v110, v4
	v_fmamk_f32 v4, v111, 0x3db8aa3b, v158
	v_exp_f32_e32 v105, v20
	v_fmamk_f32 v20, v118, 0x3db8aa3b, v158
	v_exp_f32_e32 v157, v4
	v_fmamk_f32 v4, v112, 0x3db8aa3b, v158
	v_exp_f32_e32 v109, v20
	v_fmamk_f32 v20, v119, 0x3db8aa3b, v158
	v_exp_f32_e32 v112, v4
	v_fmamk_f32 v4, v113, 0x3db8aa3b, v158
	v_exp_f32_e32 v113, v20
	v_fmamk_f32 v20, v120, 0x3db8aa3b, v158
	v_exp_f32_e32 v148, v20
	v_fmamk_f32 v20, v121, 0x3db8aa3b, v158
	v_readlane_b32 s10, v254, 34
	v_exp_f32_e32 v111, v20
	v_fmamk_f32 v20, v122, 0x3db8aa3b, v158
	s_addc_u32 s9, s10, s9
	v_lshlrev_b64 v[116:117], 9, v[198:199]
	v_exp_f32_e32 v115, v20
	v_fmamk_f32 v20, v123, 0x3db8aa3b, v158
	v_lshl_add_u64 v[116:117], s[8:9], 0, v[116:117]
	v_exp_f32_e32 v89, v20
	v_fmamk_f32 v20, v124, 0x3db8aa3b, v158
	v_cvt_pk_bf16_f32 v39, v26, v27
	v_cvt_pk_bf16_f32 v26, v32, v33
	v_cvt_pk_bf16_f32 v45, v185, v186
	v_cvt_pk_bf16_f32 v32, v187, v188
	v_lshl_add_u64 v[186:187], v[116:117], 0, v[2:3]
	s_movk_i32 s8, 0x2000
	v_exp_f32_e32 v93, v20
	v_fmamk_f32 v20, v125, 0x3db8aa3b, v158
	v_add_co_u32_e32 v120, vcc, s8, v186
	v_exp_f32_e32 v99, v20
	v_fmamk_f32 v20, v126, 0x3db8aa3b, v158
	v_addc_co_u32_e32 v121, vcc, 0, v187, vcc
; __device__ __forceinline__ int crow(int r, int hi) { return (r & 3) + 8 * (r >> 2) + 4 * hi; }
; __device__ __forceinline__ void stage_load(u32x4 (&v)[16], const bf16_t* src, int row_stride, int wave, int lane) {
;     const bf16_t* p = src + (size_t)(wave * 2 + (lane >> 5)) * row_stride + (lane & 31) * 8;
; #pragma unroll
;     for (int i = 0; i < 16; ++i) v[i] = *(const u32x4*)(p + (size_t)(16 * i) * row_stride);
; __device__ __forceinline__ void unit(const bf16_t* proj, const bf16_t* mk, const bf16_t* mvt, bf16_t* Y3, int un, LAS unsigned char* lds) {
;     ...
; #pragma unroll
;     for (int kb = 0; kb < 8; ++kb) { MEM_PK4(s[kb], 0, pa[2 * kb]); MEM_PK4(s[kb], 8, pa[2 * kb + 1]); }
;     ...
; #pragma unroll
;     for (int i = 0; i < 16; ++i) { u32x4 w_ = __builtin_bit_cast(u32x4, pa[i]); asm volatile("" : "+v"(w_)); pa[i] = __builtin_bit_cast(att::bf16x8, w_); }
;     float rli[16];
; #pragma unroll
;     for (int r = 0; r < 16; ++r) rli[r] = __shfl(linv, att::crow(r, hi));
;     stage_load(st, mvt + (size_t)((b * 4 + h) * 256) * 256, 256, wave, lane);
	s_movk_i32 s8, 0x4000
	v_exp_f32_e32 v103, v20
	v_fmamk_f32 v20, v127, 0x3db8aa3b, v158
	v_add_co_u32_e32 v124, vcc, s8, v186
	v_exp_f32_e32 v107, v20
	v_fmamk_f32 v20, v128, 0x3db8aa3b, v158
	v_addc_co_u32_e32 v125, vcc, 0, v187, vcc
	s_movk_i32 s10, 0x6000
	v_exp_f32_e32 v91, v20
	v_fmamk_f32 v20, v129, 0x3db8aa3b, v158
	v_add_co_u32_e32 v128, vcc, s10, v186
	v_fmamk_f32 v5, v114, 0x3db8aa3b, v158
	v_exp_f32_e32 v95, v20
	v_fmamk_f32 v20, v130, 0x3db8aa3b, v158
	v_fmac_f32_e32 v158, 0x3db8aa3b, v131
	v_addc_co_u32_e32 v129, vcc, 0, v187, vcc
	s_mov_b32 s8, 0x8000
	v_exp_f32_e32 v87, v158
	v_add_co_u32_e32 v158, vcc, s8, v186
	v_cvt_pk_bf16_f32 v28, v159, v160
	s_nop 0
	v_addc_co_u32_e32 v159, vcc, 0, v187, vcc
	s_mov_b32 s8, 0xa000
	v_cvt_pk_bf16_f32 v29, v161, v162
	v_add_co_u32_e32 v162, vcc, s8, v186
	v_cvt_pk_bf16_f32 v30, v163, v164
	s_nop 0
	v_addc_co_u32_e32 v163, vcc, 0, v187, vcc
	s_mov_b32 s8, 0xc000
	v_cvt_pk_bf16_f32 v31, v165, v166
	v_add_co_u32_e32 v166, vcc, s8, v186
	v_exp_f32_e32 v85, v20
	v_cvt_pk_bf16_f32 v20, v167, v168
	v_addc_co_u32_e32 v167, vcc, 0, v187, vcc
	s_mov_b32 s8, 0xe000
	v_exp_f32_e32 v4, v4
	v_exp_f32_e32 v5, v5
	v_cvt_pk_bf16_f32 v21, v169, v170
	v_add_co_u32_e32 v170, vcc, s8, v186
	v_cvt_pk_bf16_f32 v22, v171, v172
	s_nop 0
	v_addc_co_u32_e32 v171, vcc, 0, v187, vcc
	v_cvt_pk_bf16_f32 v23, v173, v174
	v_add_co_u32_e32 v174, vcc, s84, v186
	v_cvt_pk_bf16_f32 v36, v175, v176
	s_nop 0
	v_addc_co_u32_e32 v175, vcc, 0, v187, vcc
	s_mov_b32 s8, 0x12000
	v_cvt_pk_bf16_f32 v37, v177, v178
	v_cvt_pk_bf16_f32 v38, v24, v25
	v_cvt_pk_bf16_f32 v24, v179, v180
	v_cvt_pk_bf16_f32 v25, v181, v182
	v_cvt_pk_bf16_f32 v27, v34, v35
	v_cvt_pk_bf16_f32 v44, v183, v184
	v_cvt_pk_bf16_f32 v46, v40, v41
	v_cvt_pk_bf16_f32 v47, v42, v43
	v_cvt_pk_bf16_f32 v33, v189, v190
	v_cvt_pk_bf16_f32 v34, v48, v49
	v_cvt_pk_bf16_f32 v35, v50, v51
	v_cvt_pk_bf16_f32 v52, v52, v53
	v_cvt_pk_bf16_f32 v53, v54, v55
	v_cvt_pk_bf16_f32 v54, v56, v57
	v_cvt_pk_bf16_f32 v55, v58, v59
	v_cvt_pk_bf16_f32 v40, v136, v17
	v_cvt_pk_bf16_f32 v41, v133, v15
	v_cvt_pk_bf16_f32 v42, v19, v14
	v_cvt_pk_bf16_f32 v43, v18, v6
	v_cvt_pk_bf16_f32 v60, v7, v8
	v_cvt_pk_bf16_f32 v61, v9, v10
	v_cvt_pk_bf16_f32 v62, v11, v12
	v_cvt_pk_bf16_f32 v63, v13, v16
	v_cvt_pk_bf16_f32 v48, v132, v135
	v_cvt_pk_bf16_f32 v49, v137, v138
	v_cvt_pk_bf16_f32 v50, v139, v140
	v_cvt_pk_bf16_f32 v51, v141, v142
	v_cvt_pk_bf16_f32 v68, v84, v143
	v_cvt_pk_bf16_f32 v69, v86, v144
	v_cvt_pk_bf16_f32 v70, v88, v145
	v_cvt_pk_bf16_f32 v71, v90, v146
	v_cvt_pk_bf16_f32 v56, v92, v147
	v_cvt_pk_bf16_f32 v57, v94, v149
	v_cvt_pk_bf16_f32 v58, v96, v150
	v_cvt_pk_bf16_f32 v59, v98, v151
	v_cvt_pk_bf16_f32 v72, v100, v152
	v_cvt_pk_bf16_f32 v73, v102, v153
	v_cvt_pk_bf16_f32 v74, v104, v154
	v_cvt_pk_bf16_f32 v75, v106, v155
	v_cvt_pk_bf16_f32 v64, v108, v156
	v_cvt_pk_bf16_f32 v65, v110, v157
	v_cvt_pk_bf16_f32 v66, v112, v4
	v_cvt_pk_bf16_f32 v67, v5, v97
	v_cvt_pk_bf16_f32 v76, v101, v105
	v_cvt_pk_bf16_f32 v77, v109, v113
	v_cvt_pk_bf16_f32 v78, v148, v111
	v_cvt_pk_bf16_f32 v79, v115, v89
	v_cvt_pk_bf16_f32 v80, v93, v99
	v_cvt_pk_bf16_f32 v81, v103, v107
	v_cvt_pk_bf16_f32 v82, v91, v95
	v_cvt_pk_bf16_f32 v83, v85, v87
	v_add_co_u32_e32 v178, vcc, s8, v186
	v_permlane32_swap_b32_e32 v28, v30
	v_permlane32_swap_b32_e32 v29, v31
	v_permlane32_swap_b32_e32 v20, v22
	v_permlane32_swap_b32_e32 v21, v23
	v_permlane32_swap_b32_e32 v36, v38
	v_permlane32_swap_b32_e32 v37, v39
	v_permlane32_swap_b32_e32 v24, v26
	v_permlane32_swap_b32_e32 v25, v27
	v_permlane32_swap_b32_e32 v44, v46
	v_permlane32_swap_b32_e32 v45, v47
	v_permlane32_swap_b32_e32 v32, v34
	v_permlane32_swap_b32_e32 v33, v35
	v_permlane32_swap_b32_e32 v52, v54
	v_permlane32_swap_b32_e32 v53, v55
	v_permlane32_swap_b32_e32 v40, v42
	v_permlane32_swap_b32_e32 v41, v43
	v_permlane32_swap_b32_e32 v60, v62
	v_permlane32_swap_b32_e32 v61, v63
	v_permlane32_swap_b32_e32 v48, v50
	v_permlane32_swap_b32_e32 v49, v51
	v_permlane32_swap_b32_e32 v68, v70
	v_permlane32_swap_b32_e32 v69, v71
	v_permlane32_swap_b32_e32 v56, v58
	v_permlane32_swap_b32_e32 v57, v59
	v_permlane32_swap_b32_e32 v72, v74
	v_permlane32_swap_b32_e32 v73, v75
	v_permlane32_swap_b32_e32 v64, v66
	v_permlane32_swap_b32_e32 v65, v67
	v_permlane32_swap_b32_e32 v76, v78
	v_permlane32_swap_b32_e32 v77, v79
	v_permlane32_swap_b32_e32 v80, v82
	v_permlane32_swap_b32_e32 v81, v83
	v_addc_co_u32_e32 v179, vcc, 0, v187, vcc
	s_mov_b32 s8, 0x14000
	global_load_dwordx4 v[116:119], v[186:187], off
	s_nop 0
	global_load_dwordx4 v[120:123], v[120:121], off
	s_nop 0
	global_load_dwordx4 v[124:127], v[124:125], off
	s_nop 0
	global_load_dwordx4 v[128:131], v[128:129], off
	s_nop 0
	global_load_dwordx4 v[158:161], v[158:159], off
	s_nop 0
	global_load_dwordx4 v[162:165], v[162:163], off
	s_nop 0
	global_load_dwordx4 v[166:169], v[166:167], off
	s_nop 0
	global_load_dwordx4 v[170:173], v[170:171], off
	s_nop 0
	global_load_dwordx4 v[174:177], v[174:175], off
	s_nop 0
	global_load_dwordx4 v[178:181], v[178:179], off
	v_add_co_u32_e32 v182, vcc, s8, v186
	s_mov_b32 s8, 0x16000
	s_nop 0
	v_addc_co_u32_e32 v183, vcc, 0, v187, vcc
	v_add_co_u32_e32 v188, vcc, s8, v186
	s_mov_b32 s8, 0x18000
	s_nop 0
	v_addc_co_u32_e32 v189, vcc, 0, v187, vcc
	v_add_co_u32_e32 v190, vcc, s8, v186
	s_mov_b32 s8, 0x1a000
	s_nop 0
	v_addc_co_u32_e32 v191, vcc, 0, v187, vcc
	v_add_co_u32_e32 v198, vcc, s8, v186
	s_mov_b32 s8, 0x1c000
	s_nop 0
	v_addc_co_u32_e32 v199, vcc, 0, v187, vcc
	v_add_co_u32_e32 v232, vcc, s8, v186
	s_mov_b32 s8, 0x1e000
	s_nop 0
	v_addc_co_u32_e32 v233, vcc, 0, v187, vcc
; #define LAS __attribute__((address_space(3)))
; __device__ __forceinline__ int crow(int r, int hi) { return (r & 3) + 8 * (r >> 2) + 4 * hi; }
; __device__ __forceinline__ void stage_store(const u32x4 (&v)[16], LAS unsigned char* lds, int wave, int lane) {
;     const int c = lane & 31, r0 = wave * 2 + (lane >> 5);
; #pragma unroll
;     for (int i = 0; i < 16; ++i) { const int r = r0 + 16 * i; *(LAS u32x4*)(lds + r * 512 + ((c ^ (r & 31)) << 4)) = v[i]; }
; }
; __device__ __forceinline__ void unit(const bf16_t* proj, const bf16_t* mk, const bf16_t* mvt, bf16_t* Y3, int un, LAS unsigned char* lds) {
;     ...
;     stage_load(st, mvt + (size_t)((b * 4 + h) * 256) * 256, 256, wave, lane);
;     asm volatile("" ::: "memory");
;     __syncthreads();
;     stage_store(st, lds, wave, lane);
;     __syncthreads();
;     ...
;             for (int r = 0; r < 16; ++r) zz[dbi * 16 + r] = *(const unsigned*)(proj + (size_t)(bt0 + att::crow(r, hi)) * NC + C_ZM + h * 256 + (hf * 2 + dbi) * 32 + (r32 & ~1));
	global_load_dwordx4 v[182:185], v[182:183], off
	v_add_co_u32_e32 v236, vcc, s8, v186
	global_load_dwordx4 v[190:193], v[190:191], off
	s_nop 0
	v_addc_co_u32_e32 v237, vcc, 0, v187, vcc
	global_load_dwordx4 v[186:189], v[188:189], off
	v_add_f32_e32 v2, v136, v134
	global_load_dwordx4 v[246:249], v[198:199], off
	v_add_f32_e32 v2, v17, v2
	global_load_dwordx4 v[232:235], v[232:233], off
	v_add_f32_e32 v2, v133, v2
	global_load_dwordx4 v[236:239], v[236:237], off
	v_add_f32_e32 v2, v15, v2
	v_add_f32_e32 v2, v19, v2
	v_add_f32_e32 v2, v14, v2
	v_add_f32_e32 v2, v18, v2
	v_add_f32_e32 v2, v6, v2
	v_add_f32_e32 v2, v7, v2
	v_add_f32_e32 v2, v8, v2
	v_add_f32_e32 v2, v9, v2
	v_add_f32_e32 v2, v10, v2
	v_add_f32_e32 v2, v11, v2
	v_add_f32_e32 v2, v12, v2
	v_add_f32_e32 v2, v13, v2
	v_add_f32_e32 v2, v16, v2
	v_add_f32_e32 v2, v132, v2
	v_add_f32_e32 v2, v135, v2
	v_add_f32_e32 v2, v137, v2
	v_add_f32_e32 v2, v138, v2
	v_add_f32_e32 v2, v139, v2
	v_add_f32_e32 v2, v140, v2
	v_add_f32_e32 v2, v141, v2
	v_add_f32_e32 v2, v142, v2
	v_add_f32_e32 v2, v84, v2
	v_add_f32_e32 v2, v143, v2
	v_add_f32_e32 v2, v86, v2
	v_add_f32_e32 v2, v144, v2
	v_add_f32_e32 v2, v88, v2
	v_add_f32_e32 v2, v145, v2
	v_add_f32_e32 v2, v90, v2
	v_add_f32_e32 v2, v146, v2
	v_add_f32_e32 v2, v92, v2
	v_add_f32_e32 v2, v147, v2
	v_add_f32_e32 v2, v94, v2
	v_add_f32_e32 v2, v149, v2
	v_add_f32_e32 v2, v96, v2
	v_add_f32_e32 v2, v150, v2
	v_add_f32_e32 v2, v98, v2
	v_add_f32_e32 v2, v151, v2
	v_add_f32_e32 v2, v100, v2
	v_add_f32_e32 v2, v152, v2
	v_add_f32_e32 v2, v102, v2
	v_add_f32_e32 v2, v153, v2
	v_add_f32_e32 v2, v104, v2
	v_add_f32_e32 v2, v154, v2
	v_add_f32_e32 v2, v106, v2
	v_add_f32_e32 v2, v155, v2
	v_add_f32_e32 v2, v108, v2
	v_add_f32_e32 v2, v156, v2
	v_add_f32_e32 v2, v110, v2
	v_lshlrev_b32_e32 v156, 2, v200
	v_add_f32_e32 v2, v157, v2
	v_or_b32_e32 v84, s1, v156
	v_add_f32_e32 v149, v112, v2
	v_and_b32_e32 v2, 30, v220
	v_mad_i64_i32 v[6:7], s[8:9], v84, s11, v[196:197]
	v_lshl_add_u64 v[6:7], v[6:7], 0, s[2:3]
	v_lshlrev_b32_e32 v2, 1, v2
	v_or_b32_e32 v86, 1, v84
	v_lshl_add_u64 v[6:7], v[6:7], 0, v[2:3]
	v_mad_i64_i32 v[8:9], s[8:9], v86, s11, v[196:197]
	s_barrier
	s_waitcnt vmcnt(15)
	ds_write_b128 v222, v[116:119]
	s_waitcnt vmcnt(14)
	ds_write_b128 v224, v[120:123]
	s_waitcnt vmcnt(13)
	ds_write_b128 v222, v[124:127] offset:16384
	s_waitcnt vmcnt(12)
	ds_write_b128 v226, v[128:131]
	s_waitcnt vmcnt(11)
	ds_write_b128 v222, v[158:161] offset:32768
	s_waitcnt vmcnt(10)
	ds_write_b128 v228, v[162:165]
	s_waitcnt vmcnt(9)
	ds_write_b128 v222, v[166:169] offset:49152
	s_waitcnt vmcnt(8)
	ds_write_b128 v230, v[170:173]
	s_waitcnt vmcnt(7)
	ds_write_b128 v223, v[174:177]
	s_waitcnt vmcnt(6)
	ds_write_b128 v240, v[178:181]
	s_waitcnt vmcnt(5)
	ds_write_b128 v245, v[182:185]
	s_waitcnt vmcnt(3)
	ds_write_b128 v250, v[186:189]
	ds_write_b128 v251, v[190:193]
	s_waitcnt vmcnt(2)
	ds_write_b128 v194, v[246:249]
	s_waitcnt vmcnt(1)
	ds_write_b128 v195, v[232:235]
	s_waitcnt vmcnt(0)
	ds_write_b128 v244, v[236:239]
	v_lshl_add_u64 v[116:117], v[6:7], 0, s[12:13]
	v_add_co_u32_e32 v6, vcc, s10, v6
	v_lshl_add_u64 v[8:9], v[8:9], 0, s[2:3]
	v_or_b32_e32 v88, 2, v84
	v_addc_co_u32_e32 v7, vcc, 0, v7, vcc
	v_lshl_add_u64 v[8:9], v[8:9], 0, v[2:3]
	v_mad_i64_i32 v[10:11], s[8:9], v88, s11, v[196:197]
	v_lshl_add_u64 v[118:119], v[8:9], 0, s[12:13]
	v_add_co_u32_e32 v8, vcc, s10, v8
	v_lshl_add_u64 v[10:11], v[10:11], 0, s[2:3]
	v_or_b32_e32 v90, 3, v84
	v_addc_co_u32_e32 v9, vcc, 0, v9, vcc
	v_lshl_add_u64 v[10:11], v[10:11], 0, v[2:3]
	v_mad_i64_i32 v[12:13], s[8:9], v90, s11, v[196:197]
	v_lshl_add_u64 v[120:121], v[10:11], 0, s[12:13]
	v_add_co_u32_e32 v10, vcc, s10, v10
	v_lshl_add_u64 v[12:13], v[12:13], 0, s[2:3]
	v_or_b32_e32 v92, 8, v84
	v_addc_co_u32_e32 v11, vcc, 0, v11, vcc
	v_lshl_add_u64 v[12:13], v[12:13], 0, v[2:3]
	v_mad_i64_i32 v[14:15], s[8:9], v92, s11, v[196:197]
	v_lshl_add_u64 v[124:125], v[12:13], 0, s[12:13]
	v_add_co_u32_e32 v12, vcc, s10, v12
	v_lshl_add_u64 v[14:15], v[14:15], 0, s[2:3]
	v_or_b32_e32 v94, 9, v84
	v_addc_co_u32_e32 v13, vcc, 0, v13, vcc
	v_lshl_add_u64 v[14:15], v[14:15], 0, v[2:3]
	v_mad_i64_i32 v[16:17], s[8:9], v94, s11, v[196:197]
	v_lshl_add_u64 v[122:123], v[14:15], 0, s[12:13]
	v_add_co_u32_e32 v14, vcc, s10, v14
	v_lshl_add_u64 v[16:17], v[16:17], 0, s[2:3]
	v_or_b32_e32 v96, 10, v84
	v_addc_co_u32_e32 v15, vcc, 0, v15, vcc
	v_lshl_add_u64 v[16:17], v[16:17], 0, v[2:3]
	v_mad_i64_i32 v[18:19], s[8:9], v96, s11, v[196:197]
	v_lshl_add_u64 v[126:127], v[16:17], 0, s[12:13]
	v_add_co_u32_e32 v16, vcc, s10, v16
	v_lshl_add_u64 v[18:19], v[18:19], 0, s[2:3]
	v_or_b32_e32 v98, 11, v84
	v_addc_co_u32_e32 v17, vcc, 0, v17, vcc
	v_lshl_add_u64 v[18:19], v[18:19], 0, v[2:3]
	v_mad_i64_i32 v[130:131], s[8:9], v98, s11, v[196:197]
	v_lshl_add_u64 v[128:129], v[18:19], 0, s[12:13]
	v_add_co_u32_e32 v18, vcc, s10, v18
	v_lshl_add_u64 v[130:131], v[130:131], 0, s[2:3]
	s_nop 0
	v_addc_co_u32_e32 v19, vcc, 0, v19, vcc
	v_lshl_add_u64 v[132:133], v[130:131], 0, v[2:3]
	v_lshl_add_u64 v[130:131], v[132:133], 0, s[12:13]
	v_add_co_u32_e32 v132, vcc, s10, v132
	v_or_b32_e32 v100, 16, v84
	s_waitcnt lgkmcnt(0)
	s_barrier
; __device__ __forceinline__ int crow(int r, int hi) { return (r & 3) + 8 * (r >> 2) + 4 * hi; }
; __device__ __forceinline__ void unit(const bf16_t* proj, const bf16_t* mk, const bf16_t* mvt, bf16_t* Y3, int un, LAS unsigned char* lds) {
;     ...
;     for (int hf = 0; hf < 4; ++hf) { unsigned zz[32];
; #pragma unroll
;         for (int dbi = 0; dbi < 2; ++dbi)
; #pragma unroll
;             for (int r = 0; r < 16; ++r) zz[dbi * 16 + r] = *(const unsigned*)(proj + (size_t)(bt0 + att::crow(r, hi)) * NC + C_ZM + h * 256 + (hf * 2 + dbi) * 32 + (r32 & ~1));
;         asm volatile("" ::: "memory");
; #pragma unroll
;         for (int dbi = 0; dbi < 2; ++dbi) { const int db = hf * 2 + dbi; att::f32x16 o = att::f32x16{};
; #pragma unroll
;             for (int q4 = 0; q4 < 4; ++q4) { att::bf16x8 vf[4]; int rv = r32; asm volatile("" : "+v"(rv));
; #pragma unroll
;                 for (int i = 0; i < 4; ++i) vf[i] = frag(lds, db * 32 + rv, 2 * (q4 * 4 + i) + hi);
;                 asm volatile("" ::: "memory");
; #pragma unroll
;                 for (int i = 0; i < 4; ++i) o = __builtin_amdgcn_mfma_f32_32x32x16_bf16(pa[q4 * 4 + i], vf[i], o, 0, 0, 0); }
	v_addc_co_u32_e32 v133, vcc, 0, v133, vcc
	global_load_dword v224, v[6:7], off nt
	global_load_dword v223, v[8:9], off nt
	global_load_dword v193, v[10:11], off nt
	global_load_dword v192, v[12:13], off nt
	global_load_dword v222, v[14:15], off nt
	global_load_dword v199, v[16:17], off nt
	global_load_dword v198, v[18:19], off nt
	global_load_dword v191, v[132:133], off nt
	v_mad_i64_i32 v[6:7], s[8:9], v100, s11, v[196:197]
	v_lshl_add_u64 v[6:7], v[6:7], 0, s[2:3]
	v_or_b32_e32 v102, 17, v84
	v_lshl_add_u64 v[6:7], v[6:7], 0, v[2:3]
	v_mad_i64_i32 v[8:9], s[8:9], v102, s11, v[196:197]
	v_lshl_add_u64 v[132:133], v[6:7], 0, s[12:13]
	v_add_co_u32_e32 v6, vcc, s10, v6
	v_lshl_add_u64 v[8:9], v[8:9], 0, s[2:3]
	v_or_b32_e32 v104, 18, v84
	v_addc_co_u32_e32 v7, vcc, 0, v7, vcc
	v_lshl_add_u64 v[8:9], v[8:9], 0, v[2:3]
	v_mad_i64_i32 v[10:11], s[8:9], v104, s11, v[196:197]
	v_lshl_add_u64 v[134:135], v[8:9], 0, s[12:13]
	v_add_co_u32_e32 v8, vcc, s10, v8
	v_lshl_add_u64 v[10:11], v[10:11], 0, s[2:3]
	v_or_b32_e32 v106, 19, v84
	v_addc_co_u32_e32 v9, vcc, 0, v9, vcc
	v_lshl_add_u64 v[10:11], v[10:11], 0, v[2:3]
	v_mad_i64_i32 v[12:13], s[8:9], v106, s11, v[196:197]
	v_lshl_add_u64 v[136:137], v[10:11], 0, s[12:13]
	v_add_co_u32_e32 v10, vcc, s10, v10
	v_lshl_add_u64 v[12:13], v[12:13], 0, s[2:3]
	v_or_b32_e32 v108, 24, v84
	v_addc_co_u32_e32 v11, vcc, 0, v11, vcc
	v_lshl_add_u64 v[12:13], v[12:13], 0, v[2:3]
	v_mad_i64_i32 v[14:15], s[8:9], v108, s11, v[196:197]
	v_lshl_add_u64 v[140:141], v[12:13], 0, s[12:13]
	v_add_co_u32_e32 v12, vcc, s10, v12
	v_lshl_add_u64 v[14:15], v[14:15], 0, s[2:3]
	v_or_b32_e32 v110, 25, v84
	v_addc_co_u32_e32 v13, vcc, 0, v13, vcc
	v_lshl_add_u64 v[14:15], v[14:15], 0, v[2:3]
	v_mad_i64_i32 v[16:17], s[8:9], v110, s11, v[196:197]
	v_lshl_add_u64 v[138:139], v[14:15], 0, s[12:13]
	v_add_co_u32_e32 v14, vcc, s10, v14
	v_lshl_add_u64 v[16:17], v[16:17], 0, s[2:3]
	v_or_b32_e32 v112, 26, v84
	v_addc_co_u32_e32 v15, vcc, 0, v15, vcc
	v_lshl_add_u64 v[16:17], v[16:17], 0, v[2:3]
	v_mad_i64_i32 v[18:19], s[8:9], v112, s11, v[196:197]
	v_lshl_add_u64 v[142:143], v[16:17], 0, s[12:13]
	v_add_co_u32_e32 v16, vcc, s10, v16
	v_lshl_add_u64 v[18:19], v[18:19], 0, s[2:3]
	v_or_b32_e32 v114, 27, v84
	v_addc_co_u32_e32 v17, vcc, 0, v17, vcc
	v_lshl_add_u64 v[18:19], v[18:19], 0, v[2:3]
	v_mad_i64_i32 v[146:147], s[8:9], v114, s11, v[196:197]
	v_lshl_add_u64 v[144:145], v[18:19], 0, s[12:13]
	v_add_co_u32_e32 v18, vcc, s10, v18
	v_lshl_add_u64 v[146:147], v[146:147], 0, s[2:3]
	s_nop 0
	v_addc_co_u32_e32 v19, vcc, 0, v19, vcc
	v_lshl_add_u64 v[150:151], v[146:147], 0, v[2:3]
	v_lshl_add_u64 v[146:147], v[150:151], 0, s[12:13]
	v_add_co_u32_e32 v150, vcc, s10, v150
	v_mov_b32_e32 v2, v1
	s_nop 0
	v_addc_co_u32_e32 v151, vcc, 0, v151, vcc
	global_load_dword v197, v[6:7], off nt
	global_load_dword v196, v[8:9], off nt
	global_load_dword v190, v[10:11], off nt
	global_load_dword v189, v[12:13], off nt
	global_load_dword v188, v[14:15], off nt
	global_load_dword v187, v[16:17], off nt
	global_load_dword v186, v[18:19], off nt
	global_load_dword v185, v[150:151], off nt
	global_load_dword v184, v[116:117], off offset:64 nt
	global_load_dword v183, v[118:119], off offset:64 nt
	global_load_dword v182, v[120:121], off offset:64 nt
	global_load_dword v181, v[124:125], off offset:64 nt
	global_load_dword v180, v[122:123], off offset:64 nt
	global_load_dword v179, v[126:127], off offset:64 nt
	global_load_dword v178, v[128:129], off offset:64 nt
	global_load_dword v177, v[130:131], off offset:64 nt
	global_load_dword v176, v[132:133], off offset:64 nt
	global_load_dword v175, v[134:135], off offset:64 nt
	global_load_dword v174, v[136:137], off offset:64 nt
	global_load_dword v173, v[140:141], off offset:64 nt
	global_load_dword v172, v[138:139], off offset:64 nt
	global_load_dword v171, v[142:143], off offset:64 nt
	global_load_dword v170, v[144:145], off offset:64 nt
	global_load_dword v169, v[146:147], off offset:64 nt
	v_add_f32_e32 v4, v4, v149
	v_lshl_add_u32 v154, v2, 9, 0
	v_bitop3_b32 v6, v2, v200, 31 bitop3:0x6c
	v_lshl_add_u32 v6, v6, 4, v154
	ds_read_b128 v[6:9], v6
	v_add_f32_e32 v149, v5, v4
	v_bitop3_b32 v4, v2, v209, 31 bitop3:0x6c
	v_lshl_add_u32 v150, v4, 4, v154
	ds_read_b128 v[150:153], v150
	s_waitcnt lgkmcnt(1)
	v_mfma_f32_32x32x16_bf16 v[4:19], v[28:31], v[6:9], 0
	v_add_f32_e32 v97, v97, v149
	v_add_f32_e32 v97, v101, v97
	v_add_f32_e32 v97, v105, v97
	v_add_f32_e32 v97, v109, v97
	v_bitop3_b32 v101, v2, v218, 31 bitop3:0x6c
	v_add_f32_e32 v97, v113, v97
	v_lshl_add_u32 v101, v101, 4, v154
	s_waitcnt lgkmcnt(0)
	v_mfma_f32_32x32x16_bf16 v[4:19], v[20:23], v[150:153], v[4:19]
	v_add_f32_e32 v97, v148, v97
	ds_read_b128 v[148:151], v101
	v_bitop3_b32 v2, v2, v214, 31 bitop3:0x6c
	v_lshl_add_u32 v2, v2, 4, v154
	v_add_f32_e32 v97, v111, v97
	v_add_f32_e32 v97, v115, v97
	s_waitcnt lgkmcnt(0)
	v_mfma_f32_32x32x16_bf16 v[4:19], v[36:39], v[148:151], v[4:19]
	ds_read_b128 v[148:151], v2
	v_add_f32_e32 v2, v89, v97
	v_mov_b32_e32 v89, v1
	v_add_f32_e32 v2, v93, v2
	v_add_f32_e32 v2, v99, v2
	s_waitcnt lgkmcnt(0)
; __device__ __forceinline__ float bflo(unsigned w) { return __uint_as_float(w << 16); }
; __device__ __forceinline__ float bfhi(unsigned w) { return __uint_as_float(w & 0xffff0000u); }
; __device__ __forceinline__ unsigned pk2(float lo, float hi) { return f2bf(lo) | (f2bf(hi) << 16); }
; __device__ __forceinline__ int crow(int r, int hi) { return (r & 3) + 8 * (r >> 2) + 4 * hi; }
; __device__ __forceinline__ void unit(const bf16_t* proj, const bf16_t* mk, const bf16_t* mvt, bf16_t* Y3, int un, LAS unsigned char* lds) {
;     ...
;     const float linv = 1.0f / l;
;     ...
;     float rli[16];
; #pragma unroll
;     for (int r = 0; r < 16; ++r) rli[r] = __shfl(linv, att::crow(r, hi));
;     ...
;         for (int dbi = 0; dbi < 2; ++dbi) { const int db = hf * 2 + dbi; att::f32x16 o = att::f32x16{};
; #pragma unroll
;             for (int q4 = 0; q4 < 4; ++q4) { att::bf16x8 vf[4]; int rv = r32; asm volatile("" : "+v"(rv));
; #pragma unroll
;                 for (int i = 0; i < 4; ++i) vf[i] = frag(lds, db * 32 + rv, 2 * (q4 * 4 + i) + hi);
;                 asm volatile("" ::: "memory");
; #pragma unroll
;                 for (int i = 0; i < 4; ++i) o = __builtin_amdgcn_mfma_f32_32x32x16_bf16(pa[q4 * 4 + i], vf[i], o, 0, 0, 0); }
; #pragma unroll
;             for (int r = 0; r < 16; ++r) { const int bt = bt0 + att::crow(r, hi), col = h * 256 + db * 32 + r32; const float val = o[r] * rli[r], vn = __shfl_xor(val, 1);
;                 if ((r32 & 1) == 0) *(unsigned*)(Y3 + (size_t)bt * YS + col) = pk2(val * bflo(zz[dbi * 16 + r]), vn * bfhi(zz[dbi * 16 + r])); } } }
	v_mfma_f32_32x32x16_bf16 v[4:19], v[24:27], v[148:151], v[4:19]
	v_lshl_add_u32 v93, v89, 9, 0
	v_bitop3_b32 v97, v89, v217, 31 bitop3:0x6c
	v_lshl_add_u32 v97, v97, 4, v93
	ds_read_b128 v[148:151], v97
	v_add_f32_e32 v2, v103, v2
	v_add_f32_e32 v2, v107, v2
	v_add_f32_e32 v2, v91, v2
	s_waitcnt lgkmcnt(0)
	v_mfma_f32_32x32x16_bf16 v[4:19], v[44:47], v[148:151], v[4:19]
	v_bitop3_b32 v91, v89, v206, 31 bitop3:0x6c
	v_lshl_add_u32 v91, v91, 4, v93
	ds_read_b128 v[148:151], v91
	v_add_f32_e32 v2, v95, v2
	v_add_f32_e32 v2, v85, v2
	v_add_f32_e32 v2, v87, v2
	v_mov_b32_e32 v85, v2
	s_nop 1
	v_permlane32_swap_b32_e32 v2, v85
	s_waitcnt lgkmcnt(0)
	v_mfma_f32_32x32x16_bf16 v[4:19], v[32:35], v[148:151], v[4:19]
	v_add_f32_e32 v2, v2, v85
	v_bitop3_b32 v85, v89, v216, 31 bitop3:0x6c
	v_lshl_add_u32 v85, v85, 4, v93
	ds_read_b128 v[148:151], v85
	v_bitop3_b32 v87, v89, v211, 31 bitop3:0x6c
	v_lshl_add_u32 v87, v87, 4, v93
	v_mov_b32_e32 v91, v1
	s_waitcnt lgkmcnt(0)
	v_mfma_f32_32x32x16_bf16 v[4:19], v[52:55], v[148:151], v[4:19]
	ds_read_b128 v[148:151], v87
	v_div_scale_f32 v85, s[8:9], v2, v2, 1.0
	v_lshl_add_u32 v93, v91, 9, 0
	v_bitop3_b32 v95, v91, v215, 31 bitop3:0x6c
	s_waitcnt lgkmcnt(0)
	v_mfma_f32_32x32x16_bf16 v[4:19], v[40:43], v[148:151], v[4:19]
	v_lshl_add_u32 v95, v95, 4, v93
	ds_read_b128 v[148:151], v95
	v_rcp_f32_e32 v89, v85
	v_bitop3_b32 v97, v91, v202, 31 bitop3:0x6c
	v_lshl_add_u32 v97, v97, 4, v93
	ds_read_b128 v[152:155], v97
	v_fma_f32 v87, -v85, v89, 1.0
	s_waitcnt lgkmcnt(1)
	v_mfma_f32_32x32x16_bf16 v[4:19], v[60:63], v[148:151], v[4:19]
	v_fmac_f32_e32 v89, v87, v89
	v_div_scale_f32 v87, vcc, 1.0, v2, 1.0
	v_mul_f32_e32 v95, v87, v89
	v_fma_f32 v97, -v85, v95, v87
	v_fmac_f32_e32 v95, v97, v89
	v_fma_f32 v85, -v85, v95, v87
	v_div_fmas_f32 v85, v85, v89, v95
	s_waitcnt lgkmcnt(0)
	v_mfma_f32_32x32x16_bf16 v[4:19], v[48:51], v[152:155], v[4:19]
	v_div_fixup_f32 v2, v85, v2, 1.0
	v_bitop3_b32 v85, v91, v213, 31 bitop3:0x6c
	v_lshl_add_u32 v85, v85, 4, v93
	ds_read_b128 v[148:151], v85
	v_bitop3_b32 v89, v91, v208, 31 bitop3:0x6c
	v_lshl_add_u32 v89, v89, 4, v93
	ds_read_b128 v[152:155], v89
	s_waitcnt lgkmcnt(1)
	v_mfma_f32_32x32x16_bf16 v[4:19], v[68:71], v[148:151], v[4:19]
	v_mov_b32_e32 v89, v1
	v_and_b32_e32 v87, 64, v229
	v_lshl_add_u32 v91, v89, 9, 0
	v_bitop3_b32 v93, v89, v212, 31 bitop3:0x6c
	v_lshl_add_u32 v93, v93, 4, v91
	s_waitcnt lgkmcnt(0)
	v_mfma_f32_32x32x16_bf16 v[4:19], v[56:59], v[152:155], v[4:19]
	ds_read_b128 v[148:151], v93
	v_bitop3_b32 v93, v89, v201, 31 bitop3:0x6c
	v_lshl_add_u32 v93, v93, 4, v91
	ds_read_b128 v[152:155], v93
	v_bitop3_b32 v93, v89, v210, 31 bitop3:0x6c
	v_lshl_add_u32 v93, v93, 4, v91
	v_bitop3_b32 v89, v89, v204, 31 bitop3:0x6c
	s_waitcnt lgkmcnt(1)
	v_mfma_f32_32x32x16_bf16 v[4:19], v[72:75], v[148:151], v[4:19]
	ds_read_b128 v[148:151], v93
	v_lshl_add_u32 v89, v89, 4, v91
	ds_read_b128 v[232:235], v89
	v_or_b32_e32 v85, v87, v156
	v_lshlrev_b32_e32 v85, 2, v85
	ds_bpermute_b32 v168, v85, v2
	ds_bpermute_b32 v167, v85, v2 offset:4
	s_waitcnt lgkmcnt(4)
	v_mfma_f32_32x32x16_bf16 v[4:19], v[64:67], v[152:155], v[4:19]
	ds_bpermute_b32 v166, v85, v2 offset:8
	ds_bpermute_b32 v165, v85, v2 offset:12
	ds_bpermute_b32 v164, v85, v2 offset:32
	ds_bpermute_b32 v163, v85, v2 offset:36
	ds_bpermute_b32 v162, v85, v2 offset:40
	ds_bpermute_b32 v161, v85, v2 offset:44
	ds_bpermute_b32 v160, v85, v2 offset:64
	s_waitcnt lgkmcnt(10)
	v_mfma_f32_32x32x16_bf16 v[4:19], v[76:79], v[148:151], v[4:19]
	ds_bpermute_b32 v159, v85, v2 offset:68
	ds_bpermute_b32 v158, v85, v2 offset:72
	ds_bpermute_b32 v157, v85, v2 offset:76
	ds_bpermute_b32 v156, v85, v2 offset:96
	ds_bpermute_b32 v155, v85, v2 offset:100
	ds_bpermute_b32 v154, v85, v2 offset:104
	ds_bpermute_b32 v152, v85, v2 offset:108
	s_waitcnt lgkmcnt(14)
	v_mfma_f32_32x32x16_bf16 v[4:19], v[80:83], v[232:235], v[4:19]
	v_and_b32_e32 v2, 1, v220
	v_xor_b32_e32 v89, 1, v229
	v_add_u32_e32 v87, 64, v87
	v_cmp_eq_u32_e32 vcc, 0, v2
	v_or_b32_e32 v2, s0, v1
	v_cmp_lt_i32_e64 s[0:1], v89, v87
	v_ashrrev_i32_e32 v85, 31, v84
	s_nop 4
	v_mul_f32_e32 v150, v4, v168
	v_cndmask_b32_e64 v87, v229, v89, s[0:1]
	v_lshlrev_b32_e32 v153, 2, v87
	ds_bpermute_b32 v151, v153, v150
	v_readlane_b32 s0, v254, 35
	v_lshlrev_b32_e32 v2, 1, v2
	v_readlane_b32 s1, v254, 36
	v_lshlrev_b64 v[84:85], 13, v[84:85]
	s_nop 0
	v_lshl_add_u64 v[148:149], s[0:1], 0, v[2:3]
	v_lshl_add_u64 v[84:85], v[148:149], 0, v[84:85]
	s_and_saveexec_b64 s[0:1], vcc
	s_cbranch_execz .LBB0_1120
	s_waitcnt vmcnt(31)
	v_lshlrev_b32_e32 v194, 16, v224
	v_and_b32_e32 v195, 0xffff0000, v224
	s_waitcnt lgkmcnt(0)
	v_pk_mul_f32 v[150:151], v[150:151], v[194:195]
	s_nop 0
	v_and_b32_sdwa v4, v150, v227 dst_sel:DWORD dst_unused:UNUSED_PAD src0_sel:WORD_1 src1_sel:DWORD
	v_and_b32_sdwa v2, v151, v227 dst_sel:DWORD dst_unused:UNUSED_PAD src0_sel:WORD_1 src1_sel:DWORD
	v_add3_u32 v4, v150, v4, s97
	v_add3_u32 v2, v151, v2, s97
	v_lshrrev_b32_e32 v4, 16, v4
	v_and_or_b32 v2, v2, s85, v4
	global_store_dword v[84:85], v2, off

; __device__ __forceinline__ float bflo(unsigned w) { return __uint_as_float(w << 16); }
; __device__ __forceinline__ float bfhi(unsigned w) { return __uint_as_float(w & 0xffff0000u); }
; __device__ __forceinline__ unsigned pk2(float lo, float hi) { return f2bf(lo) | (f2bf(hi) << 16); }
; __device__ __forceinline__ int crow(int r, int hi) { return (r & 3) + 8 * (r >> 2) + 4 * hi; }
; __device__ __forceinline__ void unit(const bf16_t* proj, const bf16_t* mk, const bf16_t* mvt, bf16_t* Y3, int un, LAS unsigned char* lds) {
;     ...
;     for (int hf = 0; hf < 4; ++hf) { unsigned zz[32];
; #pragma unroll
;         for (int dbi = 0; dbi < 2; ++dbi)
; #pragma unroll
;             for (int r = 0; r < 16; ++r) zz[dbi * 16 + r] = *(const unsigned*)(proj + (size_t)(bt0 + att::crow(r, hi)) * NC + C_ZM + h * 256 + (hf * 2 + dbi) * 32 + (r32 & ~1));
;         asm volatile("" ::: "memory");
; #pragma unroll
;         for (int dbi = 0; dbi < 2; ++dbi) { const int db = hf * 2 + dbi; att::f32x16 o = att::f32x16{};
; #pragma unroll
;             for (int q4 = 0; q4 < 4; ++q4) { att::bf16x8 vf[4]; int rv = r32; asm volatile("" : "+v"(rv));
; #pragma unroll
;                 for (int i = 0; i < 4; ++i) vf[i] = frag(lds, db * 32 + rv, 2 * (q4 * 4 + i) + hi);
;                 asm volatile("" ::: "memory");
; #pragma unroll
;                 for (int i = 0; i < 4; ++i) o = __builtin_amdgcn_mfma_f32_32x32x16_bf16(pa[q4 * 4 + i], vf[i], o, 0, 0, 0); }
; #pragma unroll
;             for (int r = 0; r < 16; ++r) { const int bt = bt0 + att::crow(r, hi), col = h * 256 + db * 32 + r32; const float val = o[r] * rli[r], vn = __shfl_xor(val, 1);
;                 if ((r32 & 1) == 0) *(unsigned*)(Y3 + (size_t)bt * YS + col) = pk2(val * bflo(zz[dbi * 16 + r]), vn * bfhi(zz[dbi * 16 + r])); } } }
.LBB0_1182:
	s_or_b64 exec, exec, s[0:1]
	v_mov_b32_e32 v148, v1
	global_load_dword v199, v[116:117], off offset:128 nt
	global_load_dword v198, v[118:119], off offset:128 nt
	global_load_dword v197, v[120:121], off offset:128 nt
	global_load_dword v196, v[124:125], off offset:128 nt
	global_load_dword v178, v[124:125], off offset:192 nt
	global_load_dword v179, v[120:121], off offset:192 nt
	global_load_dword v180, v[118:119], off offset:192 nt
	global_load_dword v181, v[116:117], off offset:192 nt
	global_load_dword v193, v[122:123], off offset:128 nt
	global_load_dword v192, v[126:127], off offset:128 nt
	global_load_dword v191, v[128:129], off offset:128 nt
	global_load_dword v190, v[130:131], off offset:128 nt
	global_load_dword v174, v[130:131], off offset:192 nt
	global_load_dword v175, v[128:129], off offset:192 nt
	global_load_dword v176, v[126:127], off offset:192 nt
	global_load_dword v177, v[122:123], off offset:192 nt
	global_load_dword v189, v[132:133], off offset:128 nt
	global_load_dword v188, v[134:135], off offset:128 nt
	global_load_dword v187, v[136:137], off offset:128 nt
	global_load_dword v186, v[140:141], off offset:128 nt
	global_load_dword v170, v[140:141], off offset:192 nt
	global_load_dword v171, v[136:137], off offset:192 nt
	global_load_dword v172, v[134:135], off offset:192 nt
	global_load_dword v173, v[132:133], off offset:192 nt
	global_load_dword v185, v[138:139], off offset:128 nt
	global_load_dword v184, v[142:143], off offset:128 nt
	global_load_dword v183, v[144:145], off offset:128 nt
	global_load_dword v182, v[146:147], off offset:128 nt
	global_load_dword v2, v[146:147], off offset:192 nt
	global_load_dword v150, v[144:145], off offset:192 nt
	global_load_dword v151, v[142:143], off offset:192 nt
	global_load_dword v169, v[138:139], off offset:192 nt
	s_nop 0
	v_lshl_add_u32 v149, v148, 9, 0
	s_waitcnt lgkmcnt(0)
	v_bitop3_b32 v4, v148, v200, 31 bitop3:0x6c
	v_lshl_add_u32 v4, v4, 4, v149
	ds_read_b128 v[4:7], v4 offset:32768
	v_bitop3_b32 v194, v148, v209, 31 bitop3:0x6c
	v_lshl_add_u32 v194, v194, 4, v149
	ds_read_b128 v[232:235], v194 offset:32768
	s_waitcnt lgkmcnt(1)
	v_mfma_f32_32x32x16_bf16 v[4:19], v[28:31], v[4:7], 0
	v_bitop3_b32 v194, v148, v218, 31 bitop3:0x6c
	v_lshl_add_u32 v194, v194, 4, v149
	v_bitop3_b32 v148, v148, v214, 31 bitop3:0x6c
	v_lshl_add_u32 v148, v148, 4, v149
	s_waitcnt lgkmcnt(0)
	v_mfma_f32_32x32x16_bf16 v[4:19], v[20:23], v[232:235], v[4:19]
	ds_read_b128 v[232:235], v194 offset:32768
	s_waitcnt lgkmcnt(0)
	v_mfma_f32_32x32x16_bf16 v[4:19], v[36:39], v[232:235], v[4:19]
	ds_read_b128 v[232:235], v148 offset:32768
	v_mov_b32_e32 v148, v1
	s_nop 0
	v_lshl_add_u32 v149, v148, 9, 0
	v_bitop3_b32 v194, v148, v217, 31 bitop3:0x6c
	s_waitcnt lgkmcnt(0)
	v_mfma_f32_32x32x16_bf16 v[4:19], v[24:27], v[232:235], v[4:19]
	v_lshl_add_u32 v194, v194, 4, v149
	ds_read_b128 v[232:235], v194 offset:32768
	v_bitop3_b32 v194, v148, v206, 31 bitop3:0x6c
	v_lshl_add_u32 v194, v194, 4, v149
	s_waitcnt lgkmcnt(0)
	v_mfma_f32_32x32x16_bf16 v[4:19], v[44:47], v[232:235], v[4:19]
	ds_read_b128 v[232:235], v194 offset:32768
	v_bitop3_b32 v194, v148, v216, 31 bitop3:0x6c
	v_lshl_add_u32 v194, v194, 4, v149
	v_bitop3_b32 v148, v148, v211, 31 bitop3:0x6c
	v_lshl_add_u32 v148, v148, 4, v149
	s_waitcnt lgkmcnt(0)
	v_mfma_f32_32x32x16_bf16 v[4:19], v[32:35], v[232:235], v[4:19]
	ds_read_b128 v[232:235], v194 offset:32768
	s_waitcnt lgkmcnt(0)
	v_mfma_f32_32x32x16_bf16 v[4:19], v[52:55], v[232:235], v[4:19]
	ds_read_b128 v[232:235], v148 offset:32768
	v_mov_b32_e32 v148, v1
	s_nop 0
	v_lshl_add_u32 v149, v148, 9, 0
	v_bitop3_b32 v194, v148, v215, 31 bitop3:0x6c
	s_waitcnt lgkmcnt(0)
	v_mfma_f32_32x32x16_bf16 v[4:19], v[40:43], v[232:235], v[4:19]
	v_lshl_add_u32 v194, v194, 4, v149
	ds_read_b128 v[232:235], v194 offset:32768
	v_bitop3_b32 v194, v148, v202, 31 bitop3:0x6c
	v_lshl_add_u32 v194, v194, 4, v149
	s_waitcnt lgkmcnt(0)
	v_mfma_f32_32x32x16_bf16 v[4:19], v[60:63], v[232:235], v[4:19]
	ds_read_b128 v[232:235], v194 offset:32768
	v_bitop3_b32 v194, v148, v213, 31 bitop3:0x6c
	v_lshl_add_u32 v194, v194, 4, v149
	v_bitop3_b32 v148, v148, v208, 31 bitop3:0x6c
	v_lshl_add_u32 v148, v148, 4, v149
	s_waitcnt lgkmcnt(0)
	v_mfma_f32_32x32x16_bf16 v[4:19], v[48:51], v[232:235], v[4:19]
	ds_read_b128 v[232:235], v194 offset:32768
	s_waitcnt lgkmcnt(0)
	v_mfma_f32_32x32x16_bf16 v[4:19], v[68:71], v[232:235], v[4:19]
	ds_read_b128 v[232:235], v148 offset:32768
	v_mov_b32_e32 v148, v1
	s_nop 0
	v_lshl_add_u32 v149, v148, 9, 0
	v_bitop3_b32 v194, v148, v212, 31 bitop3:0x6c
	s_waitcnt lgkmcnt(0)
	v_mfma_f32_32x32x16_bf16 v[4:19], v[56:59], v[232:235], v[4:19]
	v_lshl_add_u32 v194, v194, 4, v149
	ds_read_b128 v[232:235], v194 offset:32768
	v_bitop3_b32 v194, v148, v201, 31 bitop3:0x6c
	v_lshl_add_u32 v194, v194, 4, v149
	s_waitcnt lgkmcnt(0)
	v_mfma_f32_32x32x16_bf16 v[4:19], v[72:75], v[232:235], v[4:19]
	ds_read_b128 v[232:235], v194 offset:32768
	v_bitop3_b32 v194, v148, v210, 31 bitop3:0x6c
	v_lshl_add_u32 v194, v194, 4, v149
	v_bitop3_b32 v148, v148, v204, 31 bitop3:0x6c
	v_lshl_add_u32 v148, v148, 4, v149
	s_waitcnt lgkmcnt(0)
	v_mfma_f32_32x32x16_bf16 v[4:19], v[64:67], v[232:235], v[4:19]
	ds_read_b128 v[232:235], v194 offset:32768
	s_waitcnt lgkmcnt(0)
	v_mfma_f32_32x32x16_bf16 v[4:19], v[76:79], v[232:235], v[4:19]
	ds_read_b128 v[232:235], v148 offset:32768
	s_waitcnt lgkmcnt(0)
	v_mfma_f32_32x32x16_bf16 v[4:19], v[80:83], v[232:235], v[4:19]
	s_nop 11
	v_mul_f32_e32 v148, v4, v168
	ds_bpermute_b32 v149, v153, v148
	s_and_saveexec_b64 s[0:1], vcc
	s_cbranch_execz .LBB0_1184
	s_waitcnt vmcnt(31)
	v_lshlrev_b32_e32 v194, 16, v199
	v_and_b32_e32 v195, 0xffff0000, v199
	s_waitcnt lgkmcnt(0)
	v_pk_mul_f32 v[148:149], v[148:149], v[194:195]
	s_nop 0
	v_and_b32_sdwa v194, v148, v227 dst_sel:DWORD dst_unused:UNUSED_PAD src0_sel:WORD_1 src1_sel:DWORD
	v_and_b32_sdwa v4, v149, v227 dst_sel:DWORD dst_unused:UNUSED_PAD src0_sel:WORD_1 src1_sel:DWORD
	v_add3_u32 v148, v148, v194, s97
	v_add3_u32 v4, v149, v4, s97
	v_lshrrev_b32_e32 v148, 16, v148
	v_and_or_b32 v4, v4, s85, v148
	global_store_dword v[84:85], v4, off offset:128

; __device__ __forceinline__ float bflo(unsigned w) { return __uint_as_float(w << 16); }
; __device__ __forceinline__ float bfhi(unsigned w) { return __uint_as_float(w & 0xffff0000u); }
; __device__ __forceinline__ unsigned pk2(float lo, float hi) { return f2bf(lo) | (f2bf(hi) << 16); }
; __device__ __forceinline__ int crow(int r, int hi) { return (r & 3) + 8 * (r >> 2) + 4 * hi; }
; __device__ __forceinline__ void unit(const bf16_t* proj, const bf16_t* mk, const bf16_t* mvt, bf16_t* Y3, int un, LAS unsigned char* lds) {
;     ...
;     for (int hf = 0; hf < 4; ++hf) { unsigned zz[32];
; #pragma unroll
;         for (int dbi = 0; dbi < 2; ++dbi)
; #pragma unroll
;             for (int r = 0; r < 16; ++r) zz[dbi * 16 + r] = *(const unsigned*)(proj + (size_t)(bt0 + att::crow(r, hi)) * NC + C_ZM + h * 256 + (hf * 2 + dbi) * 32 + (r32 & ~1));
;         asm volatile("" ::: "memory");
; #pragma unroll
;         for (int dbi = 0; dbi < 2; ++dbi) { const int db = hf * 2 + dbi; att::f32x16 o = att::f32x16{};
; #pragma unroll
;             for (int q4 = 0; q4 < 4; ++q4) { att::bf16x8 vf[4]; int rv = r32; asm volatile("" : "+v"(rv));
; #pragma unroll
;                 for (int i = 0; i < 4; ++i) vf[i] = frag(lds, db * 32 + rv, 2 * (q4 * 4 + i) + hi);
;                 asm volatile("" ::: "memory");
; #pragma unroll
;                 for (int i = 0; i < 4; ++i) o = __builtin_amdgcn_mfma_f32_32x32x16_bf16(pa[q4 * 4 + i], vf[i], o, 0, 0, 0); }
; #pragma unroll
;             for (int r = 0; r < 16; ++r) { const int bt = bt0 + att::crow(r, hi), col = h * 256 + db * 32 + r32; const float val = o[r] * rli[r], vn = __shfl_xor(val, 1);
;                 if ((r32 & 1) == 0) *(unsigned*)(Y3 + (size_t)bt * YS + col) = pk2(val * bflo(zz[dbi * 16 + r]), vn * bfhi(zz[dbi * 16 + r])); } } }
.LBB0_1246:
	s_or_b64 exec, exec, s[0:1]
	v_mov_b32_e32 v148, v1
	global_load_dword v199, v[116:117], off offset:256 nt
	global_load_dword v198, v[118:119], off offset:256 nt
	global_load_dword v197, v[120:121], off offset:256 nt
	global_load_dword v196, v[124:125], off offset:256 nt
	global_load_dword v178, v[124:125], off offset:320 nt
	global_load_dword v179, v[120:121], off offset:320 nt
	global_load_dword v180, v[118:119], off offset:320 nt
	global_load_dword v181, v[116:117], off offset:320 nt
	global_load_dword v193, v[122:123], off offset:256 nt
	global_load_dword v192, v[126:127], off offset:256 nt
	global_load_dword v191, v[128:129], off offset:256 nt
	global_load_dword v190, v[130:131], off offset:256 nt
	global_load_dword v174, v[130:131], off offset:320 nt
	global_load_dword v175, v[128:129], off offset:320 nt
	global_load_dword v176, v[126:127], off offset:320 nt
	global_load_dword v177, v[122:123], off offset:320 nt
	global_load_dword v189, v[132:133], off offset:256 nt
	global_load_dword v188, v[134:135], off offset:256 nt
	global_load_dword v187, v[136:137], off offset:256 nt
	global_load_dword v186, v[140:141], off offset:256 nt
	global_load_dword v170, v[140:141], off offset:320 nt
	global_load_dword v171, v[136:137], off offset:320 nt
	global_load_dword v172, v[134:135], off offset:320 nt
	global_load_dword v173, v[132:133], off offset:320 nt
	global_load_dword v185, v[138:139], off offset:256 nt
	global_load_dword v184, v[142:143], off offset:256 nt
	global_load_dword v183, v[144:145], off offset:256 nt
	global_load_dword v182, v[146:147], off offset:256 nt
	global_load_dword v2, v[146:147], off offset:320 nt
	global_load_dword v150, v[144:145], off offset:320 nt
	global_load_dword v151, v[142:143], off offset:320 nt
	global_load_dword v169, v[138:139], off offset:320 nt
	s_nop 0
	v_lshl_add_u32 v149, v148, 9, s7
	s_waitcnt lgkmcnt(0)
	v_bitop3_b32 v4, v148, v200, 31 bitop3:0x6c
	v_lshl_add_u32 v4, v4, 4, v149
	ds_read_b128 v[4:7], v4
	v_bitop3_b32 v194, v148, v209, 31 bitop3:0x6c
	v_lshl_add_u32 v194, v194, 4, v149
	ds_read_b128 v[232:235], v194
	s_waitcnt lgkmcnt(1)
	v_mfma_f32_32x32x16_bf16 v[4:19], v[28:31], v[4:7], 0
	v_bitop3_b32 v194, v148, v218, 31 bitop3:0x6c
	v_lshl_add_u32 v194, v194, 4, v149
	v_bitop3_b32 v148, v148, v214, 31 bitop3:0x6c
	v_lshl_add_u32 v148, v148, 4, v149
	s_waitcnt lgkmcnt(0)
	v_mfma_f32_32x32x16_bf16 v[4:19], v[20:23], v[232:235], v[4:19]
	ds_read_b128 v[232:235], v194
	s_waitcnt lgkmcnt(0)
	v_mfma_f32_32x32x16_bf16 v[4:19], v[36:39], v[232:235], v[4:19]
	ds_read_b128 v[232:235], v148
	v_mov_b32_e32 v148, v1
	s_nop 0
	v_lshl_add_u32 v149, v148, 9, s7
	v_bitop3_b32 v194, v148, v217, 31 bitop3:0x6c
	s_waitcnt lgkmcnt(0)
	v_mfma_f32_32x32x16_bf16 v[4:19], v[24:27], v[232:235], v[4:19]
	v_lshl_add_u32 v194, v194, 4, v149
	ds_read_b128 v[232:235], v194
	v_bitop3_b32 v194, v148, v206, 31 bitop3:0x6c
	v_lshl_add_u32 v194, v194, 4, v149
	s_waitcnt lgkmcnt(0)
	v_mfma_f32_32x32x16_bf16 v[4:19], v[44:47], v[232:235], v[4:19]
	ds_read_b128 v[232:235], v194
	v_bitop3_b32 v194, v148, v216, 31 bitop3:0x6c
	v_lshl_add_u32 v194, v194, 4, v149
	v_bitop3_b32 v148, v148, v211, 31 bitop3:0x6c
	v_lshl_add_u32 v148, v148, 4, v149
	s_waitcnt lgkmcnt(0)
	v_mfma_f32_32x32x16_bf16 v[4:19], v[32:35], v[232:235], v[4:19]
	ds_read_b128 v[232:235], v194
	s_waitcnt lgkmcnt(0)
	v_mfma_f32_32x32x16_bf16 v[4:19], v[52:55], v[232:235], v[4:19]
	ds_read_b128 v[232:235], v148
	v_mov_b32_e32 v148, v1
	s_nop 0
	v_lshl_add_u32 v149, v148, 9, s7
	v_bitop3_b32 v194, v148, v215, 31 bitop3:0x6c
	s_waitcnt lgkmcnt(0)
	v_mfma_f32_32x32x16_bf16 v[4:19], v[40:43], v[232:235], v[4:19]
	v_lshl_add_u32 v194, v194, 4, v149
	ds_read_b128 v[232:235], v194
	v_bitop3_b32 v194, v148, v202, 31 bitop3:0x6c
	v_lshl_add_u32 v194, v194, 4, v149
	s_waitcnt lgkmcnt(0)
	v_mfma_f32_32x32x16_bf16 v[4:19], v[60:63], v[232:235], v[4:19]
	ds_read_b128 v[232:235], v194
	v_bitop3_b32 v194, v148, v213, 31 bitop3:0x6c
	v_lshl_add_u32 v194, v194, 4, v149
	v_bitop3_b32 v148, v148, v208, 31 bitop3:0x6c
	v_lshl_add_u32 v148, v148, 4, v149
	s_waitcnt lgkmcnt(0)
	v_mfma_f32_32x32x16_bf16 v[4:19], v[48:51], v[232:235], v[4:19]
	ds_read_b128 v[232:235], v194
	s_waitcnt lgkmcnt(0)
	v_mfma_f32_32x32x16_bf16 v[4:19], v[68:71], v[232:235], v[4:19]
	ds_read_b128 v[232:235], v148
	v_mov_b32_e32 v148, v1
	s_nop 0
	v_lshl_add_u32 v149, v148, 9, s7
	v_bitop3_b32 v194, v148, v212, 31 bitop3:0x6c
	s_waitcnt lgkmcnt(0)
	v_mfma_f32_32x32x16_bf16 v[4:19], v[56:59], v[232:235], v[4:19]
	v_lshl_add_u32 v194, v194, 4, v149
	ds_read_b128 v[232:235], v194
	v_bitop3_b32 v194, v148, v201, 31 bitop3:0x6c
	v_lshl_add_u32 v194, v194, 4, v149
	s_waitcnt lgkmcnt(0)
	v_mfma_f32_32x32x16_bf16 v[4:19], v[72:75], v[232:235], v[4:19]
	ds_read_b128 v[232:235], v194
	v_bitop3_b32 v194, v148, v210, 31 bitop3:0x6c
	v_lshl_add_u32 v194, v194, 4, v149
	v_bitop3_b32 v148, v148, v204, 31 bitop3:0x6c
	v_lshl_add_u32 v148, v148, 4, v149
	s_waitcnt lgkmcnt(0)
	v_mfma_f32_32x32x16_bf16 v[4:19], v[64:67], v[232:235], v[4:19]
	ds_read_b128 v[232:235], v194
	s_waitcnt lgkmcnt(0)
	v_mfma_f32_32x32x16_bf16 v[4:19], v[76:79], v[232:235], v[4:19]
	ds_read_b128 v[232:235], v148
	s_waitcnt lgkmcnt(0)
	v_mfma_f32_32x32x16_bf16 v[4:19], v[80:83], v[232:235], v[4:19]
	s_nop 11
	v_mul_f32_e32 v148, v4, v168
	ds_bpermute_b32 v149, v153, v148
	s_and_saveexec_b64 s[0:1], vcc
	s_cbranch_execz .LBB0_1248
	s_waitcnt vmcnt(31)
	v_lshlrev_b32_e32 v194, 16, v199
	v_and_b32_e32 v195, 0xffff0000, v199
	s_waitcnt lgkmcnt(0)
	v_pk_mul_f32 v[148:149], v[148:149], v[194:195]
	s_nop 0
	v_and_b32_sdwa v194, v148, v227 dst_sel:DWORD dst_unused:UNUSED_PAD src0_sel:WORD_1 src1_sel:DWORD
	v_and_b32_sdwa v4, v149, v227 dst_sel:DWORD dst_unused:UNUSED_PAD src0_sel:WORD_1 src1_sel:DWORD
	v_add3_u32 v148, v148, v194, s97
	v_add3_u32 v4, v149, v4, s97
	v_lshrrev_b32_e32 v148, 16, v148
	v_and_or_b32 v4, v4, s85, v148
	global_store_dword v[84:85], v4, off offset:256

; __device__ __forceinline__ float bflo(unsigned w) { return __uint_as_float(w << 16); }
; __device__ __forceinline__ float bfhi(unsigned w) { return __uint_as_float(w & 0xffff0000u); }
; __device__ __forceinline__ unsigned pk2(float lo, float hi) { return f2bf(lo) | (f2bf(hi) << 16); }
; __device__ __forceinline__ int crow(int r, int hi) { return (r & 3) + 8 * (r >> 2) + 4 * hi; }
; __device__ __forceinline__ void unit(const bf16_t* proj, const bf16_t* mk, const bf16_t* mvt, bf16_t* Y3, int un, LAS unsigned char* lds) {
;     ...
;     for (int hf = 0; hf < 4; ++hf) { unsigned zz[32];
; #pragma unroll
;         for (int dbi = 0; dbi < 2; ++dbi)
; #pragma unroll
;             for (int r = 0; r < 16; ++r) zz[dbi * 16 + r] = *(const unsigned*)(proj + (size_t)(bt0 + att::crow(r, hi)) * NC + C_ZM + h * 256 + (hf * 2 + dbi) * 32 + (r32 & ~1));
;         asm volatile("" ::: "memory");
; #pragma unroll
;         for (int dbi = 0; dbi < 2; ++dbi) { const int db = hf * 2 + dbi; att::f32x16 o = att::f32x16{};
; #pragma unroll
;             for (int q4 = 0; q4 < 4; ++q4) { att::bf16x8 vf[4]; int rv = r32; asm volatile("" : "+v"(rv));
; #pragma unroll
;                 for (int i = 0; i < 4; ++i) vf[i] = frag(lds, db * 32 + rv, 2 * (q4 * 4 + i) + hi);
;                 asm volatile("" ::: "memory");
; #pragma unroll
;                 for (int i = 0; i < 4; ++i) o = __builtin_amdgcn_mfma_f32_32x32x16_bf16(pa[q4 * 4 + i], vf[i], o, 0, 0, 0); }
; #pragma unroll
;             for (int r = 0; r < 16; ++r) { const int bt = bt0 + att::crow(r, hi), col = h * 256 + db * 32 + r32; const float val = o[r] * rli[r], vn = __shfl_xor(val, 1);
;                 if ((r32 & 1) == 0) *(unsigned*)(Y3 + (size_t)bt * YS + col) = pk2(val * bflo(zz[dbi * 16 + r]), vn * bfhi(zz[dbi * 16 + r])); } } }
.LBB0_1310:
	s_or_b64 exec, exec, s[0:1]
	global_load_dword v180, v[116:117], off offset:384 nt
	global_load_dword v179, v[118:119], off offset:384 nt
	global_load_dword v178, v[120:121], off offset:384 nt
	global_load_dword v177, v[124:125], off offset:384 nt
	global_load_dword v148, v[124:125], off offset:448 nt
	global_load_dword v149, v[120:121], off offset:448 nt
	global_load_dword v150, v[118:119], off offset:448 nt
	global_load_dword v151, v[116:117], off offset:448 nt
	global_load_dword v176, v[122:123], off offset:384 nt
	global_load_dword v175, v[126:127], off offset:384 nt
	global_load_dword v174, v[128:129], off offset:384 nt
	global_load_dword v173, v[130:131], off offset:384 nt
	global_load_dword v125, v[130:131], off offset:448 nt
	s_nop 0
	global_load_dword v128, v[128:129], off offset:448 nt
	s_nop 0
	global_load_dword v126, v[126:127], off offset:448 nt
	s_nop 0
	global_load_dword v127, v[122:123], off offset:448 nt
	global_load_dword v172, v[132:133], off offset:384 nt
	global_load_dword v171, v[134:135], off offset:384 nt
	global_load_dword v170, v[136:137], off offset:384 nt
	global_load_dword v169, v[140:141], off offset:384 nt
	global_load_dword v121, v[140:141], off offset:448 nt
	global_load_dword v122, v[136:137], off offset:448 nt
	global_load_dword v123, v[134:135], off offset:448 nt
	global_load_dword v124, v[132:133], off offset:448 nt
	s_nop 0
	global_load_dword v132, v[138:139], off offset:384 nt
	global_load_dword v131, v[142:143], off offset:384 nt
	global_load_dword v130, v[144:145], off offset:384 nt
	global_load_dword v129, v[146:147], off offset:384 nt
	global_load_dword v2, v[146:147], off offset:448 nt
	global_load_dword v118, v[144:145], off offset:448 nt
	global_load_dword v119, v[142:143], off offset:448 nt
	global_load_dword v120, v[138:139], off offset:448 nt
	v_mov_b32_e32 v116, v1
	s_nop 0
	v_lshl_add_u32 v117, v116, 9, s5
	s_waitcnt lgkmcnt(0)
	v_bitop3_b32 v4, v116, v200, 31 bitop3:0x6c
	v_lshl_add_u32 v4, v4, 4, v117
	ds_read_b128 v[4:7], v4
	v_bitop3_b32 v133, v116, v209, 31 bitop3:0x6c
	v_lshl_add_u32 v133, v133, 4, v117
	ds_read_b128 v[134:137], v133
	s_waitcnt lgkmcnt(1)
	v_mfma_f32_32x32x16_bf16 v[4:19], v[28:31], v[4:7], 0
	v_bitop3_b32 v133, v116, v218, 31 bitop3:0x6c
	v_lshl_add_u32 v133, v133, 4, v117
	v_bitop3_b32 v116, v116, v214, 31 bitop3:0x6c
	v_lshl_add_u32 v116, v116, 4, v117
	s_waitcnt lgkmcnt(0)
	v_mfma_f32_32x32x16_bf16 v[4:19], v[20:23], v[134:137], v[4:19]
	ds_read_b128 v[134:137], v133
	s_waitcnt lgkmcnt(0)
	v_mfma_f32_32x32x16_bf16 v[4:19], v[36:39], v[134:137], v[4:19]
	ds_read_b128 v[134:137], v116
	v_mov_b32_e32 v116, v1
	s_nop 0
	v_lshl_add_u32 v117, v116, 9, s5
	v_bitop3_b32 v133, v116, v217, 31 bitop3:0x6c
	s_waitcnt lgkmcnt(0)
	v_mfma_f32_32x32x16_bf16 v[4:19], v[24:27], v[134:137], v[4:19]
	v_lshl_add_u32 v133, v133, 4, v117
	ds_read_b128 v[134:137], v133
	v_bitop3_b32 v133, v116, v206, 31 bitop3:0x6c
	v_lshl_add_u32 v133, v133, 4, v117
	s_waitcnt lgkmcnt(0)
	v_mfma_f32_32x32x16_bf16 v[4:19], v[44:47], v[134:137], v[4:19]
	ds_read_b128 v[134:137], v133
	v_bitop3_b32 v133, v116, v216, 31 bitop3:0x6c
	v_lshl_add_u32 v133, v133, 4, v117
	v_bitop3_b32 v116, v116, v211, 31 bitop3:0x6c
	v_lshl_add_u32 v116, v116, 4, v117
	s_waitcnt lgkmcnt(0)
	v_mfma_f32_32x32x16_bf16 v[4:19], v[32:35], v[134:137], v[4:19]
	ds_read_b128 v[134:137], v133
	s_waitcnt lgkmcnt(0)
	v_mfma_f32_32x32x16_bf16 v[4:19], v[52:55], v[134:137], v[4:19]
	ds_read_b128 v[134:137], v116
	v_mov_b32_e32 v116, v1
	s_nop 0
	v_lshl_add_u32 v117, v116, 9, s5
	v_bitop3_b32 v133, v116, v215, 31 bitop3:0x6c
	s_waitcnt lgkmcnt(0)
	v_mfma_f32_32x32x16_bf16 v[4:19], v[40:43], v[134:137], v[4:19]
	v_lshl_add_u32 v133, v133, 4, v117
	ds_read_b128 v[134:137], v133
	v_bitop3_b32 v133, v116, v202, 31 bitop3:0x6c
	v_lshl_add_u32 v133, v133, 4, v117
	s_waitcnt lgkmcnt(0)
	v_mfma_f32_32x32x16_bf16 v[4:19], v[60:63], v[134:137], v[4:19]
	ds_read_b128 v[134:137], v133
	v_bitop3_b32 v133, v116, v213, 31 bitop3:0x6c
	v_lshl_add_u32 v133, v133, 4, v117
	v_bitop3_b32 v116, v116, v208, 31 bitop3:0x6c
	v_lshl_add_u32 v116, v116, 4, v117
	s_waitcnt lgkmcnt(0)
	v_mfma_f32_32x32x16_bf16 v[4:19], v[48:51], v[134:137], v[4:19]
	ds_read_b128 v[134:137], v133
	s_waitcnt lgkmcnt(0)
	v_mfma_f32_32x32x16_bf16 v[4:19], v[68:71], v[134:137], v[4:19]
	ds_read_b128 v[134:137], v116
	v_mov_b32_e32 v116, v1
	s_nop 0
	v_lshl_add_u32 v117, v116, 9, s5
	v_bitop3_b32 v133, v116, v212, 31 bitop3:0x6c
	s_waitcnt lgkmcnt(0)
	v_mfma_f32_32x32x16_bf16 v[4:19], v[56:59], v[134:137], v[4:19]
	v_lshl_add_u32 v133, v133, 4, v117
	ds_read_b128 v[134:137], v133
	v_bitop3_b32 v133, v116, v201, 31 bitop3:0x6c
	v_lshl_add_u32 v133, v133, 4, v117
	s_waitcnt lgkmcnt(0)
	v_mfma_f32_32x32x16_bf16 v[4:19], v[72:75], v[134:137], v[4:19]
	ds_read_b128 v[134:137], v133
	v_bitop3_b32 v133, v116, v210, 31 bitop3:0x6c
	v_lshl_add_u32 v133, v133, 4, v117
	v_bitop3_b32 v116, v116, v204, 31 bitop3:0x6c
	v_lshl_add_u32 v116, v116, 4, v117
	s_waitcnt lgkmcnt(0)
	v_mfma_f32_32x32x16_bf16 v[4:19], v[64:67], v[134:137], v[4:19]
	ds_read_b128 v[134:137], v133
	s_waitcnt lgkmcnt(0)
	v_mfma_f32_32x32x16_bf16 v[4:19], v[76:79], v[134:137], v[4:19]
	ds_read_b128 v[134:137], v116
	s_waitcnt lgkmcnt(0)
	v_mfma_f32_32x32x16_bf16 v[4:19], v[80:83], v[134:137], v[4:19]
	s_nop 11
	v_mul_f32_e32 v116, v4, v168
	ds_bpermute_b32 v117, v153, v116
	s_and_saveexec_b64 s[0:1], vcc
	s_cbranch_execz .LBB0_1312
	s_waitcnt vmcnt(31)
	v_lshlrev_b32_e32 v134, 16, v180
	v_and_b32_e32 v135, 0xffff0000, v180
	s_waitcnt lgkmcnt(0)
	v_pk_mul_f32 v[116:117], v[116:117], v[134:135]
	s_nop 0
	v_and_b32_sdwa v133, v116, v227 dst_sel:DWORD dst_unused:UNUSED_PAD src0_sel:WORD_1 src1_sel:DWORD
	v_and_b32_sdwa v4, v117, v227 dst_sel:DWORD dst_unused:UNUSED_PAD src0_sel:WORD_1 src1_sel:DWORD
	v_add3_u32 v116, v116, v133, s97
	v_add3_u32 v4, v117, v4, s97
	v_lshrrev_b32_e32 v116, 16, v116
	v_and_or_b32 v4, v4, s85, v116
	global_store_dword v[84:85], v4, off offset:384

; __device__ __forceinline__ int crow(int r, int hi) { return (r & 3) + 8 * (r >> 2) + 4 * hi; }
; #define TP_BEGIN(c) do { if (TP_MODE != 0 && (c) && threadIdx.x == 0) MISC[25] = (unsigned)__builtin_amdgcn_s_memrealtime(); } while (0)
; #define TP_END(c)   do { if (TP_MODE != 0 && (c) && threadIdx.x == 0) MISC[24] = MISC[24] + ((unsigned)__builtin_amdgcn_s_memrealtime() - MISC[25]); } while (0)
; #define INP(k) launder_p(args.in[k])
; __device__ __forceinline__ void unit(const bf16_t* proj, const float* stats  , const float* lng, const float* lnb, const float* sw, const float* sb, bf16_t* Y2, int un, LAS unsigned char* lds) {
;     ...
;     for (int i = 0; i < 8; ++i) { const int s0 = (i >> 2) * 64 + 16 * (i & 3) + hi * 8; const float* wp = sw + ((size_t)g * 128 + t) * 128 + s0; wv[2 * i] = *(const f32x4*)wp; wv[2 * i + 1] = *(const f32x4*)(wp + 4); }
;     ...
;     for (int r = 0; r < 16; ++r) { const int tr = tb * 32 + att::crow(r, hi), bt = R0 + tr; bias[r] = sb[g * 128 + tr];
; #pragma unroll
;         for (int d = 0; d < 2; ++d) { const int ch = g * 128 + (2 * eh + d) * 32 + (r32 & ~1); uu[r * 2 + d] = *(const unsigned*)(proj + (size_t)bt * NC + C_UC + ch); zq[r * 2 + d] = *(const unsigned*)(proj + (size_t)bt * NC + C_ZC + ch); } }
; __global__ void __launch_bounds__(NWAVES * 64, 2) mega_fwd(Args args) {
;     ...
;                 if (u < 128) u = (u >> 4) * 48 + (u & 15);
;                 else if (u < 384) { const int e_ = u - 128; u = (e_ >> 5) * 48 + 16 + (e_ & 31); }
;                 if (u >= 512) {
;                     TP_BEGIN(TP_MODE == 8 && l == 1 && u == 512);
;                     sgu::unit(PROJ, (const float*)(ws + WS_STATS), INP(11) + l * BW, INP(12) + l * BW, INP(13) + (size_t)l * 8 * 128 * 128, INP(14) + l * 8 * 128, Y + 2 * BW, u - 512, lds);
;                     TP_END(TP_MODE == 8 && l == 1 && u == 512);
;                     continue; }
.LBB0_1376:
	s_andn2_b64 vcc, exec, s[0:1]
	s_cbranch_vccnz .LBB0_425
	v_readlane_b32 s4, v252, 35
	v_readlane_b32 s10, v252, 41
	v_readlane_b32 s11, v252, 42
	s_mov_b64 s[0:1], s[10:11]
	v_readlane_b32 s5, v252, 36
	v_readlane_b32 s12, v252, 43
	v_readlane_b32 s13, v252, 44
	v_readlane_b32 s10, v254, 43
	v_readlane_b32 s11, v254, 44
	s_add_u32 s0, s0, s10
	s_mov_b64 s[4:5], s[12:13]
	s_addc_u32 s1, s1, s11
	v_readlane_b32 s6, v252, 37
	v_readlane_b32 s7, v252, 38
	v_readlane_b32 s8, v252, 39
	v_readlane_b32 s9, v252, 40
	v_readlane_b32 s14, v252, 45
	v_readlane_b32 s15, v252, 46
	s_add_u32 s4, s4, s10
	s_addc_u32 s5, s5, s11
	s_mov_b64 s[6:7], s[14:15]
	v_readlane_b32 s8, v253, 54
	v_readlane_b32 s16, v252, 47
	v_readlane_b32 s17, v252, 48
	v_readlane_b32 s9, v253, 55
	s_add_u32 s12, s6, s8
	s_addc_u32 s13, s7, s9
	s_mov_b64 s[6:7], s[16:17]
	s_add_u32 s6, s6, s10
	v_readlane_b32 s8, v254, 47
	s_addc_u32 s7, s7, s11
	s_waitcnt vmcnt(23)
	v_mov_b32_e32 v176, v0
	s_and_b32 s2, s8, 7
	s_lshl_b32 s8, s8, 4
	s_add_i32 s8, s8, 0x7fffe000
	v_readfirstlane_b32 s10, v176
	s_and_b32 s11, s8, 0x7fffff80
	s_lshr_b32 s8, s10, 1
	v_and_b32_e32 v177, 31, v176
	s_and_b32 s9, s8, 0x60
	v_or_b32_e32 v182, s9, v177
	s_lshl_b32 s8, s2, 16
	s_waitcnt vmcnt(3)
	v_lshl_or_b32 v2, v182, 9, s8
	v_lshl_add_u64 v[4:5], s[12:13], 0, v[2:3]
	v_and_b32_e32 v2, 32, v176
	s_lshl_b32 s2, s2, 7
	s_ashr_i32 s8, s10, 2
	v_lshl_add_u64 v[40:41], v[4:5], 0, v[2:3]
	s_andn2_b32 s8, s8, 63
	v_and_or_b32 v2, v176, 30, s2
	s_waitcnt vmcnt(0)
	v_bfe_u32 v1, v176, 5, 1
	v_add_u32_e32 v68, s8, v2
	v_readlane_b32 s12, v253, 48
	v_lshlrev_b32_e32 v183, 3, v1
	v_lshl_or_b32 v1, v1, 2, s9
	v_ashrrev_i32_e32 v69, 31, v68
	v_readlane_b32 s13, v253, 49
	v_or_b32_e32 v2, s11, v1
	s_mov_b32 s14, 0xe800
	v_mov_b64_e32 v[100:101], s[12:13]
	v_lshlrev_b64 v[84:85], 1, v[68:69]
	v_or_b32_e32 v68, 32, v68
	v_readlane_b32 s18, v252, 49
	v_readlane_b32 s19, v252, 50
	v_mad_u64_u32 v[70:71], s[12:13], v2, s14, v[100:101]
	s_mov_b64 s[16:17], 0x4000
	v_ashrrev_i32_e32 v69, 31, v68
	v_lshl_add_u64 v[72:73], v[70:71], 0, s[16:17]
	s_mov_b64 s[18:19], 0x5000
	v_lshlrev_b64 v[86:87], 1, v[68:69]
	v_lshl_add_u64 v[70:71], v[70:71], 0, s[18:19]
	v_lshl_add_u64 v[74:75], v[72:73], 0, v[84:85]
	v_lshl_add_u64 v[68:69], v[72:73], 0, v[86:87]
	global_load_dwordx4 v[28:31], v[40:41], off offset:16
	global_load_dwordx4 v[32:35], v[40:41], off
	global_load_dwordx4 v[20:23], v[40:41], off offset:80
	global_load_dwordx4 v[24:27], v[40:41], off offset:64
	s_cmp_ge_u32 s9, 32
	s_cselect_b64 exec, -1, 0
	global_load_dwordx4 v[12:15], v[40:41], off offset:144
	global_load_dwordx4 v[16:19], v[40:41], off offset:128
	s_waitcnt lgkmcnt(0)
	global_load_dwordx4 v[4:7], v[40:41], off offset:208
	global_load_dwordx4 v[8:11], v[40:41], off offset:192
	s_cmp_ge_u32 s9, 64
	s_cselect_b64 exec, -1, 0
	global_load_dwordx4 v[60:63], v[40:41], off offset:272
	global_load_dwordx4 v[64:67], v[40:41], off offset:256
	global_load_dwordx4 v[52:55], v[40:41], off offset:336
	global_load_dwordx4 v[56:59], v[40:41], off offset:320
	s_cmp_ge_u32 s9, 0x60
	s_cselect_b64 exec, -1, 0
	global_load_dwordx4 v[44:47], v[40:41], off offset:400
	global_load_dwordx4 v[48:51], v[40:41], off offset:384
	global_load_dwordx4 v[36:39], v[40:41], off offset:464
	s_nop 0
	global_load_dwordx4 v[40:43], v[40:41], off offset:448
	s_mov_b64 exec, -1
	v_or_b32_e32 v1, s2, v1
	global_load_dword v180, v[74:75], off nt
	global_load_dword v178, v[68:69], off nt
	v_lshl_add_u64 v[74:75], v[70:71], 0, v[84:85]
	v_lshl_add_u64 v[68:69], v[70:71], 0, v[86:87]
	global_load_dword v181, v[74:75], off nt
	global_load_dword v179, v[68:69], off nt
	v_or_b32_e32 v68, 1, v2
	v_mad_u64_u32 v[68:69], s[12:13], v68, s14, v[100:101]
	v_lshl_add_u64 v[70:71], v[68:69], 0, s[16:17]
	v_lshl_add_u64 v[68:69], v[68:69], 0, s[18:19]
	v_lshl_add_u64 v[72:73], v[70:71], 0, v[84:85]
	v_lshl_add_u64 v[70:71], v[70:71], 0, v[86:87]
	global_load_dword v173, v[72:73], off nt
	global_load_dword v172, v[70:71], off nt
	v_lshl_add_u64 v[72:73], v[68:69], 0, v[84:85]
	v_lshl_add_u64 v[68:69], v[68:69], 0, v[86:87]
	global_load_dword v174, v[68:69], off nt
	v_or_b32_e32 v68, 2, v2
	v_mad_u64_u32 v[68:69], s[12:13], v68, s14, v[100:101]
	v_lshl_add_u64 v[70:71], v[68:69], 0, s[16:17]
	global_load_dword v175, v[72:73], off nt
	v_lshl_add_u64 v[68:69], v[68:69], 0, s[18:19]
	v_lshl_add_u64 v[72:73], v[70:71], 0, v[84:85]
	v_lshl_add_u64 v[70:71], v[70:71], 0, v[86:87]
	global_load_dword v170, v[72:73], off nt
	global_load_dword v168, v[70:71], off nt
	v_lshl_add_u64 v[72:73], v[68:69], 0, v[84:85]
	v_lshl_add_u64 v[68:69], v[68:69], 0, v[86:87]
	global_load_dword v169, v[68:69], off nt
	v_or_b32_e32 v68, 3, v2
	v_mad_u64_u32 v[68:69], s[12:13], v68, s14, v[100:101]
	v_lshl_add_u64 v[70:71], v[68:69], 0, s[16:17]
	global_load_dword v171, v[72:73], off nt
	v_lshl_add_u64 v[68:69], v[68:69], 0, s[18:19]
	v_lshl_add_u64 v[72:73], v[70:71], 0, v[84:85]
	v_lshl_add_u64 v[70:71], v[70:71], 0, v[86:87]
	global_load_dword v165, v[72:73], off nt
	global_load_dword v164, v[70:71], off nt
	v_lshl_add_u64 v[72:73], v[68:69], 0, v[84:85]
	v_lshl_add_u64 v[68:69], v[68:69], 0, v[86:87]
	global_load_dword v166, v[68:69], off nt
	v_or_b32_e32 v68, 8, v2
	v_mad_u64_u32 v[68:69], s[12:13], v68, s14, v[100:101]
	v_lshl_add_u64 v[70:71], v[68:69], 0, s[16:17]
	global_load_dword v167, v[72:73], off nt
	v_lshl_add_u64 v[68:69], v[68:69], 0, s[18:19]
	v_lshl_add_u64 v[72:73], v[70:71], 0, v[84:85]
	v_lshl_add_u64 v[70:71], v[70:71], 0, v[86:87]
	global_load_dword v162, v[72:73], off nt
	global_load_dword v160, v[70:71], off nt
; __device__ __forceinline__ int crow(int r, int hi) { return (r & 3) + 8 * (r >> 2) + 4 * hi; }
; __device__ __forceinline__ void unit(const bf16_t* proj, const float* stats  , const float* lng, const float* lnb, const float* sw, const float* sb, bf16_t* Y2, int un, LAS unsigned char* lds) {
;     ...
;     for (int r = 0; r < 16; ++r) { const int tr = tb * 32 + att::crow(r, hi), bt = R0 + tr; bias[r] = sb[g * 128 + tr];
; #pragma unroll
;         for (int d = 0; d < 2; ++d) { const int ch = g * 128 + (2 * eh + d) * 32 + (r32 & ~1); uu[r * 2 + d] = *(const unsigned*)(proj + (size_t)bt * NC + C_UC + ch); zq[r * 2 + d] = *(const unsigned*)(proj + (size_t)bt * NC + C_ZC + ch); } }
	v_lshl_add_u64 v[72:73], v[68:69], 0, v[84:85]
	v_lshl_add_u64 v[68:69], v[68:69], 0, v[86:87]
	global_load_dword v161, v[68:69], off nt
	v_or_b32_e32 v68, 9, v2
	v_mad_u64_u32 v[68:69], s[12:13], v68, s14, v[100:101]
	v_lshl_add_u64 v[70:71], v[68:69], 0, s[16:17]
	global_load_dword v163, v[72:73], off nt
	v_lshl_add_u64 v[68:69], v[68:69], 0, s[18:19]
	v_lshl_add_u64 v[72:73], v[70:71], 0, v[84:85]
	v_lshl_add_u64 v[70:71], v[70:71], 0, v[86:87]
	global_load_dword v157, v[72:73], off nt
	global_load_dword v156, v[70:71], off nt
	v_lshl_add_u64 v[72:73], v[68:69], 0, v[84:85]
	v_lshl_add_u64 v[68:69], v[68:69], 0, v[86:87]
	global_load_dword v158, v[68:69], off nt
	v_or_b32_e32 v68, 10, v2
	v_mad_u64_u32 v[68:69], s[12:13], v68, s14, v[100:101]
	v_lshl_add_u64 v[70:71], v[68:69], 0, s[16:17]
	global_load_dword v159, v[72:73], off nt
	v_lshl_add_u64 v[68:69], v[68:69], 0, s[18:19]
	v_lshl_add_u64 v[72:73], v[70:71], 0, v[84:85]
	v_lshl_add_u64 v[70:71], v[70:71], 0, v[86:87]
	global_load_dword v154, v[72:73], off nt
	global_load_dword v152, v[70:71], off nt
	v_lshl_add_u64 v[72:73], v[68:69], 0, v[84:85]
	v_lshl_add_u64 v[68:69], v[68:69], 0, v[86:87]
	global_load_dword v153, v[68:69], off nt
	v_or_b32_e32 v68, 11, v2
	v_mad_u64_u32 v[68:69], s[12:13], v68, s14, v[100:101]
	v_lshl_add_u64 v[70:71], v[68:69], 0, s[16:17]
	global_load_dword v155, v[72:73], off nt
	v_lshl_add_u64 v[68:69], v[68:69], 0, s[18:19]
	v_lshl_add_u64 v[72:73], v[70:71], 0, v[84:85]
	v_lshl_add_u64 v[70:71], v[70:71], 0, v[86:87]
	global_load_dword v149, v[72:73], off nt
	global_load_dword v148, v[70:71], off nt
	v_lshl_add_u64 v[72:73], v[68:69], 0, v[84:85]
	v_lshl_add_u64 v[68:69], v[68:69], 0, v[86:87]
	global_load_dword v150, v[68:69], off nt
	v_or_b32_e32 v68, 16, v2
	v_mad_u64_u32 v[68:69], s[12:13], v68, s14, v[100:101]
	v_lshl_add_u64 v[70:71], v[68:69], 0, s[16:17]
	v_lshl_add_u64 v[68:69], v[68:69], 0, s[18:19]
	v_lshl_add_u64 v[88:89], v[70:71], 0, v[84:85]
	global_load_dword v151, v[72:73], off nt
	global_load_dword v146, v[88:89], off nt
	v_lshl_add_u64 v[88:89], v[68:69], 0, v[84:85]
	v_lshl_add_u64 v[70:71], v[70:71], 0, v[86:87]
	v_lshl_add_u64 v[68:69], v[68:69], 0, v[86:87]
	global_load_dword v143, v[70:71], off nt
	global_load_dword v144, v[68:69], off nt
	v_or_b32_e32 v68, 17, v2
	v_mad_u64_u32 v[68:69], s[12:13], v68, s14, v[100:101]
	v_lshl_add_u64 v[70:71], v[68:69], 0, s[16:17]
	global_load_dword v147, v[88:89], off nt
	v_lshl_add_u64 v[68:69], v[68:69], 0, s[18:19]
	v_lshl_add_u64 v[88:89], v[70:71], 0, v[84:85]
	v_lshl_add_u64 v[70:71], v[70:71], 0, v[86:87]
	global_load_dword v140, v[88:89], off nt
	global_load_dword v139, v[70:71], off nt
	v_lshl_add_u64 v[88:89], v[68:69], 0, v[84:85]
	v_lshl_add_u64 v[68:69], v[68:69], 0, v[86:87]
	global_load_dword v141, v[68:69], off nt
	v_or_b32_e32 v68, 18, v2
	v_mad_u64_u32 v[68:69], s[12:13], v68, s14, v[100:101]
	v_lshl_add_u64 v[70:71], v[68:69], 0, s[16:17]
	global_load_dword v142, v[88:89], off nt
	v_lshl_add_u64 v[68:69], v[68:69], 0, s[18:19]
	v_lshl_add_u64 v[88:89], v[70:71], 0, v[84:85]
	v_lshl_add_u64 v[70:71], v[70:71], 0, v[86:87]
	global_load_dword v137, v[88:89], off nt
	global_load_dword v135, v[70:71], off nt
	v_lshl_add_u64 v[88:89], v[68:69], 0, v[84:85]
	v_lshl_add_u64 v[68:69], v[68:69], 0, v[86:87]
	global_load_dword v136, v[68:69], off nt
	v_or_b32_e32 v68, 19, v2
	v_mad_u64_u32 v[68:69], s[12:13], v68, s14, v[100:101]
	v_lshl_add_u64 v[70:71], v[68:69], 0, s[16:17]
	global_load_dword v138, v[88:89], off nt
	v_lshl_add_u64 v[68:69], v[68:69], 0, s[18:19]
	v_lshl_add_u64 v[88:89], v[70:71], 0, v[84:85]
	v_lshl_add_u64 v[70:71], v[70:71], 0, v[86:87]
	global_load_dword v133, v[88:89], off nt
	global_load_dword v131, v[70:71], off nt
	v_lshl_add_u64 v[88:89], v[68:69], 0, v[84:85]
	v_lshlrev_b32_e32 v1, 2, v1
	global_load_dword v134, v[88:89], off nt
	v_lshl_add_u64 v[68:69], v[68:69], 0, v[86:87]
	v_or_b32_e32 v88, 24, v2
	global_load_dwordx4 v[80:83], v1, s[6:7]
	global_load_dwordx4 v[76:79], v1, s[6:7] offset:32
	global_load_dwordx4 v[72:75], v1, s[6:7] offset:64
	global_load_dword v132, v[68:69], off nt
	v_ashrrev_i32_e32 v185, 4, v176
	global_load_dwordx4 v[68:71], v1, s[6:7] offset:96
	v_mad_u64_u32 v[88:89], s[6:7], v88, s14, v[100:101]
	v_lshl_add_u64 v[90:91], v[88:89], 0, s[16:17]
	v_lshl_add_u64 v[88:89], v[88:89], 0, s[18:19]
	v_lshl_add_u64 v[92:93], v[90:91], 0, v[84:85]
	v_lshl_add_u64 v[90:91], v[90:91], 0, v[86:87]
	global_load_dword v129, v[92:93], off nt
	global_load_dword v127, v[90:91], off nt
	v_lshl_add_u64 v[92:93], v[88:89], 0, v[84:85]
	v_lshl_add_u64 v[88:89], v[88:89], 0, v[86:87]
	v_or_b32_e32 v1, 25, v2
	global_load_dword v128, v[88:89], off nt
	v_mad_u64_u32 v[88:89], s[6:7], v1, s14, v[100:101]
	v_lshl_add_u64 v[90:91], v[88:89], 0, s[16:17]
	global_load_dword v130, v[92:93], off nt
	v_lshl_add_u64 v[88:89], v[88:89], 0, s[18:19]
	v_lshl_add_u64 v[92:93], v[90:91], 0, v[84:85]
	v_lshl_add_u64 v[90:91], v[90:91], 0, v[86:87]
	global_load_dword v125, v[92:93], off nt
	global_load_dword v123, v[90:91], off nt
	v_lshl_add_u64 v[92:93], v[88:89], 0, v[84:85]
	v_lshl_add_u64 v[88:89], v[88:89], 0, v[86:87]
	v_or_b32_e32 v1, 26, v2
	global_load_dword v124, v[88:89], off nt
	v_mad_u64_u32 v[88:89], s[6:7], v1, s14, v[100:101]
	v_lshl_add_u64 v[90:91], v[88:89], 0, s[16:17]
	global_load_dword v126, v[92:93], off nt
	v_lshl_add_u64 v[88:89], v[88:89], 0, s[18:19]
	v_lshl_add_u64 v[92:93], v[90:91], 0, v[84:85]
	v_lshl_add_u64 v[90:91], v[90:91], 0, v[86:87]
	global_load_dword v121, v[92:93], off nt
	global_load_dword v119, v[90:91], off nt
; __device__ __forceinline__ int crow(int r, int hi) { return (r & 3) + 8 * (r >> 2) + 4 * hi; }
; __device__ __forceinline__ void unit(const bf16_t* proj, const float* stats  , const float* lng, const float* lnb, const float* sw, const float* sb, bf16_t* Y2, int un, LAS unsigned char* lds) {
;     ...
;     for (int r = 0; r < 16; ++r) { const int tr = tb * 32 + att::crow(r, hi), bt = R0 + tr; bias[r] = sb[g * 128 + tr];
; #pragma unroll
;         for (int d = 0; d < 2; ++d) { const int ch = g * 128 + (2 * eh + d) * 32 + (r32 & ~1); uu[r * 2 + d] = *(const unsigned*)(proj + (size_t)bt * NC + C_UC + ch); zq[r * 2 + d] = *(const unsigned*)(proj + (size_t)bt * NC + C_ZC + ch); } }
;     { const int sr = tid >> 4, sc = (tid & 15) * 8, ch = g * 128 + sc;
;       const f32x4 g0 = *(const f32x4*)(lng + ch), g1 = *(const f32x4*)(lng + ch + 4), b0 = *(const f32x4*)(lnb + ch), b1 = *(const f32x4*)(lnb + ch + 4);
;       float mus[4], rss[4];
;       { float2 pp[4];
; #pragma unroll
;         for (int q = 0; q < 4; ++q) pp[q] = *(const float2*)(stats + ((size_t)(R0 + sr + 32 * q) * 16 + (tid & 15)) * 2);
;         asm volatile("" ::: "memory");
; #pragma unroll
;         for (int q = 0; q < 4; ++q) { float s1 = pp[q].x, s2 = pp[q].y;
; #pragma unroll
;             for (int off = 1; off < 16; off <<= 1) { s1 += __shfl_xor(s1, off); s2 += __shfl_xor(s2, off); }
;             mus[q] = s1 * (1.0f / 1024.0f); rss[q] = __builtin_amdgcn_rsqf(fmaxf(s2 * (1.0f / 1024.0f) - mus[q] * mus[q], 0.f) + LN_EPS); } }
	v_lshl_add_u64 v[92:93], v[88:89], 0, v[84:85]
	v_lshl_add_u64 v[88:89], v[88:89], 0, v[86:87]
	v_or_b32_e32 v1, 27, v2
	global_load_dword v120, v[88:89], off nt
	v_mad_u64_u32 v[88:89], s[6:7], v1, s14, v[100:101]
	v_lshl_add_u64 v[90:91], v[88:89], 0, s[16:17]
	v_lshl_add_u64 v[88:89], v[88:89], 0, s[18:19]
	global_load_dword v122, v[92:93], off nt
	v_lshl_add_u64 v[92:93], v[90:91], 0, v[84:85]
	v_lshl_add_u64 v[84:85], v[88:89], 0, v[84:85]
	global_load_dword v109, v[92:93], off nt
	global_load_dword v115, v[84:85], off nt
	v_lshl_add_u64 v[84:85], v[90:91], 0, v[86:87]
	global_load_dword v1, v[84:85], off nt
	v_lshl_add_u64 v[84:85], v[88:89], 0, v[86:87]
	global_load_dword v107, v[84:85], off nt
	v_and_b32_e32 v84, 15, v176
	v_lshlrev_b32_e32 v102, 3, v84
	v_or_b32_e32 v191, s2, v102
	v_lshlrev_b32_e32 v96, 2, v191
	global_load_dwordx4 v[84:87], v96, s[0:1] offset:16
	global_load_dwordx4 v[92:95], v96, s[0:1]
	global_load_dwordx4 v[88:91], v96, s[4:5] offset:16
	s_nop 0
	global_load_dwordx4 v[96:99], v96, s[4:5]
	v_add_u32_e32 v110, s11, v185
	v_readlane_b32 s0, v254, 37
	v_mov_b32_e32 v103, v3
	v_readlane_b32 s1, v254, 38
	v_ashrrev_i32_e32 v111, 31, v110
	v_lshlrev_b64 v[104:105], 7, v[110:111]
	v_lshl_add_u64 v[102:103], s[0:1], 0, v[102:103]
	v_lshl_add_u64 v[112:113], v[102:103], 0, v[104:105]
	global_load_dwordx2 v[104:105], v[112:113], off
	s_movk_i32 s0, 0x2000
	v_add_co_u32_e32 v116, vcc, s0, v112
	s_movk_i32 s0, 0x3000
	s_nop 0
	v_addc_co_u32_e32 v117, vcc, 0, v113, vcc
	global_load_dwordx2 v[102:103], v[116:117], off offset:-4096
	global_load_dwordx2 v[186:187], v[116:117], off
	v_add_co_u32_e32 v112, vcc, s0, v112
	v_and_b32_e32 v106, 64, v229
	s_nop 0
	v_addc_co_u32_e32 v113, vcc, 0, v113, vcc
	v_add_u32_e32 v106, 64, v106
	v_xor_b32_e32 v108, 1, v229
	v_cmp_lt_i32_e32 vcc, v108, v106
	global_load_dwordx2 v[188:189], v[112:113], off
	s_mov_b32 s0, 0x3a800000
	v_cndmask_b32_e32 v108, v229, v108, vcc
	v_lshlrev_b32_e32 v145, 2, v108
	v_xor_b32_e32 v108, 2, v229
	v_cmp_lt_i32_e32 vcc, v108, v106
	s_movk_i32 s4, 0x4000
	v_and_b32_e32 v184, 63, v176
	v_cndmask_b32_e32 v108, v229, v108, vcc
	v_lshlrev_b32_e32 v111, 2, v108
	v_xor_b32_e32 v108, 4, v229
	v_cmp_lt_i32_e32 vcc, v108, v106
	s_cmpk_gt_u32 s10, 0xff
	s_waitcnt vmcnt(3)
	ds_bpermute_b32 v112, v145, v104
	ds_bpermute_b32 v113, v145, v105
	v_cndmask_b32_e32 v108, v229, v108, vcc
	v_lshlrev_b32_e32 v190, 2, v108
	v_xor_b32_e32 v108, 8, v229
	v_cmp_lt_i32_e32 vcc, v108, v106
	s_waitcnt lgkmcnt(0)
	v_pk_add_f32 v[104:105], v[104:105], v[112:113]
	ds_bpermute_b32 v112, v111, v104
	ds_bpermute_b32 v113, v111, v105
	v_cndmask_b32_e32 v106, v229, v108, vcc
	v_lshlrev_b32_e32 v106, 2, v106
	s_waitcnt lgkmcnt(0)
	v_pk_add_f32 v[104:105], v[104:105], v[112:113]
	ds_bpermute_b32 v112, v190, v104
	ds_bpermute_b32 v113, v190, v105
	s_waitcnt lgkmcnt(0)
	v_pk_add_f32 v[104:105], v[104:105], v[112:113]
	ds_bpermute_b32 v112, v106, v104
	ds_bpermute_b32 v113, v106, v105
	s_waitcnt lgkmcnt(0)
	v_pk_add_f32 v[104:105], v[104:105], v[112:113]
	s_nop 0
	v_pk_mul_f32 v[116:117], v[104:105], s[0:1] op_sel_hi:[1,0]
	s_waitcnt vmcnt(2)
	ds_bpermute_b32 v105, v145, v103
	v_fma_f32 v104, -v116, v116, v117
	v_max_f32_e32 v104, 0, v104
	v_add_f32_e32 v104, 0x3727c5ac, v104
	v_rsq_f32_e32 v118, v104
	ds_bpermute_b32 v104, v145, v102
	s_waitcnt lgkmcnt(0)
	v_pk_add_f32 v[102:103], v[102:103], v[104:105]
	ds_bpermute_b32 v104, v111, v102
	ds_bpermute_b32 v105, v111, v103
	s_waitcnt lgkmcnt(0)
	v_pk_add_f32 v[102:103], v[102:103], v[104:105]
	ds_bpermute_b32 v104, v190, v102
	ds_bpermute_b32 v105, v190, v103
	s_waitcnt lgkmcnt(0)
	v_pk_add_f32 v[102:103], v[102:103], v[104:105]
	ds_bpermute_b32 v104, v106, v102
	ds_bpermute_b32 v105, v106, v103
	s_waitcnt lgkmcnt(0)
	v_pk_add_f32 v[102:103], v[102:103], v[104:105]
	s_nop 0
	v_pk_mul_f32 v[112:113], v[102:103], s[0:1] op_sel_hi:[1,0]
	s_waitcnt vmcnt(1)
	ds_bpermute_b32 v103, v145, v187
	v_fma_f32 v102, -v112, v112, v113
	v_max_f32_e32 v102, 0, v102
	v_add_f32_e32 v102, 0x3727c5ac, v102
	v_rsq_f32_e32 v114, v102
	ds_bpermute_b32 v102, v145, v186
	s_waitcnt lgkmcnt(0)
	v_pk_add_f32 v[102:103], v[186:187], v[102:103]
	ds_bpermute_b32 v104, v111, v102
	ds_bpermute_b32 v105, v111, v103
	s_waitcnt lgkmcnt(0)
	v_pk_add_f32 v[102:103], v[102:103], v[104:105]
	ds_bpermute_b32 v104, v190, v102
	ds_bpermute_b32 v105, v190, v103
	s_waitcnt lgkmcnt(0)
	v_pk_add_f32 v[102:103], v[102:103], v[104:105]
	ds_bpermute_b32 v104, v106, v102
	ds_bpermute_b32 v105, v106, v103
	s_waitcnt lgkmcnt(0)
	v_pk_add_f32 v[102:103], v[102:103], v[104:105]
	s_nop 0
	v_pk_mul_f32 v[102:103], v[102:103], s[0:1] op_sel_hi:[1,0]
	s_waitcnt vmcnt(0)
	ds_bpermute_b32 v105, v145, v189
	v_fma_f32 v104, -v102, v102, v103
	v_max_f32_e32 v104, 0, v104
	v_add_f32_e32 v104, 0x3727c5ac, v104
	v_rsq_f32_e32 v108, v104
	ds_bpermute_b32 v104, v145, v188
	s_waitcnt lgkmcnt(0)
	v_pk_add_f32 v[104:105], v[188:189], v[104:105]
	ds_bpermute_b32 v186, v111, v104
	ds_bpermute_b32 v187, v111, v105
	v_lshlrev_b32_e32 v111, 1, v185
	v_bfe_u32 v188, v176, 2, 2
	s_waitcnt lgkmcnt(0)
	v_pk_add_f32 v[104:105], v[104:105], v[186:187]
	ds_bpermute_b32 v186, v190, v104
	ds_bpermute_b32 v187, v190, v105
	s_waitcnt lgkmcnt(0)
	v_pk_add_f32 v[104:105], v[104:105], v[186:187]
	ds_bpermute_b32 v186, v106, v104
	ds_bpermute_b32 v187, v106, v105
	s_waitcnt lgkmcnt(0)
; __device__ __forceinline__ unsigned cvt_pk_bf16(float lo, float hi) { f32x2_t v = {lo, hi}; bf16x2_t b = __builtin_convertvector(v, bf16x2_t); return __builtin_bit_cast(unsigned, b); }
; #define LAS __attribute__((address_space(3)))
; __device__ __forceinline__ float bflo(unsigned w) { return __uint_as_float(w << 16); }
; __device__ __forceinline__ float bfhi(unsigned w) { return __uint_as_float(w & 0xffff0000u); }
; __device__ __forceinline__ int v_st(int k, int c) { const int kk = (k & ~0xC) | ((k & 4) << 1) | ((k & 8) >> 1); return ((kk >> 3) * 4 + (c >> 5)) * 512 + ((kk & 7) * 32 + (c & 31)) * 2; }
; __device__ __forceinline__ void unit(const bf16_t* proj, const float* stats  , const float* lng, const float* lnb, const float* sw, const float* sb, bf16_t* Y2, int un, LAS unsigned char* lds) {
;     ...
;       for (int q = 0; q < 4; ++q) { const int s = sr + 32 * q, row = R0 + s; const u32x4 vv = *(const u32x4*)(proj + (size_t)row * NC + C_VC + ch);
;           const float mu = mus[q], rs = rss[q];
;           u32x4 w; w.x = pg8::cvt_pk_bf16((bflo(vv.x) - mu) * rs * g0[0] + b0[0], (bfhi(vv.x) - mu) * rs * g0[1] + b0[1]); w.y = pg8::cvt_pk_bf16((bflo(vv.y) - mu) * rs * g0[2] + b0[2], (bfhi(vv.y) - mu) * rs * g0[3] + b0[3]);
;           w.z = pg8::cvt_pk_bf16((bflo(vv.z) - mu) * rs * g1[0] + b1[0], (bfhi(vv.z) - mu) * rs * g1[1] + b1[1]); w.w = pg8::cvt_pk_bf16((bflo(vv.w) - mu) * rs * g1[2] + b1[2], (bfhi(vv.w) - mu) * rs * g1[3] + b1[3]);
;           *(LAS u32x4*)(lds + (s >> 6) * att::SHM_V + att::v_st(s & 63, sc)) = w; } }
	v_pk_add_f32 v[104:105], v[104:105], v[186:187]
	v_and_b32_e32 v187, 8, v111
	v_lshrrev_b32_e32 v111, 1, v185
	v_and_b32_e32 v186, 3, v185
	v_and_or_b32 v111, v111, 4, v186
	v_pk_mul_f32 v[104:105], v[104:105], s[0:1] op_sel_hi:[1,0]
	v_lshlrev_b32_e32 v189, 6, v111
	v_mad_i64_i32 v[192:193], s[0:1], v110, s14, v[100:101]
	v_lshlrev_b32_e32 v110, 1, v191
	v_mov_b32_e32 v111, v3
	v_lshl_add_u64 v[192:193], v[192:193], 0, v[110:111]
	v_add_co_u32_e32 v192, vcc, s4, v192
	v_lshlrev_b32_e32 v186, 4, v176
	s_nop 0
	v_addc_co_u32_e32 v193, vcc, 0, v193, vcc
	global_load_dwordx4 v[196:199], v[192:193], off offset:2048
	v_and_b32_e32 v190, 48, v186
	v_fma_f32 v106, -v104, v104, v105
	v_max_f32_e32 v106, 0, v106
	v_add_f32_e32 v106, 0x3727c5ac, v106
	v_rsq_f32_e32 v106, v106
	s_waitcnt vmcnt(0)
	v_lshlrev_b32_e32 v192, 16, v196
	v_and_b32_e32 v193, 0xffff0000, v196
	v_pk_add_f32 v[192:193], v[192:193], v[116:117] op_sel_hi:[1,0] neg_lo:[0,1] neg_hi:[0,1]
	s_nop 0
	v_pk_mul_f32 v[192:193], v[118:119], v[192:193] op_sel_hi:[0,1]
	v_pk_fma_f32 v[192:193], v[92:93], v[192:193], v[96:97]
	s_nop 0
	v_cvt_pk_bf16_f32 v196, v192, v193
	v_lshlrev_b32_e32 v192, 16, v197
	v_and_b32_e32 v193, 0xffff0000, v197
	v_pk_add_f32 v[192:193], v[192:193], v[116:117] op_sel_hi:[1,0] neg_lo:[0,1] neg_hi:[0,1]
	s_nop 0
	v_pk_mul_f32 v[192:193], v[118:119], v[192:193] op_sel_hi:[0,1]
	v_pk_fma_f32 v[192:193], v[94:95], v[192:193], v[98:99]
	s_nop 0
	v_cvt_pk_bf16_f32 v197, v192, v193
	v_lshlrev_b32_e32 v192, 16, v198
	v_and_b32_e32 v193, 0xffff0000, v198
	v_pk_add_f32 v[192:193], v[192:193], v[116:117] op_sel_hi:[1,0] neg_lo:[0,1] neg_hi:[0,1]
	s_nop 0
	v_pk_mul_f32 v[192:193], v[118:119], v[192:193] op_sel_hi:[0,1]
	v_pk_fma_f32 v[192:193], v[84:85], v[192:193], v[88:89]
	s_nop 0
	v_cvt_pk_bf16_f32 v198, v192, v193
	v_lshlrev_b32_e32 v192, 16, v199
	v_and_b32_e32 v193, 0xffff0000, v199
	v_pk_add_f32 v[116:117], v[192:193], v[116:117] op_sel_hi:[1,0] neg_lo:[0,1] neg_hi:[0,1]
	s_nop 0
	v_pk_mul_f32 v[116:117], v[118:119], v[116:117] op_sel_hi:[0,1]
	v_pk_fma_f32 v[116:117], v[86:87], v[116:117], v[90:91]
	s_nop 0
	v_cvt_pk_bf16_f32 v199, v116, v117
	v_lshlrev_b32_e32 v116, 8, v185
	v_and_b32_e32 v117, 0xffffc000, v116
	v_and_or_b32 v116, v185, 48, v187
	v_lshrrev_b32_e32 v116, 1, v116
	v_or_b32_e32 v116, v116, v188
	v_lshlrev_b32_e32 v116, 9, v116
	v_add3_u32 v117, 0, v117, v116
	v_add3_u32 v117, v117, v189, v190
	ds_write_b128 v117, v[196:199]
	v_add_u32_e32 v117, 32, v185
	v_add_u32_e32 v118, s11, v117
	v_mad_i64_i32 v[192:193], s[0:1], v118, s14, v[100:101]
	v_lshl_add_u64 v[192:193], v[192:193], 0, v[110:111]
	v_add_co_u32_e32 v192, vcc, s4, v192
	s_nop 1
	v_addc_co_u32_e32 v193, vcc, 0, v193, vcc
	global_load_dwordx4 v[196:199], v[192:193], off offset:2048
	s_waitcnt vmcnt(0)
	v_lshlrev_b32_e32 v192, 16, v196
	v_and_b32_e32 v193, 0xffff0000, v196
	v_pk_add_f32 v[192:193], v[192:193], v[112:113] op_sel_hi:[1,0] neg_lo:[0,1] neg_hi:[0,1]
	s_nop 0
	v_pk_mul_f32 v[192:193], v[114:115], v[192:193] op_sel_hi:[0,1]
	v_pk_fma_f32 v[192:193], v[92:93], v[192:193], v[96:97]
	s_nop 0
	v_cvt_pk_bf16_f32 v196, v192, v193
	v_lshlrev_b32_e32 v192, 16, v197
	v_and_b32_e32 v193, 0xffff0000, v197
	v_pk_add_f32 v[192:193], v[192:193], v[112:113] op_sel_hi:[1,0] neg_lo:[0,1] neg_hi:[0,1]
	s_nop 0
	v_pk_mul_f32 v[192:193], v[114:115], v[192:193] op_sel_hi:[0,1]
	v_pk_fma_f32 v[192:193], v[94:95], v[192:193], v[98:99]
	s_nop 0
	v_cvt_pk_bf16_f32 v197, v192, v193
	v_lshlrev_b32_e32 v192, 16, v198
	v_and_b32_e32 v193, 0xffff0000, v198
	v_pk_add_f32 v[192:193], v[192:193], v[112:113] op_sel_hi:[1,0] neg_lo:[0,1] neg_hi:[0,1]
	s_nop 0
	v_pk_mul_f32 v[192:193], v[114:115], v[192:193] op_sel_hi:[0,1]
	v_pk_fma_f32 v[192:193], v[84:85], v[192:193], v[88:89]
	s_nop 0
	v_cvt_pk_bf16_f32 v198, v192, v193
	v_lshlrev_b32_e32 v192, 16, v199
	v_and_b32_e32 v193, 0xffff0000, v199
	v_pk_add_f32 v[112:113], v[192:193], v[112:113] op_sel_hi:[1,0] neg_lo:[0,1] neg_hi:[0,1]
	s_nop 0
	v_pk_mul_f32 v[112:113], v[114:115], v[112:113] op_sel_hi:[0,1]
	v_pk_fma_f32 v[112:113], v[86:87], v[112:113], v[90:91]
	v_add_u32_e32 v114, 64, v185
	v_cvt_pk_bf16_f32 v199, v112, v113
	v_and_or_b32 v113, v117, 48, v187
	v_lshrrev_b32_e32 v113, 1, v113
	v_lshlrev_b32_e32 v112, 8, v117
	v_or_b32_e32 v113, v113, v188
	v_and_b32_e32 v112, 0xffffc000, v112
	v_lshlrev_b32_e32 v113, 9, v113
	v_add3_u32 v112, 0, v112, v113
	v_add3_u32 v112, v112, v189, v190
	ds_write_b128 v112, v[196:199]
	v_add_u32_e32 v112, s11, v114
	v_mad_i64_i32 v[112:113], s[0:1], v112, s14, v[100:101]
	v_lshl_add_u64 v[112:113], v[112:113], 0, v[110:111]
	v_add_co_u32_e32 v112, vcc, s4, v112
	s_nop 1
	v_addc_co_u32_e32 v113, vcc, 0, v113, vcc
	global_load_dwordx4 v[196:199], v[112:113], off offset:2048
	s_waitcnt vmcnt(0)
; __device__ __forceinline__ unsigned cvt_pk_bf16(float lo, float hi) { f32x2_t v = {lo, hi}; bf16x2_t b = __builtin_convertvector(v, bf16x2_t); return __builtin_bit_cast(unsigned, b); }
; #define LAS __attribute__((address_space(3)))
; __device__ __forceinline__ float bflo(unsigned w) { return __uint_as_float(w << 16); }
; __device__ __forceinline__ float bfhi(unsigned w) { return __uint_as_float(w & 0xffff0000u); }
; __device__ __forceinline__ int v_st(int k, int c) { const int kk = (k & ~0xC) | ((k & 4) << 1) | ((k & 8) >> 1); return ((kk >> 3) * 4 + (c >> 5)) * 512 + ((kk & 7) * 32 + (c & 31)) * 2; }
; __device__ __forceinline__ int v_rd_base(int lane) { return ((lane & 3) << 3) | (((lane >> 2) & 3) << 6) | (((lane >> 4) & 1) << 5) | (((lane >> 5) & 1) << 8); }
; __device__ __forceinline__ void unit(const bf16_t* proj, const float* stats  , const float* lng, const float* lnb, const float* sw, const float* sb, bf16_t* Y2, int un, LAS unsigned char* lds) {
;     ...
;       for (int q = 0; q < 4; ++q) { const int s = sr + 32 * q, row = R0 + s; const u32x4 vv = *(const u32x4*)(proj + (size_t)row * NC + C_VC + ch);
;           const float mu = mus[q], rs = rss[q];
;           u32x4 w; w.x = pg8::cvt_pk_bf16((bflo(vv.x) - mu) * rs * g0[0] + b0[0], (bfhi(vv.x) - mu) * rs * g0[1] + b0[1]); w.y = pg8::cvt_pk_bf16((bflo(vv.y) - mu) * rs * g0[2] + b0[2], (bfhi(vv.y) - mu) * rs * g0[3] + b0[3]);
;           w.z = pg8::cvt_pk_bf16((bflo(vv.z) - mu) * rs * g1[0] + b1[0], (bfhi(vv.z) - mu) * rs * g1[1] + b1[1]); w.w = pg8::cvt_pk_bf16((bflo(vv.w) - mu) * rs * g1[2] + b1[2], (bfhi(vv.w) - mu) * rs * g1[3] + b1[3]);
;           *(LAS u32x4*)(lds + (s >> 6) * att::SHM_V + att::v_st(s & 63, sc)) = w; } }
;     __syncthreads();
;     att::f32x16 o0 = att::f32x16{}, o1 = att::f32x16{};
;     LAS const unsigned char* vb = lds + att::v_rd_base(lane);
; #pragma unroll
;     for (int st = 0; st < 2; ++st) {
;         if (st * 64 > tb * 32 + 31) continue;
;         att::bf16x8 pa[4];
; #pragma unroll
;         for (int k = 0; k < 4; ++k) { const int s0 = st * 64 + 16 * k + hi * 8; const f32x4 w0 = wv[2 * (st * 4 + k)], w1 = wv[2 * (st * 4 + k) + 1];
;             float x[8] = {w0[0], w0[1], w0[2], w0[3], w1[0], w1[1], w1[2], w1[3]};
; #pragma unroll
;             for (int j = 0; j < 8; ++j) x[j] = (s0 + j <= t) ? x[j] : 0.f;
	v_lshlrev_b32_e32 v112, 16, v196
	v_and_b32_e32 v113, 0xffff0000, v196
	v_pk_add_f32 v[112:113], v[112:113], v[102:103] op_sel_hi:[1,0] neg_lo:[0,1] neg_hi:[0,1]
	s_nop 0
	v_pk_mul_f32 v[112:113], v[108:109], v[112:113] op_sel_hi:[0,1]
	v_pk_fma_f32 v[112:113], v[92:93], v[112:113], v[96:97]
	s_nop 0
	v_cvt_pk_bf16_f32 v196, v112, v113
	v_lshlrev_b32_e32 v112, 16, v197
	v_and_b32_e32 v113, 0xffff0000, v197
	v_pk_add_f32 v[112:113], v[112:113], v[102:103] op_sel_hi:[1,0] neg_lo:[0,1] neg_hi:[0,1]
	s_nop 0
	v_pk_mul_f32 v[112:113], v[108:109], v[112:113] op_sel_hi:[0,1]
	v_pk_fma_f32 v[112:113], v[94:95], v[112:113], v[98:99]
	s_nop 0
	v_cvt_pk_bf16_f32 v197, v112, v113
	v_lshlrev_b32_e32 v112, 16, v198
	v_and_b32_e32 v113, 0xffff0000, v198
	v_pk_add_f32 v[112:113], v[112:113], v[102:103] op_sel_hi:[1,0] neg_lo:[0,1] neg_hi:[0,1]
	s_nop 0
	v_pk_mul_f32 v[112:113], v[108:109], v[112:113] op_sel_hi:[0,1]
	v_pk_fma_f32 v[112:113], v[84:85], v[112:113], v[88:89]
	s_nop 0
	v_cvt_pk_bf16_f32 v198, v112, v113
	v_lshlrev_b32_e32 v112, 16, v199
	v_and_b32_e32 v113, 0xffff0000, v199
	v_pk_add_f32 v[102:103], v[112:113], v[102:103] op_sel_hi:[1,0] neg_lo:[0,1] neg_hi:[0,1]
	s_nop 0
	v_pk_mul_f32 v[102:103], v[108:109], v[102:103] op_sel_hi:[0,1]
	v_pk_fma_f32 v[102:103], v[86:87], v[102:103], v[90:91]
	v_add_u32_e32 v108, 0x60, v185
	v_cvt_pk_bf16_f32 v199, v102, v103
	v_lshlrev_b32_e32 v102, 8, v114
	v_and_b32_e32 v102, 0xffffc000, v102
	v_add3_u32 v102, 0, v102, v116
	v_add3_u32 v102, v102, v189, v190
	ds_write_b128 v102, v[196:199]
	v_add_u32_e32 v102, s11, v108
	v_mad_i64_i32 v[100:101], s[0:1], v102, s14, v[100:101]
	v_lshl_add_u64 v[100:101], v[100:101], 0, v[110:111]
	v_add_co_u32_e32 v100, vcc, s4, v100
	s_cselect_b64 s[0:1], -1, 0
	s_nop 0
	v_addc_co_u32_e32 v101, vcc, 0, v101, vcc
	global_load_dwordx4 v[100:103], v[100:101], off offset:2048
	v_cmp_le_u32_e32 vcc, v183, v182
	s_mov_b64 s[4:5], -1
	s_waitcnt vmcnt(0)
	v_lshlrev_b32_e32 v110, 16, v100
	v_and_b32_e32 v111, 0xffff0000, v100
	v_pk_add_f32 v[110:111], v[110:111], v[104:105] op_sel_hi:[1,0] neg_lo:[0,1] neg_hi:[0,1]
	v_cndmask_b32_e32 v32, 0, v32, vcc
	v_pk_mul_f32 v[110:111], v[106:107], v[110:111] op_sel_hi:[0,1]
	v_pk_fma_f32 v[92:93], v[92:93], v[110:111], v[96:97]
	v_lshlrev_b32_e32 v96, 16, v101
	v_and_b32_e32 v97, 0xffff0000, v101
	v_pk_add_f32 v[96:97], v[96:97], v[104:105] op_sel_hi:[1,0] neg_lo:[0,1] neg_hi:[0,1]
	v_cvt_pk_bf16_f32 v92, v92, v93
	v_pk_mul_f32 v[96:97], v[106:107], v[96:97] op_sel_hi:[0,1]
	v_pk_fma_f32 v[94:95], v[94:95], v[96:97], v[98:99]
	v_cmp_lt_u32_e32 vcc, v183, v182
	v_cvt_pk_bf16_f32 v93, v94, v95
	v_lshlrev_b32_e32 v94, 16, v102
	v_and_b32_e32 v95, 0xffff0000, v102
	v_pk_add_f32 v[94:95], v[94:95], v[104:105] op_sel_hi:[1,0] neg_lo:[0,1] neg_hi:[0,1]
	v_cndmask_b32_e32 v33, 0, v33, vcc
	v_pk_mul_f32 v[94:95], v[106:107], v[94:95] op_sel_hi:[0,1]
	v_pk_fma_f32 v[84:85], v[84:85], v[94:95], v[88:89]
	s_nop 0
	v_cvt_pk_bf16_f32 v94, v84, v85
	v_lshlrev_b32_e32 v84, 16, v103
	v_and_b32_e32 v85, 0xffff0000, v103
	v_pk_add_f32 v[84:85], v[84:85], v[104:105] op_sel_hi:[1,0] neg_lo:[0,1] neg_hi:[0,1]
	s_nop 0
	v_pk_mul_f32 v[84:85], v[106:107], v[84:85] op_sel_hi:[0,1]
	v_pk_fma_f32 v[84:85], v[86:87], v[84:85], v[90:91]
	v_and_b32_e32 v86, 0xc0, v186
	v_cvt_pk_bf16_f32 v95, v84, v85
	v_and_or_b32 v85, v108, 48, v187
	v_lshrrev_b32_e32 v85, 1, v85
	v_lshlrev_b32_e32 v84, 8, v108
	v_or_b32_e32 v85, v85, v188
	v_and_b32_e32 v84, 0xffffc000, v84
	v_lshlrev_b32_e32 v85, 9, v85
	v_add3_u32 v84, 0, v84, v85
	v_add3_u32 v84, v84, v189, v190
	ds_write_b128 v84, v[92:95]
	v_lshlrev_b32_e32 v84, 3, v184
	v_and_b32_e32 v85, 24, v84
	v_lshlrev_b32_e32 v87, 1, v176
	v_and_b32_e32 v87, 32, v87
	v_and_b32_e32 v84, 0x100, v84
	v_add3_u32 v85, 0, v85, v86
	v_add3_u32 v100, v85, v87, v84
	v_or_b32_e32 v84, 2, v183
	v_cmp_le_u32_e32 vcc, v84, v182
	v_or_b32_e32 v84, 3, v183
	s_waitcnt lgkmcnt(0)
	v_cndmask_b32_e32 v34, 0, v34, vcc
	v_cmp_le_u32_e32 vcc, v84, v182
	v_or_b32_e32 v84, 4, v183
	s_barrier
; __device__ __forceinline__ unsigned cvt_pk_bf16(float lo, float hi) { f32x2_t v = {lo, hi}; bf16x2_t b = __builtin_convertvector(v, bf16x2_t); return __builtin_bit_cast(unsigned, b); }
; __device__ __forceinline__ s16x4 tr_read(LAS const unsigned char* p) { return __builtin_bit_cast(s16x4, __builtin_amdgcn_ds_read_tr16_b64_v4i16((LAS v4i16_t*)p)); }
; template <int D0> __device__ __forceinline__ void pv_one(f32x16& od, LAS const unsigned char* vb, bf16x8 pa0, bf16x8 pa1, bf16x8 pa2, bf16x8 pa3) {
;     const s16x4 l0 = tr_read(vb + v_rd_off(D0, 0, 0)), h0 = tr_read(vb + v_rd_off(D0, 0, 1)), l1 = tr_read(vb + v_rd_off(D0, 1, 0)), h1 = tr_read(vb + v_rd_off(D0, 1, 1));
;     const s16x4 l2 = tr_read(vb + v_rd_off(D0, 2, 0)), h2 = tr_read(vb + v_rd_off(D0, 2, 1)), l3 = tr_read(vb + v_rd_off(D0, 3, 0)), h3 = tr_read(vb + v_rd_off(D0, 3, 1));
;     ...
;     od = __builtin_amdgcn_mfma_f32_32x32x16_bf16(pa0, ATT_PK(l0, h0), od, 0, 0, 0);
;     od = __builtin_amdgcn_mfma_f32_32x32x16_bf16(pa1, ATT_PK(l1, h1), od, 0, 0, 0);
;     od = __builtin_amdgcn_mfma_f32_32x32x16_bf16(pa2, ATT_PK(l2, h2), od, 0, 0, 0);
;     od = __builtin_amdgcn_mfma_f32_32x32x16_bf16(pa3, ATT_PK(l3, h3), od, 0, 0, 0);
; __device__ __forceinline__ void unit(const bf16_t* proj, const float* stats  , const float* lng, const float* lnb, const float* sw, const float* sb, bf16_t* Y2, int un, LAS unsigned char* lds) {
;     ...
;         for (int k = 0; k < 4; ++k) { const int s0 = st * 64 + 16 * k + hi * 8; const f32x4 w0 = wv[2 * (st * 4 + k)], w1 = wv[2 * (st * 4 + k) + 1];
;             float x[8] = {w0[0], w0[1], w0[2], w0[3], w1[0], w1[1], w1[2], w1[3]};
; #pragma unroll
;             for (int j = 0; j < 8; ++j) x[j] = (s0 + j <= t) ? x[j] : 0.f;
;             u32x4 p; p.x = pg8::cvt_pk_bf16(x[0], x[1]); p.y = pg8::cvt_pk_bf16(x[2], x[3]); p.z = pg8::cvt_pk_bf16(x[4], x[5]); p.w = pg8::cvt_pk_bf16(x[6], x[7]); pa[k] = __builtin_bit_cast(att::bf16x8, p); }
;         if (eh == 0) { att::pv_one<0>(o0, vb + st * att::SHM_V, pa[0], pa[1], pa[2], pa[3]); att::pv_one<1>(o1, vb + st * att::SHM_V, pa[0], pa[1], pa[2], pa[3]); }
;         else         { att::pv_one<2>(o0, vb + st * att::SHM_V, pa[0], pa[1], pa[2], pa[3]); att::pv_one<3>(o1, vb + st * att::SHM_V, pa[0], pa[1], pa[2], pa[3]); }
	v_cndmask_b32_e32 v35, 0, v35, vcc
	v_cmp_le_u32_e32 vcc, v84, v182
	v_or_b32_e32 v84, 5, v183
	v_cvt_pk_bf16_f32 v85, v34, v35
	v_cndmask_b32_e32 v28, 0, v28, vcc
	v_cmp_le_u32_e32 vcc, v84, v182
	v_or_b32_e32 v84, 6, v183
	s_nop 0
	v_cndmask_b32_e32 v29, 0, v29, vcc
	v_cmp_le_u32_e32 vcc, v84, v182
	v_or_b32_e32 v84, 7, v183
	v_cvt_pk_bf16_f32 v86, v28, v29
	v_cndmask_b32_e32 v30, 0, v30, vcc
	v_cmp_le_u32_e32 vcc, v84, v182
	v_or_b32_e32 v28, 16, v183
	v_cvt_pk_bf16_f32 v84, v32, v33
	v_cndmask_b32_e32 v31, 0, v31, vcc
	v_cmp_le_u32_e32 vcc, v28, v182
	v_or_b32_e32 v28, 17, v183
	v_cvt_pk_bf16_f32 v87, v30, v31
	v_cndmask_b32_e32 v24, 0, v24, vcc
	v_cmp_le_u32_e32 vcc, v28, v182
	v_or_b32_e32 v28, 18, v183
	s_nop 0
	v_cndmask_b32_e32 v25, 0, v25, vcc
	v_cmp_le_u32_e32 vcc, v28, v182
	v_or_b32_e32 v28, 19, v183
	v_cvt_pk_bf16_f32 v88, v24, v25
	v_cndmask_b32_e32 v26, 0, v26, vcc
	v_cmp_le_u32_e32 vcc, v28, v182
	v_or_b32_e32 v28, 20, v183
	s_nop 0
	v_cndmask_b32_e32 v27, 0, v27, vcc
	v_cmp_le_u32_e32 vcc, v28, v182
	v_or_b32_e32 v28, 21, v183
	v_cvt_pk_bf16_f32 v89, v26, v27
	v_cndmask_b32_e32 v20, 0, v20, vcc
	v_cmp_le_u32_e32 vcc, v28, v182
	v_or_b32_e32 v28, 22, v183
	s_nop 0
	v_cndmask_b32_e32 v21, 0, v21, vcc
	v_cmp_le_u32_e32 vcc, v28, v182
	v_or_b32_e32 v28, 23, v183
	v_cvt_pk_bf16_f32 v90, v20, v21
	v_cndmask_b32_e32 v22, 0, v22, vcc
	v_cmp_le_u32_e32 vcc, v28, v182
	v_or_b32_e32 v20, 32, v183
	s_nop 0
	v_cndmask_b32_e32 v23, 0, v23, vcc
	v_cmp_le_u32_e32 vcc, v20, v182
	v_or_b32_e32 v20, 33, v183
	v_cvt_pk_bf16_f32 v91, v22, v23
	v_cndmask_b32_e32 v16, 0, v16, vcc
	v_cmp_le_u32_e32 vcc, v20, v182
	v_or_b32_e32 v20, 34, v183
	s_nop 0
	v_cndmask_b32_e32 v17, 0, v17, vcc
	v_cmp_le_u32_e32 vcc, v20, v182
	v_or_b32_e32 v20, 35, v183
	v_cvt_pk_bf16_f32 v96, v16, v17
	v_cndmask_b32_e32 v18, 0, v18, vcc
	v_cmp_le_u32_e32 vcc, v20, v182
	v_or_b32_e32 v20, 36, v183
	s_nop 0
	v_cndmask_b32_e32 v19, 0, v19, vcc
	v_cmp_le_u32_e32 vcc, v20, v182
	v_or_b32_e32 v20, 37, v183
	v_cvt_pk_bf16_f32 v97, v18, v19
	v_cndmask_b32_e32 v12, 0, v12, vcc
	v_cmp_le_u32_e32 vcc, v20, v182
	v_or_b32_e32 v20, 38, v183
	s_nop 0
	v_cndmask_b32_e32 v13, 0, v13, vcc
	v_cmp_le_u32_e32 vcc, v20, v182
	v_or_b32_e32 v20, 39, v183
	v_cvt_pk_bf16_f32 v98, v12, v13
	v_cndmask_b32_e32 v14, 0, v14, vcc
	v_cmp_le_u32_e32 vcc, v20, v182
	v_or_b32_e32 v12, 48, v183
	s_nop 0
	v_cndmask_b32_e32 v15, 0, v15, vcc
	v_cmp_le_u32_e32 vcc, v12, v182
	v_or_b32_e32 v12, 49, v183
	v_cvt_pk_bf16_f32 v99, v14, v15
	v_cndmask_b32_e32 v8, 0, v8, vcc
	v_cmp_le_u32_e32 vcc, v12, v182
	v_or_b32_e32 v12, 50, v183
	s_nop 0
	v_cndmask_b32_e32 v9, 0, v9, vcc
	v_cmp_le_u32_e32 vcc, v12, v182
	v_or_b32_e32 v12, 51, v183
	v_cvt_pk_bf16_f32 v92, v8, v9
	v_cndmask_b32_e32 v10, 0, v10, vcc
	v_cmp_le_u32_e32 vcc, v12, v182
	v_or_b32_e32 v12, 52, v183
	s_nop 0
	v_cndmask_b32_e32 v11, 0, v11, vcc
	v_cmp_le_u32_e32 vcc, v12, v182
	v_or_b32_e32 v12, 53, v183
	v_cvt_pk_bf16_f32 v93, v10, v11
	v_cndmask_b32_e32 v4, 0, v4, vcc
	v_cmp_le_u32_e32 vcc, v12, v182
	v_or_b32_e32 v12, 54, v183
	s_nop 0
	v_cndmask_b32_e32 v5, 0, v5, vcc
	v_cmp_le_u32_e32 vcc, v12, v182
	v_or_b32_e32 v12, 55, v183
	v_cvt_pk_bf16_f32 v94, v4, v5
	v_cndmask_b32_e32 v6, 0, v6, vcc
	v_cmp_le_u32_e32 vcc, v12, v182
	s_nop 1
	v_cndmask_b32_e32 v7, 0, v7, vcc
	v_cvt_pk_bf16_f32 v95, v6, v7
	s_and_b64 vcc, exec, s[0:1]
	s_cbranch_vccz .LBB0_1379
	ds_read_b64_tr_b16 v[4:5], v100 offset:1024
	ds_read_b64_tr_b16 v[6:7], v100 offset:3072
	ds_read_b64_tr_b16 v[20:21], v100 offset:5120
	ds_read_b64_tr_b16 v[22:23], v100 offset:7168
	s_mov_b64 s[4:5], 0
	s_waitcnt lgkmcnt(2)
	v_mfma_f32_32x32x16_bf16 v[4:19], v[84:87], v[4:7], 0
	s_waitcnt lgkmcnt(0)
	v_mfma_f32_32x32x16_bf16 v[4:19], v[88:91], v[20:23], v[4:19]
	ds_read_b64_tr_b16 v[20:21], v100 offset:9216
	ds_read_b64_tr_b16 v[22:23], v100 offset:11264
	s_waitcnt lgkmcnt(0)
	v_mfma_f32_32x32x16_bf16 v[4:19], v[96:99], v[20:23], v[4:19]
	ds_read_b64_tr_b16 v[20:21], v100 offset:13312
	ds_read_b64_tr_b16 v[22:23], v100 offset:15360
	s_waitcnt lgkmcnt(0)
	v_mfma_f32_32x32x16_bf16 v[4:19], v[92:95], v[20:23], v[4:19]
	ds_read_b64_tr_b16 v[22:23], v100 offset:3584
	ds_read_b64_tr_b16 v[20:21], v100 offset:1536
	ds_read_b64_tr_b16 v[104:105], v100 offset:7680
	ds_read_b64_tr_b16 v[102:103], v100 offset:5632
	s_waitcnt lgkmcnt(2)
	v_mfma_f32_32x32x16_bf16 v[20:35], v[84:87], v[20:23], 0
	s_waitcnt lgkmcnt(0)
	v_mfma_f32_32x32x16_bf16 v[20:35], v[88:91], v[102:105], v[20:35]
	ds_read_b64_tr_b16 v[104:105], v100 offset:11776
	ds_read_b64_tr_b16 v[102:103], v100 offset:9728
	s_waitcnt lgkmcnt(0)
	v_mfma_f32_32x32x16_bf16 v[20:35], v[96:99], v[102:105], v[20:35]
	ds_read_b64_tr_b16 v[104:105], v100 offset:15872
	ds_read_b64_tr_b16 v[102:103], v100 offset:13824
	s_waitcnt lgkmcnt(0)
	v_mfma_f32_32x32x16_bf16 v[20:35], v[92:95], v[102:105], v[20:35]
